# tile-start store-drain relaxation: first two vmcnt waits of each peeled K-iteration raised by the number of epilogue stores (P1b,P7,P10,P16,P17) with matching dummy loads after the phase prologue; dea
# baseline (speedup 1.0000x reference)
.LBB0_191:
	global_load_dwordx4 v[58:61], v[76:77], off offset:-4096
	global_load_dwordx4 v[54:57], v[76:77], off offset:-3072
	global_load_dwordx4 v[62:65], v[76:77], off offset:-2048
	global_load_dwordx4 v[38:41], v[76:77], off
	global_load_dwordx4 v[50:53], v[76:77], off offset:-1024
	global_load_dwordx4 v[46:49], v[76:77], off offset:1024
	s_waitcnt lgkmcnt(0)
	global_load_dwordx4 v[34:37], v[76:77], off offset:3072
	global_load_dwordx4 v[42:45], v[76:77], off offset:2048
	v_and_b32_e32 v82, 64, v184
	v_xor_b32_e32 v83, 1, v184
	v_add_u32_e32 v109, 64, v82
	v_cmp_lt_i32_e32 vcc, v83, v109
	v_xor_b32_e32 v105, 2, v184
	v_xor_b32_e32 v108, 4, v184
	v_cndmask_b32_e32 v82, v184, v83, vcc
	v_lshlrev_b32_e32 v186, 2, v82
	v_cmp_lt_i32_e32 vcc, v105, v109
	s_add_i32 s2, s3, s14
	s_cmpk_lt_i32 s2, 0x4000
	s_cselect_b64 s[44:45], -1, 0
	s_and_b64 s[26:27], s[44:45], exec
	s_cselect_b32 s40, s2, s14
	s_ashr_i32 s41, s40, 31
	s_lshl_b64 s[26:27], s[40:41], 13
	s_lshl_b64 s[50:51], s[40:41], 11
	s_waitcnt vmcnt(7)
	v_mov_b32_e32 v84, v59
	s_waitcnt vmcnt(6)
	v_mov_b32_e32 v85, v55
	v_mov_b32_e32 v88, v61
	v_mov_b32_e32 v89, v57
	v_mov_b32_e32 v82, v58
	v_mov_b32_e32 v83, v54
	v_mov_b32_e32 v86, v60
	v_mov_b32_e32 v87, v56
	s_waitcnt vmcnt(5)
	v_pk_mul_f32 v[90:91], v[64:65], v[64:65]
	v_pk_mul_f32 v[92:93], v[62:63], v[62:63]
	v_pk_mul_f32 v[84:85], v[84:85], v[84:85]
	v_pk_mul_f32 v[88:89], v[88:89], v[88:89]
	v_pk_mov_b32 v[106:107], v[92:93], v[90:91] op_sel:[1,0]
	v_mov_b32_e32 v93, v91
	v_pk_fma_f32 v[82:83], v[82:83], v[82:83], v[84:85]
	v_pk_fma_f32 v[84:85], v[86:87], v[86:87], v[88:89]
	s_waitcnt vmcnt(3)
	v_mul_f32_e32 v94, v51, v51
	v_mul_f32_e32 v96, v53, v53
	v_pk_add_f32 v[86:87], v[106:107], v[92:93]
	v_pk_add_f32 v[82:83], v[82:83], v[84:85]
	v_mul_f32_e32 v110, v38, v38
	v_mul_f32_e32 v111, v39, v39
	v_mul_f32_e32 v112, v40, v40
	v_mul_f32_e32 v113, v41, v41
	v_pk_fma_f32 v[90:91], v[50:51], v[50:51], v[94:95] op_sel_hi:[1,1,0]
	v_pk_fma_f32 v[94:95], v[52:53], v[52:53], v[96:97] op_sel_hi:[1,1,0]
	v_pk_add_f32 v[84:85], v[86:87], v[86:87] op_sel:[0,1] op_sel_hi:[1,0]
	v_pk_add_f32 v[82:83], v[82:83], v[82:83] op_sel:[0,1] op_sel_hi:[1,0]
	s_waitcnt vmcnt(2)
	v_pk_mul_f32 v[98:99], v[48:49], v[48:49]
	v_pk_mul_f32 v[100:101], v[46:47], v[46:47]
	v_mov_b32_e32 v91, v112
	v_mov_b32_e32 v95, v113
	v_mov_b32_e32 v85, v111
	v_mov_b32_e32 v83, v110
	v_pk_mov_b32 v[96:97], v[100:101], v[98:99] op_sel:[1,0]
	v_mov_b32_e32 v101, v99
	v_pk_add_f32 v[86:87], v[90:91], v[94:95]
	v_pk_add_f32 v[82:83], v[82:83], v[84:85]
	s_waitcnt vmcnt(0)
	v_mul_f32_e32 v102, v43, v43
	v_mul_f32_e32 v104, v45, v45
	v_pk_add_f32 v[88:89], v[96:97], v[100:101]
	v_pk_add_f32 v[82:83], v[82:83], v[86:87]
	v_mul_f32_e32 v114, v34, v34
	v_mul_f32_e32 v115, v35, v35
	v_mul_f32_e32 v116, v36, v36
	v_mul_f32_e32 v117, v37, v37
	v_pk_fma_f32 v[98:99], v[42:43], v[42:43], v[102:103] op_sel_hi:[1,1,0]
	v_pk_fma_f32 v[102:103], v[44:45], v[44:45], v[104:105] op_sel_hi:[1,1,0]
	v_pk_add_f32 v[88:89], v[88:89], v[88:89] op_sel:[0,1] op_sel_hi:[1,0]
	v_pk_add_f32 v[82:83], v[82:83], v[82:83] op_sel:[0,1] op_sel_hi:[1,0]
	v_mov_b32_e32 v99, v116
	v_mov_b32_e32 v103, v117
	v_mov_b32_e32 v89, v115
	v_mov_b32_e32 v83, v114
	v_pk_add_f32 v[90:91], v[98:99], v[102:103]
	v_pk_add_f32 v[82:83], v[82:83], v[88:89]
	v_cndmask_b32_e32 v85, v184, v105, vcc
	v_pk_add_f32 v[82:83], v[82:83], v[90:91]
	v_lshlrev_b32_e32 v187, 2, v85
	v_add_f32_e32 v82, v82, v83
	ds_bpermute_b32 v83, v186, v82
	v_cmp_lt_i32_e32 vcc, v108, v109
	v_xor_b32_e32 v84, 8, v184
	v_xor_b32_e32 v85, 16, v184
	v_cndmask_b32_e32 v86, v184, v108, vcc
	s_waitcnt lgkmcnt(0)
	v_add_f32_e32 v82, v82, v83
	ds_bpermute_b32 v83, v187, v82
	v_lshlrev_b32_e32 v188, 2, v86
	v_cmp_lt_i32_e32 vcc, v84, v109
	v_xor_b32_e32 v86, 32, v184
	v_lshl_add_u64 v[98:99], v[68:69], 0, s[26:27]
	s_waitcnt lgkmcnt(0)
	v_add_f32_e32 v82, v82, v83
	ds_bpermute_b32 v83, v188, v82
	v_cndmask_b32_e32 v84, v184, v84, vcc
	v_lshlrev_b32_e32 v189, 2, v84
	v_cmp_lt_i32_e32 vcc, v85, v109
	s_lshl_b64 s[26:27], s[40:41], 12
	s_waitcnt lgkmcnt(0)
	v_add_f32_e32 v84, v82, v83
	ds_bpermute_b32 v87, v189, v84
	v_cndmask_b32_e32 v85, v184, v85, vcc
	v_lshlrev_b32_e32 v190, 2, v85
	v_cmp_lt_i32_e32 vcc, v86, v109
	v_lshl_add_u64 v[82:83], s[28:29], 0, v[80:81]
	s_waitcnt lgkmcnt(0)
	v_add_f32_e32 v84, v84, v87
	ds_bpermute_b32 v85, v190, v84
	v_cndmask_b32_e32 v86, v184, v86, vcc
	v_lshlrev_b32_e32 v191, 2, v86
	v_add_co_u32_e32 v86, vcc, s15, v82
	s_waitcnt lgkmcnt(0)
	v_add_f32_e32 v84, v84, v85
	ds_bpermute_b32 v85, v191, v84
	v_addc_co_u32_e32 v87, vcc, 0, v83, vcc
	s_waitcnt lgkmcnt(0)
	v_add_f32_e32 v82, v84, v85
	v_fmamk_f32 v82, v82, 0x3a000000, v183
	v_mul_f32_e32 v83, 0x4b800000, v82
	v_cmp_gt_f32_e32 vcc, s13, v82
	s_nop 1
	v_cndmask_b32_e32 v82, v82, v83, vcc
	v_rsq_f32_e32 v82, v82
	s_nop 0
	v_mul_f32_e32 v83, 0x45800000, v82
	v_cndmask_b32_e32 v88, v82, v83, vcc
	v_pk_mul_f32 v[58:59], v[58:59], v[88:89] op_sel_hi:[1,0]
	v_pk_mul_f32 v[60:61], v[60:61], v[88:89] op_sel_hi:[1,0]
	v_pk_mul_f32 v[54:55], v[54:55], v[88:89] op_sel_hi:[1,0]
	v_pk_mul_f32 v[56:57], v[56:57], v[88:89] op_sel_hi:[1,0]
	v_pk_mul_f32 v[90:91], v[62:63], v[88:89] op_sel_hi:[1,0]
	v_pk_mul_f32 v[92:93], v[64:65], v[88:89] op_sel_hi:[1,0]
	v_pk_mul_f32 v[82:83], v[4:5], v[60:61]
	v_pk_mul_f32 v[84:85], v[2:3], v[58:59]
	v_pk_mul_f32 v[62:63], v[8:9], v[56:57]
	v_pk_mul_f32 v[64:65], v[6:7], v[54:55]
	v_cvt_pk_bf16_f32 v58, v84, v85
	v_cvt_pk_bf16_f32 v59, v82, v83
	v_cvt_pk_bf16_f32 v61, v62, v63
	v_pk_mul_f32 v[50:51], v[50:51], v[88:89] op_sel_hi:[1,0]
	v_cvt_pk_bf16_f32 v60, v64, v65
	v_pk_mul_f32 v[52:53], v[52:53], v[88:89] op_sel_hi:[1,0]
	v_pk_mul_f32 v[54:55], v[12:13], v[92:93]
	v_pk_mul_f32 v[56:57], v[10:11], v[90:91]
	v_cvt_pk_bf16_f32 v91, v54, v55
	v_pk_mul_f32 v[38:39], v[38:39], v[88:89] op_sel_hi:[1,0]
	v_cvt_pk_bf16_f32 v90, v56, v57
	global_store_dwordx2 v[86:87], v[58:59], off
	global_store_dwordx2 v[86:87], v[60:61], off offset:512
	global_store_dwordx2 v[86:87], v[90:91], off offset:1024
	v_pk_mul_f32 v[58:59], v[16:17], v[52:53]
	v_pk_mul_f32 v[60:61], v[14:15], v[50:51]
	v_cvt_pk_bf16_f32 v51, v58, v59
	v_pk_mul_f32 v[40:41], v[40:41], v[88:89] op_sel_hi:[1,0]
	v_cvt_pk_bf16_f32 v50, v60, v61
	global_store_dwordx2 v[86:87], v[50:51], off offset:1536
	v_pk_mul_f32 v[50:51], v[20:21], v[40:41]
	v_pk_mul_f32 v[52:53], v[18:19], v[38:39]
	v_cvt_pk_bf16_f32 v39, v50, v51
	v_pk_mul_f32 v[40:41], v[48:49], v[88:89] op_sel_hi:[1,0]
	v_cvt_pk_bf16_f32 v38, v52, v53
	global_store_dwordx2 v[86:87], v[38:39], off offset:2048
	v_pk_mul_f32 v[38:39], v[46:47], v[88:89] op_sel_hi:[1,0]
	v_pk_mul_f32 v[46:47], v[24:25], v[40:41]
	v_pk_mul_f32 v[48:49], v[22:23], v[38:39]
	v_cvt_pk_bf16_f32 v39, v46, v47
	v_pk_mul_f32 v[40:41], v[42:43], v[88:89] op_sel_hi:[1,0]
	v_cvt_pk_bf16_f32 v38, v48, v49
	global_store_dwordx2 v[86:87], v[38:39], off offset:2560
	v_pk_mul_f32 v[38:39], v[44:45], v[88:89] op_sel_hi:[1,0]
	v_pk_mul_f32 v[40:41], v[26:27], v[40:41]
	v_pk_mul_f32 v[38:39], v[28:29], v[38:39]
	v_cvt_pk_bf16_f32 v42, v40, v41
	v_add_co_u32_e32 v102, vcc, s12, v98
	v_cvt_pk_bf16_f32 v43, v38, v39
	global_store_dwordx2 v[86:87], v[42:43], off offset:3072
	v_pk_mul_f32 v[42:43], v[34:35], v[88:89] op_sel_hi:[1,0]
	v_pk_mul_f32 v[34:35], v[36:37], v[88:89] op_sel_hi:[1,0]
	v_pk_mul_f32 v[36:37], v[30:31], v[42:43]
	v_pk_mul_f32 v[34:35], v[32:33], v[34:35]
	v_cvt_pk_bf16_f32 v42, v36, v37
	v_addc_co_u32_e32 v103, vcc, 0, v99, vcc
	v_cvt_pk_bf16_f32 v43, v34, v35
	global_store_dwordx2 v[86:87], v[42:43], off offset:3584
	global_load_dwordx4 v[42:45], v[98:99], off
	s_nop 0
	global_load_dwordx4 v[86:89], v[98:99], off offset:1024
	global_load_dwordx4 v[90:93], v[98:99], off offset:2048
	global_load_dwordx4 v[94:97], v[102:103], off
	s_nop 0
	global_load_dwordx4 v[98:101], v[98:99], off offset:3072
	s_nop 0
	global_load_dwordx4 v[192:195], v[102:103], off offset:1024
	global_load_dwordx4 v[196:199], v[102:103], off offset:3072
	global_load_dwordx4 v[200:203], v[102:103], off offset:2048
	s_waitcnt vmcnt(4)
	v_mul_f32_e32 v210, v94, v94
	v_mov_b32_e32 v104, v43
	v_mov_b32_e32 v105, v87
	v_mov_b32_e32 v108, v45
	v_mov_b32_e32 v109, v89
	v_mov_b32_e32 v102, v42
	v_mov_b32_e32 v103, v86
	v_mov_b32_e32 v106, v44
	v_mov_b32_e32 v107, v88
	v_pk_mul_f32 v[110:111], v[92:93], v[92:93]
	v_pk_mul_f32 v[112:113], v[90:91], v[90:91]
	v_pk_mul_f32 v[104:105], v[104:105], v[104:105]
	v_pk_mul_f32 v[108:109], v[108:109], v[108:109]
	v_pk_mov_b32 v[208:209], v[112:113], v[110:111] op_sel:[1,0]
	v_mov_b32_e32 v113, v111
	v_pk_fma_f32 v[102:103], v[102:103], v[102:103], v[104:105]
	v_pk_fma_f32 v[104:105], v[106:107], v[106:107], v[108:109]
	s_waitcnt vmcnt(3)
	v_mul_f32_e32 v114, v99, v99
	v_mul_f32_e32 v116, v101, v101
	v_pk_add_f32 v[106:107], v[208:209], v[112:113]
	v_pk_add_f32 v[102:103], v[102:103], v[104:105]
	v_mul_f32_e32 v211, v95, v95
	v_mul_f32_e32 v212, v96, v96
	v_mul_f32_e32 v213, v97, v97
	v_pk_fma_f32 v[110:111], v[98:99], v[98:99], v[114:115] op_sel_hi:[1,1,0]
	v_pk_fma_f32 v[114:115], v[100:101], v[100:101], v[116:117] op_sel_hi:[1,1,0]
	v_pk_add_f32 v[104:105], v[106:107], v[106:107] op_sel:[0,1] op_sel_hi:[1,0]
	v_pk_add_f32 v[102:103], v[102:103], v[102:103] op_sel:[0,1] op_sel_hi:[1,0]
	s_waitcnt vmcnt(2)
	v_pk_mul_f32 v[204:205], v[194:195], v[194:195]
	v_pk_mul_f32 v[206:207], v[192:193], v[192:193]
	v_mov_b32_e32 v111, v212
	v_mov_b32_e32 v115, v213
	v_mov_b32_e32 v105, v211
	v_mov_b32_e32 v103, v210
	v_pk_mov_b32 v[116:117], v[206:207], v[204:205] op_sel:[1,0]
	v_pk_add_f32 v[106:107], v[110:111], v[114:115]
	v_pk_add_f32 v[102:103], v[102:103], v[104:105]
	v_mov_b32_e32 v207, v205
	v_pk_add_f32 v[102:103], v[102:103], v[106:107]
	v_pk_add_f32 v[104:105], v[116:117], v[206:207]
	s_waitcnt vmcnt(1)
	v_mul_f32_e32 v106, v196, v196
	v_mul_f32_e32 v107, v197, v197
	v_pk_add_f32 v[102:103], v[102:103], v[102:103] op_sel:[0,1] op_sel_hi:[1,0]
	v_pk_add_f32 v[104:105], v[104:105], v[104:105] op_sel:[0,1] op_sel_hi:[1,0]
	v_mov_b32_e32 v103, v106
	v_mov_b32_e32 v105, v107
	v_pk_add_f32 v[102:103], v[102:103], v[104:105]
	s_waitcnt vmcnt(0)
	v_mul_f32_e32 v104, v201, v201
	v_mul_f32_e32 v106, v203, v203
	v_mul_f32_e32 v108, v198, v198
	v_mul_f32_e32 v109, v199, v199
	v_pk_fma_f32 v[104:105], v[200:201], v[200:201], v[104:105] op_sel_hi:[1,1,0]
	v_pk_fma_f32 v[106:107], v[202:203], v[202:203], v[106:107] op_sel_hi:[1,1,0]
	v_mov_b32_e32 v105, v108
	v_mov_b32_e32 v107, v109
	v_pk_add_f32 v[104:105], v[104:105], v[106:107]
	v_lshl_add_u64 v[204:205], v[70:71], 0, s[26:27]
	v_pk_add_f32 v[102:103], v[102:103], v[104:105]
	s_nop 0
	v_add_f32_e32 v102, v102, v103
	ds_bpermute_b32 v103, v186, v102
	s_waitcnt lgkmcnt(0)
	v_add_f32_e32 v102, v102, v103
	ds_bpermute_b32 v103, v187, v102
	s_waitcnt lgkmcnt(0)
	v_add_f32_e32 v102, v102, v103
	ds_bpermute_b32 v103, v188, v102
	s_waitcnt lgkmcnt(0)
	v_add_f32_e32 v102, v102, v103
	ds_bpermute_b32 v103, v189, v102
	s_waitcnt lgkmcnt(0)
	v_add_f32_e32 v102, v102, v103
	ds_bpermute_b32 v103, v190, v102
	s_waitcnt lgkmcnt(0)
	v_add_f32_e32 v102, v102, v103
	ds_bpermute_b32 v103, v191, v102
	s_waitcnt lgkmcnt(0)
	v_add_f32_e32 v102, v102, v103
	v_fmamk_f32 v102, v102, 0x3a000000, v183
	v_mul_f32_e32 v103, 0x4b800000, v102
	v_cmp_gt_f32_e32 vcc, s13, v102
	s_nop 1
	v_cndmask_b32_e32 v102, v102, v103, vcc
	v_rsq_f32_e32 v102, v102
	s_nop 0
	v_mul_f32_e32 v103, 0x45800000, v102
	v_cndmask_b32_e32 v206, v102, v103, vcc
	v_pk_mul_f32 v[42:43], v[42:43], v[206:207] op_sel_hi:[1,0]
	v_pk_mul_f32 v[44:45], v[44:45], v[206:207] op_sel_hi:[1,0]
	v_pk_mul_f32 v[86:87], v[86:87], v[206:207] op_sel_hi:[1,0]
	v_pk_mul_f32 v[88:89], v[88:89], v[206:207] op_sel_hi:[1,0]
	v_pk_mul_f32 v[114:115], v[4:5], v[44:45]
	v_pk_mul_f32 v[116:117], v[2:3], v[42:43]
	v_pk_mul_f32 v[110:111], v[8:9], v[88:89]
	v_pk_mul_f32 v[112:113], v[6:7], v[86:87]
	v_cvt_pk_bf16_f32 v42, v116, v117
	v_cvt_pk_bf16_f32 v43, v114, v115
	v_cvt_pk_bf16_f32 v45, v110, v111
	global_store_dwordx2 v[204:205], v[42:43], off
	v_cvt_pk_bf16_f32 v44, v112, v113
	global_store_dwordx2 v[204:205], v[44:45], off offset:512
	v_pk_mul_f32 v[42:43], v[90:91], v[206:207] op_sel_hi:[1,0]
	v_pk_mul_f32 v[44:45], v[92:93], v[206:207] op_sel_hi:[1,0]
	v_pk_mul_f32 v[108:109], v[10:11], v[42:43]
	v_pk_mul_f32 v[104:105], v[12:13], v[44:45]
	v_cvt_pk_bf16_f32 v42, v108, v109
	v_pk_mul_f32 v[44:45], v[100:101], v[206:207] op_sel_hi:[1,0]
	v_cvt_pk_bf16_f32 v43, v104, v105
	global_store_dwordx2 v[204:205], v[42:43], off offset:1024
	v_pk_mul_f32 v[42:43], v[98:99], v[206:207] op_sel_hi:[1,0]
	v_pk_mul_f32 v[102:103], v[16:17], v[44:45]
	v_pk_mul_f32 v[106:107], v[14:15], v[42:43]
	v_cvt_pk_bf16_f32 v43, v102, v103
	v_pk_mul_f32 v[44:45], v[96:97], v[206:207] op_sel_hi:[1,0]
	v_cvt_pk_bf16_f32 v42, v106, v107
	global_store_dwordx2 v[204:205], v[42:43], off offset:1536
	v_pk_mul_f32 v[42:43], v[94:95], v[206:207] op_sel_hi:[1,0]
	v_pk_mul_f32 v[96:97], v[20:21], v[44:45]
	v_pk_mul_f32 v[100:101], v[18:19], v[42:43]
	v_cvt_pk_bf16_f32 v43, v96, v97
	v_pk_mul_f32 v[44:45], v[194:195], v[206:207] op_sel_hi:[1,0]
	v_cvt_pk_bf16_f32 v42, v100, v101
	global_store_dwordx2 v[204:205], v[42:43], off offset:2048
	v_pk_mul_f32 v[42:43], v[192:193], v[206:207] op_sel_hi:[1,0]
	v_pk_mul_f32 v[94:95], v[24:25], v[44:45]
	v_pk_mul_f32 v[98:99], v[22:23], v[42:43]
	v_cvt_pk_bf16_f32 v43, v94, v95
	v_pk_mul_f32 v[44:45], v[202:203], v[206:207] op_sel_hi:[1,0]
	v_cvt_pk_bf16_f32 v42, v98, v99
	global_store_dwordx2 v[204:205], v[42:43], off offset:2560
	v_pk_mul_f32 v[42:43], v[200:201], v[206:207] op_sel_hi:[1,0]
	v_med3_f32 v86, v84, s17, v185
	v_med3_f32 v87, v85, s17, v185
	v_pk_mul_f32 v[88:89], v[28:29], v[44:45]
	v_pk_mul_f32 v[90:91], v[26:27], v[42:43]
	v_cvt_pk_bf16_f32 v43, v88, v89
	v_cvt_pk_fp8_f32 v192, v86, v87
	v_cvt_pk_bf16_f32 v42, v90, v91
	global_store_dwordx2 v[204:205], v[42:43], off offset:3072
	v_pk_mul_f32 v[44:45], v[196:197], v[206:207] op_sel_hi:[1,0]
	v_pk_mul_f32 v[42:43], v[198:199], v[206:207] op_sel_hi:[1,0]
	v_pk_mul_f32 v[92:93], v[30:31], v[44:45]
	v_pk_mul_f32 v[42:43], v[32:33], v[42:43]
	v_cvt_pk_bf16_f32 v44, v92, v93
	v_med3_f32 v86, v116, s17, v185
	v_cvt_pk_bf16_f32 v45, v42, v43
	global_store_dwordx2 v[204:205], v[44:45], off offset:3584
	v_med3_f32 v44, v82, s17, v185
	v_med3_f32 v45, v83, s17, v185
	v_med3_f32 v87, v117, s17, v185
	v_cvt_pk_fp8_f32 v192, v44, v45 op_sel:[0,0,1]
	v_cvt_pk_fp8_f32 v193, v86, v87
	v_lshl_add_u64 v[44:45], s[28:29], 0, v[78:79]
	v_add_co_u32_e32 v44, vcc, s35, v44
	v_med3_f32 v86, v114, s17, v185
	s_nop 0
	v_addc_co_u32_e32 v45, vcc, 0, v45, vcc
	v_med3_f32 v87, v115, s17, v185
	global_store_dword v[44:45], v192, off
	v_cvt_pk_fp8_f32 v193, v86, v87 op_sel:[0,0,1]
	v_med3_f32 v192, v64, s17, v185
	v_med3_f32 v194, v65, s17, v185
	v_cvt_pk_fp8_f32 v195, v192, v194
	v_lshl_add_u64 v[86:87], v[72:73], 0, s[50:51]
	global_store_dword v[86:87], v193, off
	v_med3_f32 v192, v62, s17, v185
	v_med3_f32 v193, v63, s17, v185
	v_cvt_pk_fp8_f32 v195, v192, v193 op_sel:[0,0,1]
	v_med3_f32 v192, v112, s17, v185
	v_med3_f32 v193, v113, s17, v185
	v_cvt_pk_fp8_f32 v194, v192, v193
	v_med3_f32 v192, v110, s17, v185
	v_med3_f32 v193, v111, s17, v185
	global_store_dword v[44:45], v195, off offset:256
	v_cvt_pk_fp8_f32 v194, v192, v193 op_sel:[0,0,1]
	v_med3_f32 v192, v56, s17, v185
	v_med3_f32 v193, v57, s17, v185
	v_cvt_pk_fp8_f32 v195, v192, v193
	v_med3_f32 v192, v54, s17, v185
	v_med3_f32 v193, v55, s17, v185
	global_store_dword v[86:87], v194, off offset:256
	v_cvt_pk_fp8_f32 v195, v192, v193 op_sel:[0,0,1]
	v_med3_f32 v192, v108, s17, v185
	v_med3_f32 v193, v109, s17, v185
	v_cvt_pk_fp8_f32 v194, v192, v193
	v_med3_f32 v192, v104, s17, v185
	v_med3_f32 v193, v105, s17, v185
	global_store_dword v[44:45], v195, off offset:512
	v_cvt_pk_fp8_f32 v194, v192, v193 op_sel:[0,0,1]
	v_med3_f32 v192, v60, s17, v185
	v_med3_f32 v193, v61, s17, v185
	v_cvt_pk_fp8_f32 v195, v192, v193
	v_med3_f32 v192, v58, s17, v185
	v_med3_f32 v193, v59, s17, v185
	global_store_dword v[86:87], v194, off offset:512
	v_cvt_pk_fp8_f32 v195, v192, v193 op_sel:[0,0,1]
	v_med3_f32 v192, v106, s17, v185
	v_med3_f32 v193, v107, s17, v185
	v_cvt_pk_fp8_f32 v194, v192, v193
	v_med3_f32 v192, v102, s17, v185
	v_med3_f32 v193, v103, s17, v185
	global_store_dword v[44:45], v195, off offset:768
	v_cvt_pk_fp8_f32 v194, v192, v193 op_sel:[0,0,1]
	v_med3_f32 v192, v52, s17, v185
	v_med3_f32 v193, v53, s17, v185
	v_cvt_pk_fp8_f32 v195, v192, v193
	v_med3_f32 v192, v50, s17, v185
	v_med3_f32 v193, v51, s17, v185
	global_store_dword v[86:87], v194, off offset:768
	v_cvt_pk_fp8_f32 v195, v192, v193 op_sel:[0,0,1]
	v_med3_f32 v192, v100, s17, v185
	v_med3_f32 v193, v101, s17, v185
	v_cvt_pk_fp8_f32 v194, v192, v193
	v_med3_f32 v192, v96, s17, v185
	v_med3_f32 v193, v97, s17, v185
	global_store_dword v[44:45], v195, off offset:1024
	v_cvt_pk_fp8_f32 v194, v192, v193 op_sel:[0,0,1]
	v_med3_f32 v192, v48, s17, v185
	v_med3_f32 v193, v49, s17, v185
	v_cvt_pk_fp8_f32 v195, v192, v193
	v_med3_f32 v192, v46, s17, v185
	v_med3_f32 v193, v47, s17, v185
	global_store_dword v[86:87], v194, off offset:1024
	v_cvt_pk_fp8_f32 v195, v192, v193 op_sel:[0,0,1]
	v_med3_f32 v192, v98, s17, v185
	v_med3_f32 v193, v99, s17, v185
	v_cvt_pk_fp8_f32 v194, v192, v193
	v_med3_f32 v192, v94, s17, v185
	v_med3_f32 v193, v95, s17, v185
	global_store_dword v[44:45], v195, off offset:1280
	v_cvt_pk_fp8_f32 v194, v192, v193 op_sel:[0,0,1]
	v_med3_f32 v193, v40, s17, v185
	v_med3_f32 v195, v41, s17, v185
	v_cvt_pk_fp8_f32 v192, v193, v195
	global_store_dword v[86:87], v194, off offset:1280
	v_med3_f32 v193, v38, s17, v185
	v_med3_f32 v194, v39, s17, v185
	v_cvt_pk_fp8_f32 v192, v193, v194 op_sel:[0,0,1]
	v_med3_f32 v194, v90, s17, v185
	v_med3_f32 v195, v91, s17, v185
	v_cvt_pk_fp8_f32 v193, v194, v195
	v_med3_f32 v197, v36, s17, v185
	v_med3_f32 v198, v37, s17, v185
	v_cvt_pk_fp8_f32 v194, v197, v198
	ds_read_b128 v[198:201], v118
	ds_read_b128 v[202:205], v118 offset:1024
	v_med3_f32 v195, v88, s17, v185
	v_med3_f32 v196, v89, s17, v185
	v_cvt_pk_fp8_f32 v193, v195, v196 op_sel:[0,0,1]
	v_med3_f32 v195, v34, s17, v185
	v_med3_f32 v196, v35, s17, v185
	v_cvt_pk_fp8_f32 v194, v195, v196 op_sel:[0,0,1]
	v_med3_f32 v196, v92, s17, v185
	v_med3_f32 v197, v93, s17, v185
	v_mov_b32_e32 v195, 0
	v_cvt_pk_fp8_f32 v195, v196, v197
	s_waitcnt lgkmcnt(1)
	v_mul_f32_e32 v197, v85, v199
	v_mul_f32_e32 v199, v117, v199
	v_fmac_f32_e32 v197, v84, v198
	v_fmac_f32_e32 v199, v116, v198
	v_mul_f32_e32 v198, v115, v201
	v_mul_f32_e32 v206, v83, v201
	v_fmac_f32_e32 v198, v114, v200
	v_fmac_f32_e32 v206, v82, v200
	v_add_f32_e32 v198, v199, v198
	v_add_f32_e32 v197, v197, v206
	v_add_f32_e32 v206, 0, v198
	s_waitcnt lgkmcnt(0)
	v_mul_f32_e32 v198, v65, v203
	v_mul_f32_e32 v199, v63, v205
	v_fmac_f32_e32 v198, v64, v202
	v_fmac_f32_e32 v199, v62, v204
	v_add_f32_e32 v197, 0, v197
	v_add_f32_e32 v198, v198, v199
	v_add_f32_e32 v197, v197, v198
	v_mul_f32_e32 v203, v113, v203
	ds_read_b128 v[198:201], v118 offset:2048
	v_fmac_f32_e32 v203, v112, v202
	v_mul_f32_e32 v202, v111, v205
	v_fmac_f32_e32 v202, v110, v204
	v_add_f32_e32 v202, v203, v202
	v_add_f32_e32 v206, v206, v202
	ds_read_b128 v[202:205], v118 offset:3072
	s_waitcnt lgkmcnt(1)
	v_mul_f32_e32 v207, v57, v199
	v_mul_f32_e32 v199, v109, v199
	v_fmac_f32_e32 v207, v56, v198
	v_fmac_f32_e32 v199, v108, v198
	v_mul_f32_e32 v198, v105, v201
	v_fmac_f32_e32 v198, v104, v200
	v_mul_f32_e32 v208, v55, v201
	v_add_f32_e32 v198, v199, v198
	v_fmac_f32_e32 v208, v54, v200
	v_add_f32_e32 v206, v206, v198
	s_waitcnt lgkmcnt(0)
	v_mul_f32_e32 v198, v61, v203
	v_mul_f32_e32 v199, v59, v205
	v_add_f32_e32 v207, v207, v208
	v_fmac_f32_e32 v198, v60, v202
	v_fmac_f32_e32 v199, v58, v204
	v_add_f32_e32 v197, v197, v207
	v_add_f32_e32 v198, v198, v199
	v_add_f32_e32 v197, v197, v198
	v_mul_f32_e32 v203, v107, v203
	ds_read_b128 v[198:201], v118 offset:4096
	v_fmac_f32_e32 v203, v106, v202
	v_mul_f32_e32 v202, v103, v205
	v_fmac_f32_e32 v202, v102, v204
	v_add_f32_e32 v202, v203, v202
	v_add_f32_e32 v206, v206, v202
	ds_read_b128 v[202:205], v118 offset:5120
	s_waitcnt lgkmcnt(1)
	v_mul_f32_e32 v207, v53, v199
	v_mul_f32_e32 v199, v101, v199
	v_fmac_f32_e32 v207, v52, v198
	v_fmac_f32_e32 v199, v100, v198
	v_mul_f32_e32 v198, v97, v201
	v_fmac_f32_e32 v198, v96, v200
	v_mul_f32_e32 v208, v51, v201
	v_add_f32_e32 v198, v199, v198
	v_fmac_f32_e32 v208, v50, v200
	v_add_f32_e32 v206, v206, v198
	s_waitcnt lgkmcnt(0)
	v_mul_f32_e32 v198, v49, v203
	v_mul_f32_e32 v199, v47, v205
	v_add_f32_e32 v207, v207, v208
	v_fmac_f32_e32 v198, v48, v202
	v_fmac_f32_e32 v199, v46, v204
	v_add_f32_e32 v197, v197, v207
	v_add_f32_e32 v198, v198, v199
	v_add_f32_e32 v197, v197, v198
	v_mul_f32_e32 v203, v99, v203
	ds_read_b128 v[198:201], v118 offset:6144
	v_fmac_f32_e32 v203, v98, v202
	v_mul_f32_e32 v202, v95, v205
	v_fmac_f32_e32 v202, v94, v204
	v_add_f32_e32 v202, v203, v202
	v_add_f32_e32 v206, v206, v202
	ds_read_b128 v[202:205], v118 offset:7168
	s_waitcnt lgkmcnt(1)
	v_mul_f32_e32 v207, v41, v199
	v_mul_f32_e32 v199, v91, v199
	v_fmac_f32_e32 v207, v40, v198
	v_fmac_f32_e32 v199, v90, v198
	v_mul_f32_e32 v198, v89, v201
	v_fmac_f32_e32 v198, v88, v200
	v_mul_f32_e32 v208, v39, v201
	v_add_f32_e32 v198, v199, v198
	v_fmac_f32_e32 v208, v38, v200
	v_add_f32_e32 v199, v206, v198
	s_waitcnt lgkmcnt(0)
	v_mul_f32_e32 v198, v37, v203
	v_mul_f32_e32 v200, v35, v205
	v_add_f32_e32 v207, v207, v208
	v_fmac_f32_e32 v198, v36, v202
	v_fmac_f32_e32 v200, v34, v204
	v_add_f32_e32 v197, v197, v207
	v_add_f32_e32 v198, v198, v200
	v_add_f32_e32 v198, v197, v198
	v_mul_f32_e32 v197, v93, v203
	v_fmac_f32_e32 v197, v92, v202
	ds_read_b128 v[200:203], v118 offset:8192
	v_mul_f32_e32 v205, v43, v205
	v_fmac_f32_e32 v205, v42, v204
	v_add_f32_e32 v197, v197, v205
	ds_read_b128 v[204:207], v118 offset:9216
	v_add_f32_e32 v197, v199, v197
	s_waitcnt lgkmcnt(1)
	v_mul_f32_e32 v199, v85, v201
	v_mul_f32_e32 v201, v117, v201
	v_fmac_f32_e32 v199, v84, v200
	v_fmac_f32_e32 v201, v116, v200
	v_mul_f32_e32 v200, v115, v203
	v_mul_f32_e32 v208, v83, v203
	v_fmac_f32_e32 v200, v114, v202
	v_fmac_f32_e32 v208, v82, v202
	v_add_f32_e32 v200, v201, v200
	v_add_f32_e32 v199, v199, v208
	v_add_f32_e32 v208, 0, v200
	s_waitcnt lgkmcnt(0)
	v_mul_f32_e32 v200, v65, v205
	v_mul_f32_e32 v201, v63, v207
	v_fmac_f32_e32 v200, v64, v204
	v_fmac_f32_e32 v201, v62, v206
	v_add_f32_e32 v199, 0, v199
	v_add_f32_e32 v200, v200, v201
	v_add_f32_e32 v199, v199, v200
	v_mul_f32_e32 v205, v113, v205
	ds_read_b128 v[200:203], v118 offset:10240
	v_fmac_f32_e32 v205, v112, v204
	v_mul_f32_e32 v204, v111, v207
	v_fmac_f32_e32 v204, v110, v206
	v_add_f32_e32 v204, v205, v204
	v_add_f32_e32 v208, v208, v204
	ds_read_b128 v[204:207], v118 offset:11264
	s_waitcnt lgkmcnt(1)
	v_mul_f32_e32 v209, v57, v201
	v_mul_f32_e32 v201, v109, v201
	v_fmac_f32_e32 v209, v56, v200
	v_fmac_f32_e32 v201, v108, v200
	v_mul_f32_e32 v200, v105, v203
	v_fmac_f32_e32 v200, v104, v202
	v_mul_f32_e32 v210, v55, v203
	v_add_f32_e32 v200, v201, v200
	v_fmac_f32_e32 v210, v54, v202
	v_add_f32_e32 v208, v208, v200
	s_waitcnt lgkmcnt(0)
	v_mul_f32_e32 v200, v61, v205
	v_mul_f32_e32 v201, v59, v207
	v_add_f32_e32 v209, v209, v210
	v_fmac_f32_e32 v200, v60, v204
	v_fmac_f32_e32 v201, v58, v206
	v_add_f32_e32 v199, v199, v209
	v_add_f32_e32 v200, v200, v201
	v_add_f32_e32 v199, v199, v200
	v_mul_f32_e32 v205, v107, v205
	ds_read_b128 v[200:203], v118 offset:12288
	v_fmac_f32_e32 v205, v106, v204
	v_mul_f32_e32 v204, v103, v207
	v_fmac_f32_e32 v204, v102, v206
	v_add_f32_e32 v204, v205, v204
	v_add_f32_e32 v208, v208, v204
	ds_read_b128 v[204:207], v118 offset:13312
	s_waitcnt lgkmcnt(1)
	v_mul_f32_e32 v209, v53, v201
	v_mul_f32_e32 v201, v101, v201
	v_fmac_f32_e32 v209, v52, v200
	v_fmac_f32_e32 v201, v100, v200
	v_mul_f32_e32 v200, v97, v203
	v_fmac_f32_e32 v200, v96, v202
	v_mul_f32_e32 v210, v51, v203
	v_add_f32_e32 v200, v201, v200
	v_fmac_f32_e32 v210, v50, v202
	v_add_f32_e32 v208, v208, v200
	s_waitcnt lgkmcnt(0)
	v_mul_f32_e32 v200, v49, v205
	v_mul_f32_e32 v201, v47, v207
	v_add_f32_e32 v209, v209, v210
	v_fmac_f32_e32 v200, v48, v204
	v_fmac_f32_e32 v201, v46, v206
	v_add_f32_e32 v199, v199, v209
	v_add_f32_e32 v200, v200, v201
	v_add_f32_e32 v199, v199, v200
	v_mul_f32_e32 v205, v99, v205
	ds_read_b128 v[200:203], v118 offset:14336
	v_fmac_f32_e32 v205, v98, v204
	v_mul_f32_e32 v204, v95, v207
	v_fmac_f32_e32 v204, v94, v206
	v_add_f32_e32 v204, v205, v204
	v_add_f32_e32 v208, v208, v204
	ds_read_b128 v[204:207], v118 offset:15360
	s_waitcnt lgkmcnt(1)
	v_mul_f32_e32 v209, v41, v201
	v_mul_f32_e32 v201, v91, v201
	v_fmac_f32_e32 v209, v40, v200
	v_fmac_f32_e32 v201, v90, v200
	v_mul_f32_e32 v200, v89, v203
	v_fmac_f32_e32 v200, v88, v202
	v_mul_f32_e32 v210, v39, v203
	v_add_f32_e32 v200, v201, v200
	v_fmac_f32_e32 v210, v38, v202
	v_add_f32_e32 v201, v208, v200
	s_waitcnt lgkmcnt(0)
	v_mul_f32_e32 v200, v37, v205
	v_mul_f32_e32 v202, v35, v207
	v_add_f32_e32 v209, v209, v210
	v_fmac_f32_e32 v200, v36, v204
	v_fmac_f32_e32 v202, v34, v206
	v_add_f32_e32 v199, v199, v209
	v_add_f32_e32 v200, v200, v202
	v_add_f32_e32 v200, v199, v200
	v_mul_f32_e32 v199, v93, v205
	v_fmac_f32_e32 v199, v92, v204
	ds_read_b128 v[202:205], v118 offset:16384
	v_mul_f32_e32 v207, v43, v207
	v_fmac_f32_e32 v207, v42, v206
	v_add_f32_e32 v199, v199, v207
	ds_read_b128 v[206:209], v118 offset:17408
	v_add_f32_e32 v199, v201, v199
	s_waitcnt lgkmcnt(1)
	v_mul_f32_e32 v201, v85, v203
	v_mul_f32_e32 v203, v117, v203
	v_fmac_f32_e32 v201, v84, v202
	v_fmac_f32_e32 v203, v116, v202
	v_mul_f32_e32 v202, v115, v205
	v_mul_f32_e32 v210, v83, v205
	v_fmac_f32_e32 v202, v114, v204
	v_fmac_f32_e32 v210, v82, v204
	v_add_f32_e32 v202, v203, v202
	v_add_f32_e32 v201, v201, v210
	v_add_f32_e32 v210, 0, v202
	s_waitcnt lgkmcnt(0)
	v_mul_f32_e32 v202, v65, v207
	v_mul_f32_e32 v203, v63, v209
	v_fmac_f32_e32 v202, v64, v206
	v_fmac_f32_e32 v203, v62, v208
	v_add_f32_e32 v201, 0, v201
	v_add_f32_e32 v202, v202, v203
	v_add_f32_e32 v201, v201, v202
	v_mul_f32_e32 v207, v113, v207
	ds_read_b128 v[202:205], v118 offset:18432
	v_fmac_f32_e32 v207, v112, v206
	v_mul_f32_e32 v206, v111, v209
	v_fmac_f32_e32 v206, v110, v208
	v_add_f32_e32 v206, v207, v206
	v_add_f32_e32 v210, v210, v206
	ds_read_b128 v[206:209], v118 offset:19456
	s_waitcnt lgkmcnt(1)
	v_mul_f32_e32 v211, v57, v203
	v_mul_f32_e32 v203, v109, v203
	v_fmac_f32_e32 v211, v56, v202
	v_fmac_f32_e32 v203, v108, v202
	v_mul_f32_e32 v202, v105, v205
	v_fmac_f32_e32 v202, v104, v204
	v_mul_f32_e32 v212, v55, v205
	v_add_f32_e32 v202, v203, v202
	v_fmac_f32_e32 v212, v54, v204
	v_add_f32_e32 v210, v210, v202
	s_waitcnt lgkmcnt(0)
	v_mul_f32_e32 v202, v61, v207
	v_mul_f32_e32 v203, v59, v209
	v_add_f32_e32 v211, v211, v212
	v_fmac_f32_e32 v202, v60, v206
	v_fmac_f32_e32 v203, v58, v208
	v_add_f32_e32 v201, v201, v211
	v_add_f32_e32 v202, v202, v203
	v_add_f32_e32 v201, v201, v202
	v_mul_f32_e32 v207, v107, v207
	ds_read_b128 v[202:205], v118 offset:20480
	v_fmac_f32_e32 v207, v106, v206
	v_mul_f32_e32 v206, v103, v209
	v_fmac_f32_e32 v206, v102, v208
	v_add_f32_e32 v206, v207, v206
	v_add_f32_e32 v210, v210, v206
	ds_read_b128 v[206:209], v118 offset:21504
	s_waitcnt lgkmcnt(1)
	v_mul_f32_e32 v211, v53, v203
	v_mul_f32_e32 v203, v101, v203
	v_fmac_f32_e32 v211, v52, v202
	v_fmac_f32_e32 v203, v100, v202
	v_mul_f32_e32 v202, v97, v205
	v_fmac_f32_e32 v202, v96, v204
	v_mul_f32_e32 v212, v51, v205
	v_add_f32_e32 v202, v203, v202
	v_fmac_f32_e32 v212, v50, v204
	v_add_f32_e32 v210, v210, v202
	s_waitcnt lgkmcnt(0)
	v_mul_f32_e32 v202, v49, v207
	v_mul_f32_e32 v203, v47, v209
	v_add_f32_e32 v211, v211, v212
	v_fmac_f32_e32 v202, v48, v206
	v_fmac_f32_e32 v203, v46, v208
	v_add_f32_e32 v201, v201, v211
	v_add_f32_e32 v202, v202, v203
	v_add_f32_e32 v201, v201, v202
	v_mul_f32_e32 v207, v99, v207
	ds_read_b128 v[202:205], v118 offset:22528
	v_fmac_f32_e32 v207, v98, v206
	v_mul_f32_e32 v206, v95, v209
	v_fmac_f32_e32 v206, v94, v208
	v_add_f32_e32 v206, v207, v206
	v_add_f32_e32 v210, v210, v206
	ds_read_b128 v[206:209], v118 offset:23552
	s_waitcnt lgkmcnt(1)
	v_mul_f32_e32 v211, v41, v203
	v_mul_f32_e32 v203, v91, v203
	v_fmac_f32_e32 v211, v40, v202
	v_fmac_f32_e32 v203, v90, v202
	v_mul_f32_e32 v202, v89, v205
	v_fmac_f32_e32 v202, v88, v204
	v_mul_f32_e32 v212, v39, v205
	v_add_f32_e32 v202, v203, v202
	v_fmac_f32_e32 v212, v38, v204
	v_add_f32_e32 v203, v210, v202
	s_waitcnt lgkmcnt(0)
	v_mul_f32_e32 v202, v37, v207
	v_mul_f32_e32 v204, v35, v209
	v_add_f32_e32 v211, v211, v212
	v_fmac_f32_e32 v202, v36, v206
	v_fmac_f32_e32 v204, v34, v208
	v_add_f32_e32 v201, v201, v211
	v_add_f32_e32 v202, v202, v204
	v_add_f32_e32 v202, v201, v202
	v_mul_f32_e32 v201, v93, v207
	v_fmac_f32_e32 v201, v92, v206
	ds_read_b128 v[204:207], v118 offset:24576
	v_mul_f32_e32 v209, v43, v209
	v_fmac_f32_e32 v209, v42, v208
	v_add_f32_e32 v201, v201, v209
	ds_read_b128 v[208:211], v118 offset:25600
	v_add_f32_e32 v201, v203, v201
	s_waitcnt lgkmcnt(1)
	v_mul_f32_e32 v203, v85, v205
	v_mul_f32_e32 v205, v117, v205
	v_fmac_f32_e32 v203, v84, v204
	v_fmac_f32_e32 v205, v116, v204
	v_mul_f32_e32 v204, v115, v207
	v_mul_f32_e32 v212, v83, v207
	v_fmac_f32_e32 v204, v114, v206
	v_fmac_f32_e32 v212, v82, v206
	v_add_f32_e32 v204, v205, v204
	v_add_f32_e32 v203, v203, v212
	v_add_f32_e32 v212, 0, v204
	s_waitcnt lgkmcnt(0)
	v_mul_f32_e32 v204, v65, v209
	v_mul_f32_e32 v205, v63, v211
	v_fmac_f32_e32 v204, v64, v208
	v_fmac_f32_e32 v205, v62, v210
	v_add_f32_e32 v203, 0, v203
	v_add_f32_e32 v204, v204, v205
	v_add_f32_e32 v203, v203, v204
	v_mul_f32_e32 v209, v113, v209
	ds_read_b128 v[204:207], v118 offset:26624
	v_fmac_f32_e32 v209, v112, v208
	v_mul_f32_e32 v208, v111, v211
	v_fmac_f32_e32 v208, v110, v210
	v_add_f32_e32 v208, v209, v208
	v_add_f32_e32 v212, v212, v208
	ds_read_b128 v[208:211], v118 offset:27648
	s_waitcnt lgkmcnt(1)
	v_mul_f32_e32 v213, v57, v205
	v_mul_f32_e32 v205, v109, v205
	v_fmac_f32_e32 v213, v56, v204
	v_fmac_f32_e32 v205, v108, v204
	v_mul_f32_e32 v204, v105, v207
	v_fmac_f32_e32 v204, v104, v206
	v_mul_f32_e32 v214, v55, v207
	v_add_f32_e32 v204, v205, v204
	v_fmac_f32_e32 v214, v54, v206
	v_add_f32_e32 v212, v212, v204
	s_waitcnt lgkmcnt(0)
	v_mul_f32_e32 v204, v61, v209
	v_mul_f32_e32 v205, v59, v211
	v_add_f32_e32 v213, v213, v214
	v_fmac_f32_e32 v204, v60, v208
	v_fmac_f32_e32 v205, v58, v210
	v_add_f32_e32 v203, v203, v213
	v_add_f32_e32 v204, v204, v205
	v_add_f32_e32 v203, v203, v204
	v_mul_f32_e32 v209, v107, v209
	ds_read_b128 v[204:207], v118 offset:28672
	v_fmac_f32_e32 v209, v106, v208
	v_mul_f32_e32 v208, v103, v211
	v_fmac_f32_e32 v208, v102, v210
	v_add_f32_e32 v208, v209, v208
	v_add_f32_e32 v212, v212, v208
	ds_read_b128 v[208:211], v118 offset:29696
	s_waitcnt lgkmcnt(1)
	v_mul_f32_e32 v213, v53, v205
	v_mul_f32_e32 v205, v101, v205
	v_fmac_f32_e32 v213, v52, v204
	v_fmac_f32_e32 v205, v100, v204
	v_mul_f32_e32 v204, v97, v207
	v_fmac_f32_e32 v204, v96, v206
	v_mul_f32_e32 v214, v51, v207
	v_add_f32_e32 v204, v205, v204
	v_fmac_f32_e32 v214, v50, v206
	v_add_f32_e32 v212, v212, v204
	s_waitcnt lgkmcnt(0)
	v_mul_f32_e32 v204, v49, v209
	v_mul_f32_e32 v205, v47, v211
	v_add_f32_e32 v213, v213, v214
	v_fmac_f32_e32 v204, v48, v208
	v_fmac_f32_e32 v205, v46, v210
	v_add_f32_e32 v203, v203, v213
	v_add_f32_e32 v204, v204, v205
	v_add_f32_e32 v203, v203, v204
	v_mul_f32_e32 v209, v99, v209
	ds_read_b128 v[204:207], v118 offset:30720
	v_fmac_f32_e32 v209, v98, v208
	v_mul_f32_e32 v208, v95, v211
	v_fmac_f32_e32 v208, v94, v210
	v_add_f32_e32 v208, v209, v208
	v_add_f32_e32 v212, v212, v208
	ds_read_b128 v[208:211], v118 offset:31744
	s_waitcnt lgkmcnt(1)
	v_mul_f32_e32 v213, v41, v205
	v_mul_f32_e32 v205, v91, v205
	v_fmac_f32_e32 v213, v40, v204
	v_fmac_f32_e32 v205, v90, v204
	v_mul_f32_e32 v204, v89, v207
	v_fmac_f32_e32 v204, v88, v206
	v_mul_f32_e32 v214, v39, v207
	v_add_f32_e32 v204, v205, v204
	v_fmac_f32_e32 v214, v38, v206
	v_add_f32_e32 v205, v212, v204
	s_waitcnt lgkmcnt(0)
	v_mul_f32_e32 v204, v37, v209
	v_mul_f32_e32 v206, v35, v211
	v_add_f32_e32 v213, v213, v214
	v_fmac_f32_e32 v204, v36, v208
	v_fmac_f32_e32 v206, v34, v210
	v_add_f32_e32 v203, v203, v213
	v_add_f32_e32 v204, v204, v206
	v_add_f32_e32 v204, v203, v204
	v_mul_f32_e32 v203, v93, v209
	v_fmac_f32_e32 v203, v92, v208
	ds_read_b128 v[206:209], v118 offset:32768
	v_mul_f32_e32 v211, v43, v211
	v_fmac_f32_e32 v211, v42, v210
	v_add_f32_e32 v203, v203, v211
	ds_read_b128 v[210:213], v118 offset:33792
	v_add_f32_e32 v203, v205, v203
	s_waitcnt lgkmcnt(1)
	v_mul_f32_e32 v205, v85, v207
	v_mul_f32_e32 v207, v117, v207
	v_fmac_f32_e32 v205, v84, v206
	v_fmac_f32_e32 v207, v116, v206
	v_mul_f32_e32 v206, v115, v209
	v_mul_f32_e32 v214, v83, v209
	v_fmac_f32_e32 v206, v114, v208
	v_fmac_f32_e32 v214, v82, v208
	v_add_f32_e32 v206, v207, v206
	v_add_f32_e32 v205, v205, v214
	v_add_f32_e32 v214, 0, v206
	s_waitcnt lgkmcnt(0)
	v_mul_f32_e32 v206, v65, v211
	v_mul_f32_e32 v207, v63, v213
	v_fmac_f32_e32 v206, v64, v210
	v_fmac_f32_e32 v207, v62, v212
	v_add_f32_e32 v205, 0, v205
	v_add_f32_e32 v206, v206, v207
	v_add_f32_e32 v205, v205, v206
	v_mul_f32_e32 v211, v113, v211
	ds_read_b128 v[206:209], v118 offset:34816
	v_fmac_f32_e32 v211, v112, v210
	v_mul_f32_e32 v210, v111, v213
	v_fmac_f32_e32 v210, v110, v212
	v_add_f32_e32 v210, v211, v210
	v_add_f32_e32 v214, v214, v210
	ds_read_b128 v[210:213], v118 offset:35840
	s_waitcnt lgkmcnt(1)
	v_mul_f32_e32 v215, v57, v207
	v_mul_f32_e32 v207, v109, v207
	v_fmac_f32_e32 v215, v56, v206
	v_fmac_f32_e32 v207, v108, v206
	v_mul_f32_e32 v206, v105, v209
	v_fmac_f32_e32 v206, v104, v208
	v_mul_f32_e32 v216, v55, v209
	v_add_f32_e32 v206, v207, v206
	v_fmac_f32_e32 v216, v54, v208
	v_add_f32_e32 v214, v214, v206
	s_waitcnt lgkmcnt(0)
	v_mul_f32_e32 v206, v61, v211
	v_mul_f32_e32 v207, v59, v213
	v_add_f32_e32 v215, v215, v216
	v_fmac_f32_e32 v206, v60, v210
	v_fmac_f32_e32 v207, v58, v212
	v_add_f32_e32 v205, v205, v215
	v_add_f32_e32 v206, v206, v207
	v_add_f32_e32 v205, v205, v206
	v_mul_f32_e32 v211, v107, v211
	ds_read_b128 v[206:209], v118 offset:36864
	v_fmac_f32_e32 v211, v106, v210
	v_mul_f32_e32 v210, v103, v213
	v_fmac_f32_e32 v210, v102, v212
	v_add_f32_e32 v210, v211, v210
	v_add_f32_e32 v214, v214, v210
	ds_read_b128 v[210:213], v118 offset:37888
	s_waitcnt lgkmcnt(1)
	v_mul_f32_e32 v215, v53, v207
	v_mul_f32_e32 v207, v101, v207
	v_fmac_f32_e32 v215, v52, v206
	v_fmac_f32_e32 v207, v100, v206
	v_mul_f32_e32 v206, v97, v209
	v_fmac_f32_e32 v206, v96, v208
	v_mul_f32_e32 v216, v51, v209
	v_add_f32_e32 v206, v207, v206
	v_fmac_f32_e32 v216, v50, v208
	v_add_f32_e32 v214, v214, v206
	s_waitcnt lgkmcnt(0)
	v_mul_f32_e32 v206, v49, v211
	v_mul_f32_e32 v207, v47, v213
	v_add_f32_e32 v215, v215, v216
	v_fmac_f32_e32 v206, v48, v210
	v_fmac_f32_e32 v207, v46, v212
	v_add_f32_e32 v205, v205, v215
	v_add_f32_e32 v206, v206, v207
	v_add_f32_e32 v205, v205, v206
	v_mul_f32_e32 v211, v99, v211
	ds_read_b128 v[206:209], v118 offset:38912
	v_fmac_f32_e32 v211, v98, v210
	v_mul_f32_e32 v210, v95, v213
	v_fmac_f32_e32 v210, v94, v212
	v_add_f32_e32 v210, v211, v210
	v_add_f32_e32 v214, v214, v210
	ds_read_b128 v[210:213], v118 offset:39936
	s_waitcnt lgkmcnt(1)
	v_mul_f32_e32 v215, v41, v207
	v_mul_f32_e32 v207, v91, v207
	v_fmac_f32_e32 v215, v40, v206
	v_fmac_f32_e32 v207, v90, v206
	v_mul_f32_e32 v206, v89, v209
	v_fmac_f32_e32 v206, v88, v208
	v_mul_f32_e32 v216, v39, v209
	v_add_f32_e32 v206, v207, v206
	v_fmac_f32_e32 v216, v38, v208
	v_add_f32_e32 v207, v214, v206
	s_waitcnt lgkmcnt(0)
	v_mul_f32_e32 v206, v37, v211
	v_mul_f32_e32 v208, v35, v213
	v_add_f32_e32 v215, v215, v216
	v_fmac_f32_e32 v206, v36, v210
	v_fmac_f32_e32 v208, v34, v212
	v_add_f32_e32 v205, v205, v215
	v_add_f32_e32 v206, v206, v208
	v_add_f32_e32 v206, v205, v206
	v_mul_f32_e32 v205, v93, v211
	v_fmac_f32_e32 v205, v92, v210
	ds_read_b128 v[208:211], v118 offset:40960
	v_mul_f32_e32 v213, v43, v213
	v_fmac_f32_e32 v213, v42, v212
	v_add_f32_e32 v205, v205, v213
	ds_read_b128 v[212:215], v118 offset:41984
	v_add_f32_e32 v205, v207, v205
	s_waitcnt lgkmcnt(1)
	v_mul_f32_e32 v207, v85, v209
	v_mul_f32_e32 v209, v117, v209
	v_fmac_f32_e32 v207, v84, v208
	v_fmac_f32_e32 v209, v116, v208
	v_mul_f32_e32 v208, v115, v211
	v_mul_f32_e32 v216, v83, v211
	v_fmac_f32_e32 v208, v114, v210
	v_fmac_f32_e32 v216, v82, v210
	v_add_f32_e32 v208, v209, v208
	v_add_f32_e32 v207, v207, v216
	v_add_f32_e32 v216, 0, v208
	s_waitcnt lgkmcnt(0)
	v_mul_f32_e32 v208, v65, v213
	v_mul_f32_e32 v209, v63, v215
	v_fmac_f32_e32 v208, v64, v212
	v_fmac_f32_e32 v209, v62, v214
	v_add_f32_e32 v207, 0, v207
	v_add_f32_e32 v208, v208, v209
	v_add_f32_e32 v207, v207, v208
	v_mul_f32_e32 v213, v113, v213
	ds_read_b128 v[208:211], v118 offset:43008
	v_fmac_f32_e32 v213, v112, v212
	v_mul_f32_e32 v212, v111, v215
	v_fmac_f32_e32 v212, v110, v214
	v_add_f32_e32 v212, v213, v212
	v_add_f32_e32 v216, v216, v212
	ds_read_b128 v[212:215], v118 offset:44032
	s_waitcnt lgkmcnt(1)
	v_mul_f32_e32 v217, v57, v209
	v_mul_f32_e32 v209, v109, v209
	v_fmac_f32_e32 v217, v56, v208
	v_fmac_f32_e32 v209, v108, v208
	v_mul_f32_e32 v208, v105, v211
	v_fmac_f32_e32 v208, v104, v210
	v_mul_f32_e32 v219, v55, v211
	v_add_f32_e32 v208, v209, v208
	v_fmac_f32_e32 v219, v54, v210
	v_add_f32_e32 v216, v216, v208
	s_waitcnt lgkmcnt(0)
	v_mul_f32_e32 v208, v61, v213
	v_mul_f32_e32 v209, v59, v215
	v_add_f32_e32 v217, v217, v219
	v_fmac_f32_e32 v208, v60, v212
	v_fmac_f32_e32 v209, v58, v214
	v_add_f32_e32 v207, v207, v217
	v_add_f32_e32 v208, v208, v209
	v_add_f32_e32 v207, v207, v208
	v_mul_f32_e32 v213, v107, v213
	ds_read_b128 v[208:211], v118 offset:45056
	v_fmac_f32_e32 v213, v106, v212
	v_mul_f32_e32 v212, v103, v215
	v_fmac_f32_e32 v212, v102, v214
	v_add_f32_e32 v212, v213, v212
	v_add_f32_e32 v216, v216, v212
	ds_read_b128 v[212:215], v118 offset:46080
	s_waitcnt lgkmcnt(1)
	v_mul_f32_e32 v217, v53, v209
	v_mul_f32_e32 v209, v101, v209
	v_fmac_f32_e32 v217, v52, v208
	v_fmac_f32_e32 v209, v100, v208
	v_mul_f32_e32 v208, v97, v211
	v_fmac_f32_e32 v208, v96, v210
	v_mul_f32_e32 v219, v51, v211
	v_add_f32_e32 v208, v209, v208
	v_fmac_f32_e32 v219, v50, v210
	v_add_f32_e32 v216, v216, v208
	s_waitcnt lgkmcnt(0)
	v_mul_f32_e32 v208, v49, v213
	v_mul_f32_e32 v209, v47, v215
	v_add_f32_e32 v217, v217, v219
	v_fmac_f32_e32 v208, v48, v212
	v_fmac_f32_e32 v209, v46, v214
	v_add_f32_e32 v207, v207, v217
	v_add_f32_e32 v208, v208, v209
	v_add_f32_e32 v207, v207, v208
	v_mul_f32_e32 v213, v99, v213
	ds_read_b128 v[208:211], v118 offset:47104
	v_fmac_f32_e32 v213, v98, v212
	v_mul_f32_e32 v212, v95, v215
	v_fmac_f32_e32 v212, v94, v214
	v_add_f32_e32 v212, v213, v212
	v_add_f32_e32 v216, v216, v212
	ds_read_b128 v[212:215], v118 offset:48128
	s_waitcnt lgkmcnt(1)
	v_mul_f32_e32 v217, v41, v209
	v_mul_f32_e32 v209, v91, v209
	v_fmac_f32_e32 v217, v40, v208
	v_fmac_f32_e32 v209, v90, v208
	v_mul_f32_e32 v208, v89, v211
	v_fmac_f32_e32 v208, v88, v210
	v_mul_f32_e32 v219, v39, v211
	v_add_f32_e32 v208, v209, v208
	v_fmac_f32_e32 v219, v38, v210
	v_add_f32_e32 v209, v216, v208
	s_waitcnt lgkmcnt(0)
	v_mul_f32_e32 v208, v37, v213
	v_mul_f32_e32 v210, v35, v215
	v_add_f32_e32 v217, v217, v219
	v_fmac_f32_e32 v208, v36, v212
	v_fmac_f32_e32 v210, v34, v214
	v_add_f32_e32 v207, v207, v217
	v_add_f32_e32 v208, v208, v210
	v_add_f32_e32 v208, v207, v208
	v_mul_f32_e32 v207, v93, v213
	v_fmac_f32_e32 v207, v92, v212
	ds_read_b128 v[210:213], v118 offset:49152
	v_mul_f32_e32 v215, v43, v215
	v_fmac_f32_e32 v215, v42, v214
	v_add_f32_e32 v207, v207, v215
	ds_read_b128 v[214:217], v118 offset:50176
	v_add_f32_e32 v207, v209, v207
	s_waitcnt lgkmcnt(1)
	v_mul_f32_e32 v209, v85, v211
	v_mul_f32_e32 v211, v117, v211
	v_fmac_f32_e32 v209, v84, v210
	v_fmac_f32_e32 v211, v116, v210
	v_mul_f32_e32 v210, v115, v213
	v_mul_f32_e32 v219, v83, v213
	v_fmac_f32_e32 v210, v114, v212
	v_fmac_f32_e32 v219, v82, v212
	v_add_f32_e32 v210, v211, v210
	v_add_f32_e32 v209, v209, v219
	v_add_f32_e32 v219, 0, v210
	s_waitcnt lgkmcnt(0)
	v_mul_f32_e32 v210, v65, v215
	v_mul_f32_e32 v211, v63, v217
	v_fmac_f32_e32 v210, v64, v214
	v_fmac_f32_e32 v211, v62, v216
	v_add_f32_e32 v209, 0, v209
	v_add_f32_e32 v210, v210, v211
	v_add_f32_e32 v209, v209, v210
	v_mul_f32_e32 v215, v113, v215
	ds_read_b128 v[210:213], v118 offset:51200
	v_fmac_f32_e32 v215, v112, v214
	v_mul_f32_e32 v214, v111, v217
	v_fmac_f32_e32 v214, v110, v216
	v_add_f32_e32 v214, v215, v214
	v_add_f32_e32 v219, v219, v214
	ds_read_b128 v[214:217], v118 offset:52224
	s_waitcnt lgkmcnt(1)
	v_mul_f32_e32 v220, v57, v211
	v_mul_f32_e32 v211, v109, v211
	v_fmac_f32_e32 v220, v56, v210
	v_fmac_f32_e32 v211, v108, v210
	v_mul_f32_e32 v210, v105, v213
	v_fmac_f32_e32 v210, v104, v212
	v_mul_f32_e32 v221, v55, v213
	v_add_f32_e32 v210, v211, v210
	v_fmac_f32_e32 v221, v54, v212
	v_add_f32_e32 v219, v219, v210
	s_waitcnt lgkmcnt(0)
	v_mul_f32_e32 v210, v61, v215
	v_mul_f32_e32 v211, v59, v217
	v_add_f32_e32 v220, v220, v221
	v_fmac_f32_e32 v210, v60, v214
	v_fmac_f32_e32 v211, v58, v216
	v_add_f32_e32 v209, v209, v220
	v_add_f32_e32 v210, v210, v211
	v_add_f32_e32 v209, v209, v210
	v_mul_f32_e32 v215, v107, v215
	ds_read_b128 v[210:213], v118 offset:53248
	v_fmac_f32_e32 v215, v106, v214
	v_mul_f32_e32 v214, v103, v217
	v_fmac_f32_e32 v214, v102, v216
	v_add_f32_e32 v214, v215, v214
	v_add_f32_e32 v219, v219, v214
	ds_read_b128 v[214:217], v118 offset:54272
	s_waitcnt lgkmcnt(1)
	v_mul_f32_e32 v220, v53, v211
	v_mul_f32_e32 v211, v101, v211
	v_fmac_f32_e32 v220, v52, v210
	v_fmac_f32_e32 v211, v100, v210
	v_mul_f32_e32 v210, v97, v213
	v_fmac_f32_e32 v210, v96, v212
	v_mul_f32_e32 v221, v51, v213
	v_add_f32_e32 v210, v211, v210
	v_fmac_f32_e32 v221, v50, v212
	v_add_f32_e32 v219, v219, v210
	s_waitcnt lgkmcnt(0)
	v_mul_f32_e32 v210, v49, v215
	v_mul_f32_e32 v211, v47, v217
	v_add_f32_e32 v220, v220, v221
	v_fmac_f32_e32 v210, v48, v214
	v_fmac_f32_e32 v211, v46, v216
	v_add_f32_e32 v209, v209, v220
	v_add_f32_e32 v210, v210, v211
	v_add_f32_e32 v209, v209, v210
	v_mul_f32_e32 v215, v99, v215
	ds_read_b128 v[210:213], v118 offset:55296
	v_fmac_f32_e32 v215, v98, v214
	v_mul_f32_e32 v214, v95, v217
	v_fmac_f32_e32 v214, v94, v216
	v_add_f32_e32 v214, v215, v214
	v_add_f32_e32 v219, v219, v214
	ds_read_b128 v[214:217], v118 offset:56320
	s_waitcnt lgkmcnt(1)
	v_mul_f32_e32 v220, v41, v211
	v_mul_f32_e32 v211, v91, v211
	v_fmac_f32_e32 v220, v40, v210
	v_fmac_f32_e32 v211, v90, v210
	v_mul_f32_e32 v210, v89, v213
	v_fmac_f32_e32 v210, v88, v212
	v_mul_f32_e32 v221, v39, v213
	v_add_f32_e32 v210, v211, v210
	v_fmac_f32_e32 v221, v38, v212
	v_add_f32_e32 v211, v219, v210
	s_waitcnt lgkmcnt(0)
	v_mul_f32_e32 v210, v37, v215
	v_mul_f32_e32 v212, v35, v217
	v_add_f32_e32 v220, v220, v221
	v_fmac_f32_e32 v210, v36, v214
	v_fmac_f32_e32 v212, v34, v216
	v_add_f32_e32 v209, v209, v220
	v_add_f32_e32 v210, v210, v212
	v_add_f32_e32 v210, v209, v210
	v_mul_f32_e32 v209, v93, v215
	v_fmac_f32_e32 v209, v92, v214
	ds_read_b128 v[212:215], v118 offset:57344
	ds_read_b128 v[220:223], v118 offset:58368
	v_mul_f32_e32 v217, v43, v217
	v_fmac_f32_e32 v217, v42, v216
	v_add_f32_e32 v209, v209, v217
	v_add_f32_e32 v209, v211, v209
	s_waitcnt lgkmcnt(1)
	v_mul_f32_e32 v211, v85, v213
	v_mul_f32_e32 v213, v117, v213
	v_fmac_f32_e32 v211, v84, v212
	v_fmac_f32_e32 v213, v116, v212
	v_mul_f32_e32 v212, v115, v215
	v_mul_f32_e32 v216, v83, v215
	v_fmac_f32_e32 v212, v114, v214
	v_fmac_f32_e32 v216, v82, v214
	v_add_f32_e32 v212, v213, v212
	v_add_f32_e32 v211, v211, v216
	v_add_f32_e32 v216, 0, v212
	s_waitcnt lgkmcnt(0)
	v_mul_f32_e32 v212, v65, v221
	v_mul_f32_e32 v213, v63, v223
	v_fmac_f32_e32 v212, v64, v220
	v_fmac_f32_e32 v213, v62, v222
	v_add_f32_e32 v211, 0, v211
	v_add_f32_e32 v212, v212, v213
	v_add_f32_e32 v211, v211, v212
	ds_read_b128 v[212:215], v118 offset:59392
	v_mul_f32_e32 v217, v113, v221
	v_mul_f32_e32 v219, v111, v223
	v_fmac_f32_e32 v217, v112, v220
	v_fmac_f32_e32 v219, v110, v222
	v_add_f32_e32 v217, v217, v219
	ds_read_b128 v[220:223], v118 offset:60416
	v_add_f32_e32 v216, v216, v217
	s_waitcnt lgkmcnt(1)
	v_mul_f32_e32 v217, v57, v213
	v_mul_f32_e32 v213, v109, v213
	v_fmac_f32_e32 v217, v56, v212
	v_fmac_f32_e32 v213, v108, v212
	v_mul_f32_e32 v212, v105, v215
	v_fmac_f32_e32 v212, v104, v214
	v_mul_f32_e32 v219, v55, v215
	v_add_f32_e32 v212, v213, v212
	v_fmac_f32_e32 v219, v54, v214
	v_add_f32_e32 v216, v216, v212
	s_waitcnt lgkmcnt(0)
	v_mul_f32_e32 v212, v61, v221
	v_mul_f32_e32 v213, v59, v223
	v_add_f32_e32 v217, v217, v219
	v_fmac_f32_e32 v212, v60, v220
	v_fmac_f32_e32 v213, v58, v222
	v_add_f32_e32 v211, v211, v217
	v_add_f32_e32 v212, v212, v213
	v_add_f32_e32 v211, v211, v212
	ds_read_b128 v[212:215], v118 offset:61440
	v_mul_f32_e32 v217, v107, v221
	v_mul_f32_e32 v219, v103, v223
	v_fmac_f32_e32 v217, v106, v220
	v_fmac_f32_e32 v219, v102, v222
	v_add_f32_e32 v217, v217, v219
	ds_read_b128 v[220:223], v118 offset:62464
	v_add_f32_e32 v216, v216, v217
	s_waitcnt lgkmcnt(1)
	v_mul_f32_e32 v217, v53, v213
	v_mul_f32_e32 v213, v101, v213
	v_fmac_f32_e32 v217, v52, v212
	v_fmac_f32_e32 v213, v100, v212
	v_mul_f32_e32 v212, v97, v215
	v_fmac_f32_e32 v212, v96, v214
	v_mul_f32_e32 v219, v51, v215
	v_add_f32_e32 v212, v213, v212
	v_fmac_f32_e32 v219, v50, v214
	v_add_f32_e32 v216, v216, v212
	s_waitcnt lgkmcnt(0)
	v_mul_f32_e32 v212, v49, v221
	v_mul_f32_e32 v213, v47, v223
	v_add_f32_e32 v217, v217, v219
	v_fmac_f32_e32 v212, v48, v220
	v_fmac_f32_e32 v213, v46, v222
	v_add_f32_e32 v211, v211, v217
	v_add_f32_e32 v212, v212, v213
	v_add_f32_e32 v211, v211, v212
	ds_read_b128 v[212:215], v118 offset:63488
	v_mul_f32_e32 v217, v99, v221
	v_mul_f32_e32 v219, v95, v223
	v_fmac_f32_e32 v217, v98, v220
	v_fmac_f32_e32 v219, v94, v222
	v_add_f32_e32 v217, v217, v219
	ds_read_b128 v[220:223], v118 offset:64512
	v_add_f32_e32 v216, v216, v217
	s_waitcnt lgkmcnt(1)
	v_mul_f32_e32 v217, v41, v213
	v_mul_f32_e32 v213, v91, v213
	v_fmac_f32_e32 v217, v40, v212
	v_fmac_f32_e32 v213, v90, v212
	v_mul_f32_e32 v212, v89, v215
	v_fmac_f32_e32 v212, v88, v214
	v_mul_f32_e32 v219, v39, v215
	v_add_f32_e32 v212, v213, v212
	v_fmac_f32_e32 v219, v38, v214
	v_add_f32_e32 v213, v216, v212
	s_waitcnt lgkmcnt(0)
	v_mul_f32_e32 v212, v37, v221
	v_mul_f32_e32 v214, v35, v223
	v_add_f32_e32 v217, v217, v219
	v_fmac_f32_e32 v212, v36, v220
	v_fmac_f32_e32 v214, v34, v222
	v_add_f32_e32 v211, v211, v217
	v_add_f32_e32 v212, v212, v214
	ds_read_b128 v[214:217], v119
	v_add_f32_e32 v212, v211, v212
	v_mul_f32_e32 v211, v93, v221
	v_mul_f32_e32 v219, v43, v223
	v_fmac_f32_e32 v211, v92, v220
	v_fmac_f32_e32 v219, v42, v222
	v_add_f32_e32 v211, v211, v219
	ds_read_b128 v[220:223], v120
	v_add_f32_e32 v211, v213, v211
	s_waitcnt lgkmcnt(1)
	v_mul_f32_e32 v213, v85, v215
	v_mul_f32_e32 v215, v117, v215
	v_fmac_f32_e32 v213, v84, v214
	v_fmac_f32_e32 v215, v116, v214
	v_mul_f32_e32 v214, v115, v217
	v_mul_f32_e32 v219, v83, v217
	v_fmac_f32_e32 v214, v114, v216
	v_fmac_f32_e32 v219, v82, v216
	v_add_f32_e32 v214, v215, v214
	v_add_f32_e32 v213, v213, v219
	v_add_f32_e32 v219, 0, v214
	s_waitcnt lgkmcnt(0)
	v_mul_f32_e32 v214, v65, v221
	v_mul_f32_e32 v215, v63, v223
	v_fmac_f32_e32 v214, v64, v220
	v_fmac_f32_e32 v215, v62, v222
	v_add_f32_e32 v213, 0, v213
	v_add_f32_e32 v214, v214, v215
	v_add_f32_e32 v213, v213, v214
	v_mul_f32_e32 v221, v113, v221
	ds_read_b128 v[214:217], v121
	v_fmac_f32_e32 v221, v112, v220
	v_mul_f32_e32 v220, v111, v223
	v_fmac_f32_e32 v220, v110, v222
	v_add_f32_e32 v220, v221, v220
	v_add_f32_e32 v219, v219, v220
	ds_read_b128 v[220:223], v122
	s_waitcnt lgkmcnt(1)
	v_mul_f32_e32 v224, v57, v215
	v_mul_f32_e32 v215, v109, v215
	v_fmac_f32_e32 v224, v56, v214
	v_fmac_f32_e32 v215, v108, v214
	v_mul_f32_e32 v214, v105, v217
	v_fmac_f32_e32 v214, v104, v216
	v_mul_f32_e32 v225, v55, v217
	v_add_f32_e32 v214, v215, v214
	v_fmac_f32_e32 v225, v54, v216
	v_add_f32_e32 v219, v219, v214
	s_waitcnt lgkmcnt(0)
	v_mul_f32_e32 v214, v61, v221
	v_mul_f32_e32 v215, v59, v223
	v_add_f32_e32 v224, v224, v225
	v_fmac_f32_e32 v214, v60, v220
	v_fmac_f32_e32 v215, v58, v222
	v_add_f32_e32 v213, v213, v224
	v_add_f32_e32 v214, v214, v215
	v_add_f32_e32 v213, v213, v214
	v_mul_f32_e32 v221, v107, v221
	ds_read_b128 v[214:217], v123
	v_fmac_f32_e32 v221, v106, v220
	v_mul_f32_e32 v220, v103, v223
	v_fmac_f32_e32 v220, v102, v222
	v_add_f32_e32 v220, v221, v220
	v_add_f32_e32 v219, v219, v220
	ds_read_b128 v[220:223], v124
	s_waitcnt lgkmcnt(1)
	v_mul_f32_e32 v224, v53, v215
	v_mul_f32_e32 v215, v101, v215
	v_fmac_f32_e32 v224, v52, v214
	v_fmac_f32_e32 v215, v100, v214
	v_mul_f32_e32 v214, v97, v217
	v_fmac_f32_e32 v214, v96, v216
	v_mul_f32_e32 v225, v51, v217
	v_add_f32_e32 v214, v215, v214
	v_fmac_f32_e32 v225, v50, v216
	v_add_f32_e32 v219, v219, v214
	s_waitcnt lgkmcnt(0)
	v_mul_f32_e32 v214, v49, v221
	v_mul_f32_e32 v215, v47, v223
	v_add_f32_e32 v224, v224, v225
	v_fmac_f32_e32 v214, v48, v220
	v_fmac_f32_e32 v215, v46, v222
	v_add_f32_e32 v213, v213, v224
	v_add_f32_e32 v214, v214, v215
	v_add_f32_e32 v213, v213, v214
	v_mul_f32_e32 v221, v99, v221
	ds_read_b128 v[214:217], v125
	v_fmac_f32_e32 v221, v98, v220
	v_mul_f32_e32 v220, v95, v223
	v_fmac_f32_e32 v220, v94, v222
	v_add_f32_e32 v220, v221, v220
	v_add_f32_e32 v219, v219, v220
	ds_read_b128 v[220:223], v126
	s_waitcnt lgkmcnt(1)
	v_mul_f32_e32 v224, v41, v215
	v_mul_f32_e32 v215, v91, v215
	v_fmac_f32_e32 v224, v40, v214
	v_fmac_f32_e32 v215, v90, v214
	v_mul_f32_e32 v214, v89, v217
	v_mul_f32_e32 v225, v39, v217
	v_fmac_f32_e32 v214, v88, v216
	v_fmac_f32_e32 v225, v38, v216
	v_add_f32_e32 v214, v215, v214
	v_add_f32_e32 v224, v224, v225
	v_add_f32_e32 v215, v219, v214
	s_waitcnt lgkmcnt(0)
	v_mul_f32_e32 v214, v37, v221
	v_mul_f32_e32 v216, v35, v223
	v_add_f32_e32 v213, v213, v224
	v_fmac_f32_e32 v214, v36, v220
	v_fmac_f32_e32 v216, v34, v222
	ds_read_b128 v[224:227], v127
	v_add_f32_e32 v214, v214, v216
	v_add_f32_e32 v214, v213, v214
	v_mul_f32_e32 v213, v93, v221
	v_mul_f32_e32 v216, v43, v223
	v_fmac_f32_e32 v213, v92, v220
	v_fmac_f32_e32 v216, v42, v222
	v_add_f32_e32 v213, v213, v216
	ds_read_b128 v[220:223], v128
	v_add_f32_e32 v213, v215, v213
	s_waitcnt lgkmcnt(1)
	v_mul_f32_e32 v215, v85, v225
	v_mul_f32_e32 v216, v83, v227
	v_fmac_f32_e32 v215, v84, v224
	v_fmac_f32_e32 v216, v82, v226
	v_add_f32_e32 v215, v215, v216
	v_mul_f32_e32 v216, v117, v225
	v_mul_f32_e32 v217, v115, v227
	v_fmac_f32_e32 v216, v116, v224
	v_fmac_f32_e32 v217, v114, v226
	v_add_f32_e32 v216, v216, v217
	s_waitcnt lgkmcnt(0)
	v_mul_f32_e32 v217, v65, v221
	v_mul_f32_e32 v219, v63, v223
	v_fmac_f32_e32 v217, v64, v220
	v_fmac_f32_e32 v219, v62, v222
	ds_read_b128 v[224:227], v129
	v_add_f32_e32 v215, 0, v215
	v_add_f32_e32 v217, v217, v219
	v_add_f32_e32 v215, v215, v217
	v_mul_f32_e32 v217, v113, v221
	v_mul_f32_e32 v219, v111, v223
	v_fmac_f32_e32 v217, v112, v220
	v_fmac_f32_e32 v219, v110, v222
	v_add_f32_e32 v216, 0, v216
	v_add_f32_e32 v217, v217, v219
	v_add_f32_e32 v216, v216, v217
	ds_read_b128 v[220:223], v130
	s_waitcnt lgkmcnt(1)
	v_mul_f32_e32 v217, v57, v225
	v_mul_f32_e32 v219, v55, v227
	v_fmac_f32_e32 v217, v56, v224
	v_fmac_f32_e32 v219, v54, v226
	v_add_f32_e32 v217, v217, v219
	v_add_f32_e32 v215, v215, v217
	v_mul_f32_e32 v217, v109, v225
	v_mul_f32_e32 v219, v105, v227
	v_fmac_f32_e32 v217, v108, v224
	v_fmac_f32_e32 v219, v104, v226
	v_add_f32_e32 v217, v217, v219
	v_add_f32_e32 v216, v216, v217
	s_waitcnt lgkmcnt(0)
	v_mul_f32_e32 v217, v61, v221
	v_mul_f32_e32 v219, v59, v223
	v_fmac_f32_e32 v217, v60, v220
	v_fmac_f32_e32 v219, v58, v222
	ds_read_b128 v[224:227], v131
	v_add_f32_e32 v217, v217, v219
	v_add_f32_e32 v215, v215, v217
	v_mul_f32_e32 v217, v107, v221
	v_mul_f32_e32 v219, v103, v223
	v_fmac_f32_e32 v217, v106, v220
	v_fmac_f32_e32 v219, v102, v222
	v_add_f32_e32 v217, v217, v219
	v_add_f32_e32 v216, v216, v217
	ds_read_b128 v[220:223], v132
	s_waitcnt lgkmcnt(1)
	v_mul_f32_e32 v217, v53, v225
	v_mul_f32_e32 v219, v51, v227
	v_fmac_f32_e32 v217, v52, v224
	v_fmac_f32_e32 v219, v50, v226
	v_add_f32_e32 v217, v217, v219
	v_add_f32_e32 v215, v215, v217
	v_mul_f32_e32 v217, v101, v225
	v_mul_f32_e32 v219, v97, v227
	v_fmac_f32_e32 v217, v100, v224
	v_fmac_f32_e32 v219, v96, v226
	v_add_f32_e32 v217, v217, v219
	v_add_f32_e32 v216, v216, v217
	s_waitcnt lgkmcnt(0)
	v_mul_f32_e32 v217, v49, v221
	v_mul_f32_e32 v219, v47, v223
	v_fmac_f32_e32 v217, v48, v220
	v_fmac_f32_e32 v219, v46, v222
	ds_read_b128 v[224:227], v133
	v_add_f32_e32 v217, v217, v219
	v_add_f32_e32 v215, v215, v217
	v_mul_f32_e32 v217, v99, v221
	v_mul_f32_e32 v219, v95, v223
	v_fmac_f32_e32 v217, v98, v220
	v_fmac_f32_e32 v219, v94, v222
	v_add_f32_e32 v217, v217, v219
	v_add_f32_e32 v216, v216, v217
	ds_read_b128 v[220:223], v134
	s_waitcnt lgkmcnt(1)
	v_mul_f32_e32 v217, v41, v225
	v_mul_f32_e32 v219, v39, v227
	v_fmac_f32_e32 v217, v40, v224
	v_fmac_f32_e32 v219, v38, v226
	v_add_f32_e32 v217, v217, v219
	v_add_f32_e32 v215, v215, v217
	v_mul_f32_e32 v217, v91, v225
	v_mul_f32_e32 v219, v89, v227
	v_fmac_f32_e32 v217, v90, v224
	v_fmac_f32_e32 v219, v88, v226
	v_add_f32_e32 v217, v217, v219
	v_add_f32_e32 v217, v216, v217
	s_waitcnt lgkmcnt(0)
	v_mul_f32_e32 v216, v37, v221
	v_mul_f32_e32 v219, v35, v223
	v_fmac_f32_e32 v216, v36, v220
	v_fmac_f32_e32 v219, v34, v222
	ds_read_b128 v[224:227], v135
	v_add_f32_e32 v216, v216, v219
	v_add_f32_e32 v216, v215, v216
	v_mul_f32_e32 v215, v93, v221
	v_mul_f32_e32 v219, v43, v223
	v_fmac_f32_e32 v215, v92, v220
	v_fmac_f32_e32 v219, v42, v222
	v_add_f32_e32 v215, v215, v219
	v_add_f32_e32 v215, v217, v215
	ds_read_b128 v[220:223], v136
	s_waitcnt lgkmcnt(1)
	v_mul_f32_e32 v217, v85, v225
	v_mul_f32_e32 v219, v83, v227
	v_fmac_f32_e32 v217, v84, v224
	v_fmac_f32_e32 v219, v82, v226
	v_add_f32_e32 v217, v217, v219
	v_mul_f32_e32 v219, v117, v225
	v_fmac_f32_e32 v219, v116, v224
	v_mul_f32_e32 v224, v115, v227
	v_fmac_f32_e32 v224, v114, v226
	v_add_f32_e32 v219, v219, v224
	s_waitcnt lgkmcnt(0)
	v_mul_f32_e32 v224, v65, v221
	v_mul_f32_e32 v225, v63, v223
	v_fmac_f32_e32 v224, v64, v220
	v_fmac_f32_e32 v225, v62, v222
	v_add_f32_e32 v217, 0, v217
	v_add_f32_e32 v224, v224, v225
	v_add_f32_e32 v217, v217, v224
	v_mul_f32_e32 v221, v113, v221
	ds_read_b128 v[224:227], v137
	v_fmac_f32_e32 v221, v112, v220
	v_mul_f32_e32 v220, v111, v223
	v_fmac_f32_e32 v220, v110, v222
	v_add_f32_e32 v219, 0, v219
	v_add_f32_e32 v220, v221, v220
	v_add_f32_e32 v219, v219, v220
	ds_read_b128 v[220:223], v138
	s_waitcnt lgkmcnt(1)
	v_mul_f32_e32 v228, v57, v225
	v_mul_f32_e32 v225, v109, v225
	v_fmac_f32_e32 v228, v56, v224
	v_fmac_f32_e32 v225, v108, v224
	v_mul_f32_e32 v224, v105, v227
	v_fmac_f32_e32 v224, v104, v226
	v_mul_f32_e32 v229, v55, v227
	v_add_f32_e32 v224, v225, v224
	v_fmac_f32_e32 v229, v54, v226
	v_add_f32_e32 v219, v219, v224
	s_waitcnt lgkmcnt(0)
	v_mul_f32_e32 v224, v61, v221
	v_mul_f32_e32 v225, v59, v223
	v_add_f32_e32 v228, v228, v229
	v_fmac_f32_e32 v224, v60, v220
	v_fmac_f32_e32 v225, v58, v222
	v_add_f32_e32 v217, v217, v228
	v_add_f32_e32 v224, v224, v225
	v_add_f32_e32 v217, v217, v224
	v_mul_f32_e32 v221, v107, v221
	ds_read_b128 v[224:227], v139
	v_fmac_f32_e32 v221, v106, v220
	v_mul_f32_e32 v220, v103, v223
	v_fmac_f32_e32 v220, v102, v222
	v_add_f32_e32 v220, v221, v220
	v_add_f32_e32 v219, v219, v220
	ds_read_b128 v[220:223], v140
	s_waitcnt lgkmcnt(1)
	v_mul_f32_e32 v228, v53, v225
	v_mul_f32_e32 v225, v101, v225
	v_fmac_f32_e32 v228, v52, v224
	v_fmac_f32_e32 v225, v100, v224
	v_mul_f32_e32 v224, v97, v227
	v_fmac_f32_e32 v224, v96, v226
	v_mul_f32_e32 v229, v51, v227
	v_add_f32_e32 v224, v225, v224
	v_fmac_f32_e32 v229, v50, v226
	v_add_f32_e32 v219, v219, v224
	s_waitcnt lgkmcnt(0)
	v_mul_f32_e32 v224, v49, v221
	v_mul_f32_e32 v225, v47, v223
	v_add_f32_e32 v228, v228, v229
	v_fmac_f32_e32 v224, v48, v220
	v_fmac_f32_e32 v225, v46, v222
	v_add_f32_e32 v217, v217, v228
	v_add_f32_e32 v224, v224, v225
	v_add_f32_e32 v217, v217, v224
	v_mul_f32_e32 v221, v99, v221
	ds_read_b128 v[224:227], v141
	v_fmac_f32_e32 v221, v98, v220
	v_mul_f32_e32 v220, v95, v223
	v_fmac_f32_e32 v220, v94, v222
	v_add_f32_e32 v220, v221, v220
	v_add_f32_e32 v219, v219, v220
	ds_read_b128 v[220:223], v142
	s_waitcnt lgkmcnt(1)
	v_mul_f32_e32 v228, v41, v225
	v_mul_f32_e32 v225, v91, v225
	v_fmac_f32_e32 v228, v40, v224
	v_mul_f32_e32 v229, v39, v227
	v_fmac_f32_e32 v225, v90, v224
	v_mul_f32_e32 v224, v89, v227
	v_fmac_f32_e32 v229, v38, v226
	v_fmac_f32_e32 v224, v88, v226
	v_add_f32_e32 v228, v228, v229
	v_add_f32_e32 v224, v225, v224
	v_add_f32_e32 v217, v217, v228
	v_add_f32_e32 v228, v219, v224
	s_waitcnt lgkmcnt(0)
	v_mul_f32_e32 v219, v37, v221
	v_mul_f32_e32 v224, v35, v223
	v_fmac_f32_e32 v219, v36, v220
	v_fmac_f32_e32 v224, v34, v222
	v_add_f32_e32 v219, v219, v224
	ds_read_b128 v[224:227], v143
	v_add_f32_e32 v219, v217, v219
	v_mul_f32_e32 v217, v93, v221
	v_fmac_f32_e32 v217, v92, v220
	v_mul_f32_e32 v220, v43, v223
	v_fmac_f32_e32 v220, v42, v222
	v_add_f32_e32 v217, v217, v220
	ds_read_b128 v[220:223], v144
	v_add_f32_e32 v217, v228, v217
	s_waitcnt lgkmcnt(1)
	v_mul_f32_e32 v228, v85, v225
	v_mul_f32_e32 v225, v117, v225
	v_fmac_f32_e32 v228, v84, v224
	v_fmac_f32_e32 v225, v116, v224
	v_mul_f32_e32 v224, v115, v227
	v_mul_f32_e32 v229, v83, v227
	v_fmac_f32_e32 v224, v114, v226
	v_fmac_f32_e32 v229, v82, v226
	v_add_f32_e32 v224, v225, v224
	v_add_f32_e32 v228, v228, v229
	v_add_f32_e32 v229, 0, v224
	s_waitcnt lgkmcnt(0)
	v_mul_f32_e32 v224, v65, v221
	v_mul_f32_e32 v225, v63, v223
	v_fmac_f32_e32 v224, v64, v220
	v_fmac_f32_e32 v225, v62, v222
	v_add_f32_e32 v228, 0, v228
	v_add_f32_e32 v224, v224, v225
	v_add_f32_e32 v228, v228, v224
	v_mul_f32_e32 v221, v113, v221
	ds_read_b128 v[224:227], v145
	v_fmac_f32_e32 v221, v112, v220
	v_mul_f32_e32 v220, v111, v223
	v_fmac_f32_e32 v220, v110, v222
	v_add_f32_e32 v220, v221, v220
	v_add_f32_e32 v229, v229, v220
	ds_read_b128 v[220:223], v146
	s_waitcnt lgkmcnt(1)
	v_mul_f32_e32 v230, v57, v225
	v_mul_f32_e32 v225, v109, v225
	v_fmac_f32_e32 v230, v56, v224
	v_fmac_f32_e32 v225, v108, v224
	v_mul_f32_e32 v224, v105, v227
	v_fmac_f32_e32 v224, v104, v226
	v_mul_f32_e32 v231, v55, v227
	v_add_f32_e32 v224, v225, v224
	v_fmac_f32_e32 v231, v54, v226
	v_add_f32_e32 v229, v229, v224
	s_waitcnt lgkmcnt(0)
	v_mul_f32_e32 v224, v61, v221
	v_mul_f32_e32 v225, v59, v223
	v_add_f32_e32 v230, v230, v231
	v_fmac_f32_e32 v224, v60, v220
	v_fmac_f32_e32 v225, v58, v222
	v_add_f32_e32 v228, v228, v230
	v_add_f32_e32 v224, v224, v225
	v_add_f32_e32 v228, v228, v224
	v_mul_f32_e32 v221, v107, v221
	ds_read_b128 v[224:227], v147
	v_fmac_f32_e32 v221, v106, v220
	v_mul_f32_e32 v220, v103, v223
	v_fmac_f32_e32 v220, v102, v222
	v_add_f32_e32 v220, v221, v220
	v_add_f32_e32 v229, v229, v220
	ds_read_b128 v[220:223], v148
	s_waitcnt lgkmcnt(1)
	v_mul_f32_e32 v230, v53, v225
	v_mul_f32_e32 v225, v101, v225
	v_fmac_f32_e32 v230, v52, v224
	v_fmac_f32_e32 v225, v100, v224
	v_mul_f32_e32 v224, v97, v227
	v_fmac_f32_e32 v224, v96, v226
	v_mul_f32_e32 v231, v51, v227
	v_add_f32_e32 v224, v225, v224
	v_fmac_f32_e32 v231, v50, v226
	v_add_f32_e32 v229, v229, v224
	s_waitcnt lgkmcnt(0)
	v_mul_f32_e32 v224, v49, v221
	v_mul_f32_e32 v225, v47, v223
	v_add_f32_e32 v230, v230, v231
	v_fmac_f32_e32 v224, v48, v220
	v_fmac_f32_e32 v225, v46, v222
	v_add_f32_e32 v228, v228, v230
	v_add_f32_e32 v224, v224, v225
	v_add_f32_e32 v232, v228, v224
	ds_read_b128 v[224:227], v149
	v_mul_f32_e32 v221, v99, v221
	v_fmac_f32_e32 v221, v98, v220
	v_mul_f32_e32 v220, v95, v223
	v_fmac_f32_e32 v220, v94, v222
	v_add_f32_e32 v220, v221, v220
	v_add_f32_e32 v220, v229, v220
	ds_read_b128 v[228:231], v150
	s_waitcnt lgkmcnt(1)
	v_mul_f32_e32 v221, v41, v225
	v_mul_f32_e32 v222, v39, v227
	v_fmac_f32_e32 v221, v40, v224
	v_fmac_f32_e32 v222, v38, v226
	v_add_f32_e32 v221, v221, v222
	v_mul_f32_e32 v222, v91, v225
	v_mul_f32_e32 v223, v89, v227
	v_fmac_f32_e32 v222, v90, v224
	v_fmac_f32_e32 v223, v88, v226
	v_add_f32_e32 v222, v222, v223
	v_add_f32_e32 v220, v220, v222
	s_waitcnt lgkmcnt(0)
	v_mul_f32_e32 v222, v37, v229
	v_mul_f32_e32 v223, v35, v231
	v_fmac_f32_e32 v222, v36, v228
	v_fmac_f32_e32 v223, v34, v230
	v_add_f32_e32 v221, v232, v221
	v_add_f32_e32 v222, v222, v223
	v_add_f32_e32 v221, v221, v222
	ds_read_b128 v[222:225], v151
	v_mul_f32_e32 v226, v93, v229
	v_mul_f32_e32 v227, v43, v231
	v_fmac_f32_e32 v226, v92, v228
	v_fmac_f32_e32 v227, v42, v230
	v_add_f32_e32 v226, v226, v227
	v_add_f32_e32 v220, v220, v226
	ds_read_b128 v[226:229], v152
	s_waitcnt lgkmcnt(1)
	v_mul_f32_e32 v230, v85, v223
	v_mul_f32_e32 v223, v117, v223
	v_fmac_f32_e32 v230, v84, v222
	v_fmac_f32_e32 v223, v116, v222
	v_mul_f32_e32 v222, v115, v225
	v_mul_f32_e32 v231, v83, v225
	v_fmac_f32_e32 v222, v114, v224
	v_fmac_f32_e32 v231, v82, v224
	v_add_f32_e32 v222, v223, v222
	v_add_f32_e32 v230, v230, v231
	v_add_f32_e32 v231, 0, v222
	s_waitcnt lgkmcnt(0)
	v_mul_f32_e32 v222, v65, v227
	v_mul_f32_e32 v223, v63, v229
	v_fmac_f32_e32 v222, v64, v226
	v_fmac_f32_e32 v223, v62, v228
	v_add_f32_e32 v230, 0, v230
	v_add_f32_e32 v222, v222, v223
	v_add_f32_e32 v230, v230, v222
	v_mul_f32_e32 v227, v113, v227
	ds_read_b128 v[222:225], v153
	v_fmac_f32_e32 v227, v112, v226
	v_mul_f32_e32 v226, v111, v229
	v_fmac_f32_e32 v226, v110, v228
	v_add_f32_e32 v226, v227, v226
	v_add_f32_e32 v231, v231, v226
	ds_read_b128 v[226:229], v154
	s_waitcnt lgkmcnt(1)
	v_mul_f32_e32 v232, v57, v223
	v_mul_f32_e32 v223, v109, v223
	v_fmac_f32_e32 v232, v56, v222
	v_fmac_f32_e32 v223, v108, v222
	v_mul_f32_e32 v222, v105, v225
	v_fmac_f32_e32 v222, v104, v224
	v_mul_f32_e32 v233, v55, v225
	v_add_f32_e32 v222, v223, v222
	v_fmac_f32_e32 v233, v54, v224
	v_add_f32_e32 v231, v231, v222
	s_waitcnt lgkmcnt(0)
	v_mul_f32_e32 v222, v61, v227
	v_mul_f32_e32 v223, v59, v229
	v_add_f32_e32 v232, v232, v233
	v_fmac_f32_e32 v222, v60, v226
	v_fmac_f32_e32 v223, v58, v228
	v_add_f32_e32 v230, v230, v232
	v_add_f32_e32 v222, v222, v223
	v_add_f32_e32 v230, v230, v222
	v_mul_f32_e32 v227, v107, v227
	ds_read_b128 v[222:225], v155
	v_fmac_f32_e32 v227, v106, v226
	v_mul_f32_e32 v226, v103, v229
	v_fmac_f32_e32 v226, v102, v228
	v_add_f32_e32 v226, v227, v226
	v_add_f32_e32 v231, v231, v226
	ds_read_b128 v[226:229], v156
	s_waitcnt lgkmcnt(1)
	v_mul_f32_e32 v232, v53, v223
	v_mul_f32_e32 v223, v101, v223
	v_fmac_f32_e32 v232, v52, v222
	v_fmac_f32_e32 v223, v100, v222
	v_mul_f32_e32 v222, v97, v225
	v_fmac_f32_e32 v222, v96, v224
	v_mul_f32_e32 v233, v51, v225
	v_add_f32_e32 v222, v223, v222
	v_fmac_f32_e32 v233, v50, v224
	v_add_f32_e32 v231, v231, v222
	s_waitcnt lgkmcnt(0)
	v_mul_f32_e32 v222, v49, v227
	v_mul_f32_e32 v223, v47, v229
	v_add_f32_e32 v232, v232, v233
	v_fmac_f32_e32 v222, v48, v226
	v_fmac_f32_e32 v223, v46, v228
	v_add_f32_e32 v230, v230, v232
	v_add_f32_e32 v222, v222, v223
	v_mul_f32_e32 v227, v99, v227
	v_add_f32_e32 v230, v230, v222
	v_fmac_f32_e32 v227, v98, v226
	v_mul_f32_e32 v226, v95, v229
	ds_read_b128 v[222:225], v157
	v_fmac_f32_e32 v226, v94, v228
	v_add_f32_e32 v226, v227, v226
	v_add_f32_e32 v231, v231, v226
	ds_read_b128 v[226:229], v158
	s_waitcnt lgkmcnt(1)
	v_mul_f32_e32 v232, v41, v223
	v_mul_f32_e32 v223, v91, v223
	v_fmac_f32_e32 v232, v40, v222
	v_fmac_f32_e32 v223, v90, v222
	v_mul_f32_e32 v222, v89, v225
	v_mul_f32_e32 v233, v39, v225
	v_fmac_f32_e32 v222, v88, v224
	v_fmac_f32_e32 v233, v38, v224
	v_add_f32_e32 v222, v223, v222
	s_waitcnt lgkmcnt(0)
	v_mul_f32_e32 v223, v37, v227
	v_mul_f32_e32 v224, v35, v229
	v_add_f32_e32 v232, v232, v233
	v_fmac_f32_e32 v223, v36, v226
	v_fmac_f32_e32 v224, v34, v228
	v_add_f32_e32 v230, v230, v232
	v_add_f32_e32 v223, v223, v224
	v_add_f32_e32 v223, v230, v223
	v_mul_f32_e32 v230, v93, v227
	v_fmac_f32_e32 v230, v92, v226
	ds_read_b128 v[224:227], v159
	v_mul_f32_e32 v229, v43, v229
	v_fmac_f32_e32 v229, v42, v228
	v_add_f32_e32 v222, v231, v222
	v_add_f32_e32 v228, v230, v229
	v_add_f32_e32 v222, v222, v228
	ds_read_b128 v[228:231], v160
	s_waitcnt lgkmcnt(1)
	v_mul_f32_e32 v232, v85, v225
	v_mul_f32_e32 v225, v117, v225
	v_fmac_f32_e32 v232, v84, v224
	v_fmac_f32_e32 v225, v116, v224
	v_mul_f32_e32 v224, v115, v227
	v_mul_f32_e32 v233, v83, v227
	v_fmac_f32_e32 v224, v114, v226
	v_fmac_f32_e32 v233, v82, v226
	v_add_f32_e32 v224, v225, v224
	v_add_f32_e32 v232, v232, v233
	v_add_f32_e32 v233, 0, v224
	s_waitcnt lgkmcnt(0)
	v_mul_f32_e32 v224, v65, v229
	v_mul_f32_e32 v225, v63, v231
	v_fmac_f32_e32 v224, v64, v228
	v_fmac_f32_e32 v225, v62, v230
	v_add_f32_e32 v232, 0, v232
	v_add_f32_e32 v224, v224, v225
	v_add_f32_e32 v232, v232, v224
	v_mul_f32_e32 v229, v113, v229
	ds_read_b128 v[224:227], v161
	v_fmac_f32_e32 v229, v112, v228
	v_mul_f32_e32 v228, v111, v231
	v_fmac_f32_e32 v228, v110, v230
	v_add_f32_e32 v228, v229, v228
	v_add_f32_e32 v233, v233, v228
	ds_read_b128 v[228:231], v162
	s_waitcnt lgkmcnt(1)
	v_mul_f32_e32 v234, v57, v225
	v_mul_f32_e32 v225, v109, v225
	v_fmac_f32_e32 v234, v56, v224
	v_fmac_f32_e32 v225, v108, v224
	v_mul_f32_e32 v224, v105, v227
	v_fmac_f32_e32 v224, v104, v226
	v_mul_f32_e32 v235, v55, v227
	v_add_f32_e32 v224, v225, v224
	v_fmac_f32_e32 v235, v54, v226
	v_add_f32_e32 v233, v233, v224
	s_waitcnt lgkmcnt(0)
	v_mul_f32_e32 v224, v61, v229
	v_mul_f32_e32 v225, v59, v231
	v_add_f32_e32 v234, v234, v235
	v_fmac_f32_e32 v224, v60, v228
	v_fmac_f32_e32 v225, v58, v230
	v_add_f32_e32 v232, v232, v234
	v_add_f32_e32 v224, v224, v225
	v_add_f32_e32 v232, v232, v224
	v_mul_f32_e32 v229, v107, v229
	ds_read_b128 v[224:227], v163
	v_fmac_f32_e32 v229, v106, v228
	v_mul_f32_e32 v228, v103, v231
	v_fmac_f32_e32 v228, v102, v230
	v_add_f32_e32 v228, v229, v228
	v_add_f32_e32 v233, v233, v228
	ds_read_b128 v[228:231], v164
	s_waitcnt lgkmcnt(1)
	v_mul_f32_e32 v234, v53, v225
	v_mul_f32_e32 v225, v101, v225
	v_fmac_f32_e32 v234, v52, v224
	v_fmac_f32_e32 v225, v100, v224
	v_mul_f32_e32 v224, v97, v227
	v_fmac_f32_e32 v224, v96, v226
	v_mul_f32_e32 v235, v51, v227
	v_add_f32_e32 v224, v225, v224
	v_fmac_f32_e32 v235, v50, v226
	v_add_f32_e32 v233, v233, v224
	s_waitcnt lgkmcnt(0)
	v_mul_f32_e32 v224, v49, v229
	v_mul_f32_e32 v225, v47, v231
	v_add_f32_e32 v234, v234, v235
	v_fmac_f32_e32 v224, v48, v228
	v_fmac_f32_e32 v225, v46, v230
	v_add_f32_e32 v232, v232, v234
	v_add_f32_e32 v224, v224, v225
	v_add_f32_e32 v232, v232, v224
	v_mul_f32_e32 v229, v99, v229
	ds_read_b128 v[224:227], v165
	v_fmac_f32_e32 v229, v98, v228
	v_mul_f32_e32 v228, v95, v231
	v_fmac_f32_e32 v228, v94, v230
	v_add_f32_e32 v228, v229, v228
	v_add_f32_e32 v233, v233, v228
	ds_read_b128 v[228:231], v166
	s_waitcnt lgkmcnt(1)
	v_mul_f32_e32 v234, v41, v225
	v_mul_f32_e32 v225, v91, v225
	v_fmac_f32_e32 v234, v40, v224
	v_fmac_f32_e32 v225, v90, v224
	v_mul_f32_e32 v224, v89, v227
	v_fmac_f32_e32 v224, v88, v226
	v_mul_f32_e32 v235, v39, v227
	v_add_f32_e32 v224, v225, v224
	v_fmac_f32_e32 v235, v38, v226
	v_add_f32_e32 v233, v233, v224
	s_waitcnt lgkmcnt(0)
	v_mul_f32_e32 v224, v37, v229
	v_mul_f32_e32 v225, v35, v231
	v_add_f32_e32 v234, v234, v235
	v_fmac_f32_e32 v224, v36, v228
	v_fmac_f32_e32 v225, v34, v230
	v_add_f32_e32 v232, v232, v234
	v_add_f32_e32 v224, v224, v225
	v_add_f32_e32 v232, v232, v224
	v_mul_f32_e32 v229, v93, v229
	ds_read_b128 v[224:227], v167
	v_fmac_f32_e32 v229, v92, v228
	v_mul_f32_e32 v228, v43, v231
	v_fmac_f32_e32 v228, v42, v230
	v_add_f32_e32 v228, v229, v228
	v_add_f32_e32 v233, v233, v228
	ds_read_b128 v[228:231], v168
	s_waitcnt lgkmcnt(1)
	v_mul_f32_e32 v234, v85, v225
	v_mul_f32_e32 v225, v117, v225
	v_fmac_f32_e32 v234, v84, v224
	v_fmac_f32_e32 v225, v116, v224
	v_mul_f32_e32 v224, v115, v227
	v_mul_f32_e32 v235, v83, v227
	v_fmac_f32_e32 v224, v114, v226
	v_fmac_f32_e32 v235, v82, v226
	v_add_f32_e32 v224, v225, v224
	v_add_f32_e32 v234, v234, v235
	v_add_f32_e32 v235, 0, v224
	s_waitcnt lgkmcnt(0)
	v_mul_f32_e32 v224, v65, v229
	v_mul_f32_e32 v225, v63, v231
	v_fmac_f32_e32 v224, v64, v228
	v_fmac_f32_e32 v225, v62, v230
	v_add_f32_e32 v234, 0, v234
	v_add_f32_e32 v224, v224, v225
	v_add_f32_e32 v234, v234, v224
	v_mul_f32_e32 v229, v113, v229
	ds_read_b128 v[224:227], v169
	v_fmac_f32_e32 v229, v112, v228
	v_mul_f32_e32 v228, v111, v231
	v_fmac_f32_e32 v228, v110, v230
	v_add_f32_e32 v228, v229, v228
	v_add_f32_e32 v235, v235, v228
	ds_read_b128 v[228:231], v170
	s_waitcnt lgkmcnt(1)
	v_mul_f32_e32 v236, v57, v225
	v_mul_f32_e32 v225, v109, v225
	v_fmac_f32_e32 v236, v56, v224
	v_fmac_f32_e32 v225, v108, v224
	v_mul_f32_e32 v224, v105, v227
	v_fmac_f32_e32 v224, v104, v226
	v_mul_f32_e32 v237, v55, v227
	v_add_f32_e32 v224, v225, v224
	v_fmac_f32_e32 v237, v54, v226
	v_add_f32_e32 v235, v235, v224
	s_waitcnt lgkmcnt(0)
	v_mul_f32_e32 v224, v61, v229
	v_mul_f32_e32 v225, v59, v231
	v_add_f32_e32 v236, v236, v237
	v_fmac_f32_e32 v224, v60, v228
	v_fmac_f32_e32 v225, v58, v230
	v_add_f32_e32 v234, v234, v236
	v_add_f32_e32 v224, v224, v225
	v_add_f32_e32 v234, v234, v224
	v_mul_f32_e32 v229, v107, v229
	ds_read_b128 v[224:227], v171
	v_fmac_f32_e32 v229, v106, v228
	v_mul_f32_e32 v228, v103, v231
	v_fmac_f32_e32 v228, v102, v230
	v_add_f32_e32 v228, v229, v228
	v_add_f32_e32 v235, v235, v228
	ds_read_b128 v[228:231], v172
	s_waitcnt lgkmcnt(1)
	v_mul_f32_e32 v236, v53, v225
	v_mul_f32_e32 v225, v101, v225
	v_fmac_f32_e32 v236, v52, v224
	v_fmac_f32_e32 v225, v100, v224
	v_mul_f32_e32 v224, v97, v227
	v_fmac_f32_e32 v224, v96, v226
	v_mul_f32_e32 v237, v51, v227
	v_add_f32_e32 v224, v225, v224
	v_fmac_f32_e32 v237, v50, v226
	v_add_f32_e32 v235, v235, v224
	s_waitcnt lgkmcnt(0)
	v_mul_f32_e32 v224, v49, v229
	v_mul_f32_e32 v225, v47, v231
	v_add_f32_e32 v236, v236, v237
	v_fmac_f32_e32 v224, v48, v228
	v_fmac_f32_e32 v225, v46, v230
	v_add_f32_e32 v234, v234, v236
	v_add_f32_e32 v224, v224, v225
	v_add_f32_e32 v234, v234, v224
	v_mul_f32_e32 v229, v99, v229
	ds_read_b128 v[224:227], v173
	v_fmac_f32_e32 v229, v98, v228
	v_mul_f32_e32 v228, v95, v231
	v_fmac_f32_e32 v228, v94, v230
	v_add_f32_e32 v228, v229, v228
	v_add_f32_e32 v235, v235, v228
	ds_read_b128 v[228:231], v174
	s_waitcnt lgkmcnt(1)
	v_mul_f32_e32 v236, v41, v225
	v_mul_f32_e32 v225, v91, v225
	v_fmac_f32_e32 v236, v40, v224
	v_fmac_f32_e32 v225, v90, v224
	v_mul_f32_e32 v224, v89, v227
	v_fmac_f32_e32 v224, v88, v226
	v_mul_f32_e32 v237, v39, v227
	v_add_f32_e32 v224, v225, v224
	v_fmac_f32_e32 v237, v38, v226
	v_add_f32_e32 v235, v235, v224
	s_waitcnt lgkmcnt(0)
	v_mul_f32_e32 v224, v37, v229
	v_mul_f32_e32 v225, v35, v231
	v_mul_f32_e32 v229, v93, v229
	v_add_f32_e32 v236, v236, v237
	v_fmac_f32_e32 v224, v36, v228
	v_fmac_f32_e32 v225, v34, v230
	v_fmac_f32_e32 v229, v92, v228
	v_mul_f32_e32 v228, v43, v231
	v_add_f32_e32 v234, v234, v236
	v_add_f32_e32 v224, v224, v225
	v_fmac_f32_e32 v228, v42, v230
	v_add_f32_e32 v234, v234, v224
	ds_read_b128 v[224:227], v175
	v_add_f32_e32 v228, v229, v228
	v_add_f32_e32 v235, v235, v228
	ds_read_b128 v[228:231], v176
	v_med3_f32 v196, v42, s17, v185
	s_waitcnt lgkmcnt(1)
	v_mul_f32_e32 v85, v85, v225
	v_mul_f32_e32 v83, v83, v227
	v_fmac_f32_e32 v85, v84, v224
	v_fmac_f32_e32 v83, v82, v226
	s_waitcnt lgkmcnt(0)
	v_mul_f32_e32 v65, v65, v229
	v_mul_f32_e32 v63, v63, v231
	v_add_f32_e32 v82, v85, v83
	v_fmac_f32_e32 v65, v64, v228
	v_fmac_f32_e32 v63, v62, v230
	v_add_f32_e32 v82, 0, v82
	v_mul_f32_e32 v84, v115, v227
	v_add_f32_e32 v62, v65, v63
	v_mul_f32_e32 v83, v117, v225
	v_fmac_f32_e32 v84, v114, v226
	v_add_f32_e32 v114, v82, v62
	ds_read_b128 v[62:65], v177
	v_fmac_f32_e32 v83, v116, v224
	v_add_f32_e32 v83, v83, v84
	v_mul_f32_e32 v82, v113, v229
	v_mul_f32_e32 v84, v111, v231
	v_fmac_f32_e32 v82, v112, v228
	v_fmac_f32_e32 v84, v110, v230
	v_add_f32_e32 v83, 0, v83
	v_add_f32_e32 v82, v82, v84
	v_add_f32_e32 v110, v83, v82
	ds_read_b128 v[82:85], v178
	s_waitcnt lgkmcnt(1)
	v_mul_f32_e32 v57, v57, v63
	v_mul_f32_e32 v55, v55, v65
	v_fmac_f32_e32 v57, v56, v62
	v_fmac_f32_e32 v55, v54, v64
	v_add_f32_e32 v54, v57, v55
	v_mul_f32_e32 v55, v109, v63
	v_mul_f32_e32 v56, v105, v65
	v_fmac_f32_e32 v55, v108, v62
	v_fmac_f32_e32 v56, v104, v64
	v_add_f32_e32 v55, v55, v56
	v_add_f32_e32 v62, v110, v55
	s_waitcnt lgkmcnt(0)
	v_mul_f32_e32 v55, v61, v83
	v_mul_f32_e32 v56, v59, v85
	v_fmac_f32_e32 v55, v60, v82
	v_fmac_f32_e32 v56, v58, v84
	v_mul_f32_e32 v58, v107, v83
	v_mul_f32_e32 v59, v103, v85
	v_add_f32_e32 v54, v114, v54
	v_add_f32_e32 v55, v55, v56
	v_fmac_f32_e32 v58, v106, v82
	v_fmac_f32_e32 v59, v102, v84
	v_add_f32_e32 v63, v54, v55
	ds_read_b128 v[54:57], v179
	v_add_f32_e32 v58, v58, v59
	v_add_f32_e32 v62, v62, v58
	ds_read_b128 v[58:61], v180
	s_waitcnt lgkmcnt(1)
	v_mul_f32_e32 v53, v53, v55
	v_mul_f32_e32 v51, v51, v57
	v_fmac_f32_e32 v53, v52, v54
	v_fmac_f32_e32 v51, v50, v56
	s_waitcnt lgkmcnt(0)
	v_mul_f32_e32 v49, v49, v59
	v_mul_f32_e32 v47, v47, v61
	v_add_f32_e32 v50, v53, v51
	v_mul_f32_e32 v51, v101, v55
	v_mul_f32_e32 v52, v97, v57
	v_fmac_f32_e32 v49, v48, v58
	v_fmac_f32_e32 v47, v46, v60
	v_add_f32_e32 v50, v63, v50
	v_fmac_f32_e32 v51, v100, v54
	v_fmac_f32_e32 v52, v96, v56
	v_add_f32_e32 v46, v49, v47
	v_add_f32_e32 v51, v51, v52
	v_add_f32_e32 v54, v50, v46
	v_mul_f32_e32 v50, v99, v59
	v_mul_f32_e32 v52, v95, v61
	v_fmac_f32_e32 v50, v98, v58
	v_fmac_f32_e32 v52, v94, v60
	v_add_f32_e32 v51, v62, v51
	v_add_f32_e32 v50, v50, v52
	ds_read_b128 v[46:49], v181
	v_add_f32_e32 v55, v51, v50
	ds_read_b128 v[50:53], v182
	s_waitcnt lgkmcnt(1)
	v_mul_f32_e32 v41, v41, v47
	v_mul_f32_e32 v39, v39, v49
	s_waitcnt lgkmcnt(0)
	v_mul_f32_e32 v37, v37, v51
	v_mul_f32_e32 v35, v35, v53
	v_fmac_f32_e32 v37, v36, v50
	v_fmac_f32_e32 v35, v34, v52
	v_fmac_f32_e32 v41, v40, v46
	v_fmac_f32_e32 v39, v38, v48
	v_add_f32_e32 v34, v37, v35
	v_mul_f32_e32 v35, v93, v51
	v_mul_f32_e32 v36, v43, v53
	v_add_f32_e32 v38, v41, v39
	v_fmac_f32_e32 v35, v92, v50
	v_fmac_f32_e32 v36, v42, v52
	v_add_f32_e32 v38, v54, v38
	v_mul_f32_e32 v39, v91, v47
	v_mul_f32_e32 v40, v89, v49
	v_add_f32_e32 v35, v35, v36
	v_cndmask_b32_e64 v36, v198, v214, s[0:1]
	v_fmac_f32_e32 v39, v90, v46
	v_fmac_f32_e32 v40, v88, v48
	v_add_f32_e32 v34, v38, v34
	ds_bpermute_b32 v36, v191, v36
	v_cndmask_b32_e64 v38, v200, v216, s[0:1]
	v_add_f32_e32 v39, v39, v40
	ds_bpermute_b32 v38, v191, v38
	v_cndmask_b32_e64 v40, v202, v219, s[0:1]
	ds_bpermute_b32 v40, v191, v40
	v_cndmask_b32_e64 v37, v214, v198, s[0:1]
	s_waitcnt lgkmcnt(2)
	v_add_f32_e32 v36, v37, v36
	v_cndmask_b32_e64 v37, v216, v200, s[0:1]
	s_waitcnt lgkmcnt(1)
	v_add_f32_e32 v37, v37, v38
	v_cndmask_b32_e64 v38, v219, v202, s[0:1]
	s_waitcnt lgkmcnt(0)
	v_add_f32_e32 v38, v38, v40
	v_cndmask_b32_e64 v40, v204, v221, s[0:1]
	ds_bpermute_b32 v40, v191, v40
	v_cndmask_b32_e64 v42, v206, v223, s[0:1]
	ds_bpermute_b32 v42, v191, v42
	v_cndmask_b32_e64 v46, v208, v232, s[0:1]
	ds_bpermute_b32 v46, v191, v46
	v_cndmask_b32_e64 v41, v221, v204, s[0:1]
	s_waitcnt lgkmcnt(2)
	v_add_f32_e32 v40, v41, v40
	v_cndmask_b32_e64 v41, v223, v206, s[0:1]
	s_waitcnt lgkmcnt(1)
	v_add_f32_e32 v41, v41, v42
	v_cndmask_b32_e64 v42, v232, v208, s[0:1]
	s_waitcnt lgkmcnt(0)
	v_add_f32_e32 v42, v42, v46
	v_cndmask_b32_e64 v46, v210, v234, s[0:1]
	ds_bpermute_b32 v46, v191, v46
	v_cndmask_b32_e64 v48, v212, v34, s[0:1]
	ds_bpermute_b32 v48, v191, v48
	v_cndmask_b32_e64 v47, v234, v210, s[0:1]
	v_cndmask_b32_e64 v34, v34, v212, s[0:1]
	s_waitcnt lgkmcnt(1)
	v_add_f32_e32 v46, v47, v46
	v_cndmask_b32_e64 v49, v36, v41, s[4:5]
	s_waitcnt lgkmcnt(0)
	v_add_f32_e32 v34, v34, v48
	v_cndmask_b32_e64 v36, v41, v36, s[4:5]
	v_cndmask_b32_e64 v41, v37, v42, s[4:5]
	v_cndmask_b32_e64 v37, v42, v37, s[4:5]
	v_cndmask_b32_e64 v42, v38, v46, s[4:5]
	ds_bpermute_b32 v49, v190, v49
	ds_bpermute_b32 v42, v190, v42
	v_cndmask_b32_e64 v47, v40, v34, s[4:5]
	ds_bpermute_b32 v41, v190, v41
	ds_bpermute_b32 v47, v190, v47
	v_cndmask_b32_e64 v38, v46, v38, s[4:5]
	s_waitcnt lgkmcnt(3)
	v_add_f32_e32 v36, v36, v49
	s_waitcnt lgkmcnt(2)
	v_add_f32_e32 v38, v38, v42
	v_cndmask_b32_e64 v34, v34, v40, s[4:5]
	s_waitcnt lgkmcnt(1)
	v_add_f32_e32 v37, v37, v41
	s_waitcnt lgkmcnt(0)
	v_add_f32_e32 v34, v34, v47
	v_cndmask_b32_e64 v40, v36, v38, s[6:7]
	ds_bpermute_b32 v40, v189, v40
	v_cndmask_b32_e64 v41, v37, v34, s[6:7]
	ds_bpermute_b32 v41, v189, v41
	v_cndmask_b32_e64 v36, v38, v36, s[6:7]
	v_cndmask_b32_e64 v38, v197, v213, s[0:1]
	s_waitcnt lgkmcnt(1)
	v_add_f32_e32 v36, v36, v40
	v_cndmask_b32_e64 v34, v34, v37, s[6:7]
	ds_bpermute_b32 v38, v191, v38
	v_cndmask_b32_e64 v40, v199, v215, s[0:1]
	s_waitcnt lgkmcnt(1)
	v_add_f32_e32 v34, v34, v41
	ds_bpermute_b32 v40, v191, v40
	v_cndmask_b32_e64 v41, v201, v217, s[0:1]
	ds_bpermute_b32 v41, v191, v41
	v_add_f32_e32 v39, v55, v39
	v_add_f32_e32 v35, v39, v35
	v_cndmask_b32_e64 v39, v213, v197, s[0:1]
	s_waitcnt lgkmcnt(2)
	v_add_f32_e32 v38, v39, v38
	v_cndmask_b32_e64 v39, v215, v199, s[0:1]
	s_waitcnt lgkmcnt(1)
	v_add_f32_e32 v39, v39, v40
	v_cndmask_b32_e64 v40, v217, v201, s[0:1]
	s_waitcnt lgkmcnt(0)
	v_add_f32_e32 v40, v40, v41
	v_cndmask_b32_e64 v41, v203, v220, s[0:1]
	ds_bpermute_b32 v41, v191, v41
	v_cndmask_b32_e64 v46, v205, v222, s[0:1]
	ds_bpermute_b32 v46, v191, v46
	v_cndmask_b32_e64 v47, v207, v233, s[0:1]
	ds_bpermute_b32 v47, v191, v47
	v_cndmask_b32_e64 v42, v220, v203, s[0:1]
	s_waitcnt lgkmcnt(2)
	v_add_f32_e32 v41, v42, v41
	v_cndmask_b32_e64 v42, v222, v205, s[0:1]
	s_waitcnt lgkmcnt(1)
	v_add_f32_e32 v42, v42, v46
	v_cndmask_b32_e64 v46, v233, v207, s[0:1]
	s_waitcnt lgkmcnt(0)
	v_add_f32_e32 v46, v46, v47
	v_cndmask_b32_e64 v47, v209, v235, s[0:1]
	v_cndmask_b32_e64 v49, v211, v35, s[0:1]
	ds_bpermute_b32 v47, v191, v47
	ds_bpermute_b32 v49, v191, v49
	v_cndmask_b32_e64 v48, v235, v209, s[0:1]
	v_cndmask_b32_e64 v35, v35, v211, s[0:1]
	v_cndmask_b32_e64 v50, v38, v42, s[4:5]
	s_waitcnt lgkmcnt(1)
	v_add_f32_e32 v47, v48, v47
	s_waitcnt lgkmcnt(0)
	v_add_f32_e32 v35, v35, v49
	v_cndmask_b32_e64 v38, v42, v38, s[4:5]
	v_cndmask_b32_e64 v42, v39, v46, s[4:5]
	v_cndmask_b32_e64 v39, v46, v39, s[4:5]
	v_cndmask_b32_e64 v46, v40, v47, s[4:5]
	v_cndmask_b32_e64 v48, v41, v35, s[4:5]
	ds_bpermute_b32 v50, v190, v50
	ds_bpermute_b32 v42, v190, v42
	ds_bpermute_b32 v46, v190, v46
	ds_bpermute_b32 v48, v190, v48
	v_cndmask_b32_e64 v40, v47, v40, s[4:5]
	v_cndmask_b32_e64 v35, v35, v41, s[4:5]
	s_waitcnt lgkmcnt(3)
	v_add_f32_e32 v38, v38, v50
	s_waitcnt lgkmcnt(2)
	v_add_f32_e32 v39, v39, v42
	s_waitcnt lgkmcnt(1)
	v_add_f32_e32 v40, v40, v46
	s_waitcnt lgkmcnt(0)
	v_add_f32_e32 v35, v35, v48
	v_cndmask_b32_e64 v41, v38, v40, s[6:7]
	v_cndmask_b32_e64 v42, v39, v35, s[6:7]
	ds_bpermute_b32 v41, v189, v41
	ds_bpermute_b32 v42, v189, v42
	v_cndmask_b32_e64 v38, v40, v38, s[6:7]
	v_cndmask_b32_e64 v35, v35, v39, s[6:7]
	v_cndmask_b32_e64 v37, v36, v34, s[8:9]
	s_waitcnt lgkmcnt(1)
	v_add_f32_e32 v38, v38, v41
	s_waitcnt lgkmcnt(0)
	v_add_f32_e32 v35, v35, v42
	v_cndmask_b32_e64 v39, v38, v35, s[8:9]
	ds_bpermute_b32 v37, v188, v37
	ds_bpermute_b32 v39, v188, v39
	v_cndmask_b32_e64 v34, v34, v36, s[8:9]
	v_cndmask_b32_e64 v35, v35, v38, s[8:9]
	s_waitcnt lgkmcnt(1)
	v_add_f32_e32 v34, v34, v37
	s_waitcnt lgkmcnt(0)
	v_add_f32_e32 v35, v35, v39
	ds_bpermute_b32 v36, v187, v34
	ds_bpermute_b32 v38, v187, v35
	v_med3_f32 v37, v43, s17, v185
	v_cvt_pk_fp8_f32 v195, v196, v37 op_sel:[0,0,1]
	global_store_dword v[44:45], v192, off offset:1536
	global_store_dword v[86:87], v193, off offset:1536
	global_store_dword v[44:45], v194, off offset:1792
	global_store_dword v[86:87], v195, off offset:1792
	s_waitcnt lgkmcnt(1)
	v_add_f32_e32 v36, v34, v36
	s_waitcnt lgkmcnt(0)
	v_add_f32_e32 v34, v35, v38
	ds_bpermute_b32 v37, v186, v36
	ds_bpermute_b32 v35, v186, v34
	s_and_saveexec_b64 s[50:51], s[10:11]
	s_cbranch_execz .LBB0_190
	s_waitcnt lgkmcnt(1)
	v_add_f32_e32 v36, v36, v37
	v_add_f32_e32 v38, v1, v36
	v_lshl_add_u64 v[36:37], s[28:29], 0, v[74:75]
	s_andn2_b64 vcc, exec, s[44:45]
	global_store_dword v[36:37], v38, off
	s_cbranch_vccnz .LBB0_190
	s_waitcnt lgkmcnt(0)
	v_add_f32_e32 v34, v34, v35
	s_lshl_b64 s[26:27], s[40:41], 6
	v_add_f32_e32 v36, v1, v34
	v_lshl_add_u64 v[34:35], v[66:67], 0, s[26:27]
	global_store_dword v[34:35], v36, off
	s_branch .LBB0_190

.LBB0_275:
	s_mov_b64 s[16:17], 0x8000
	s_add_i32 m0, s33, 0x18000
	v_lshl_add_u64 v[8:9], v[2:3], 0, s[16:17]
	s_mov_b64 s[18:19], 0xa000
	s_waitcnt vmcnt(2)
	s_barrier
	global_load_lds_dwordx4 v[8:9], off
	v_lshl_add_u64 v[8:9], v[2:3], 0, s[18:19]
	s_add_i32 m0, s33, 0x1a000
	s_mov_b64 s[20:21], 0x80
	s_add_i32 s86, s33, 0x8000
	global_load_lds_dwordx4 v[8:9], off
	v_lshl_add_u64 v[4:5], v[4:5], 0, s[20:21]
	s_mov_b32 m0, s86
	s_add_i32 s87, s33, 0xa000
	global_load_lds_dwordx4 v[4:5], off
	v_lshl_add_u64 v[4:5], v[6:7], 0, s[20:21]
	s_mov_b32 m0, s87
	s_mov_b64 s[22:23], 0xc000
	global_load_lds_dwordx4 v[4:5], off
	s_add_i32 m0, s33, 0x1c000
	v_lshl_add_u64 v[4:5], v[2:3], 0, s[22:23]
	s_mov_b64 s[24:25], 0xe000
	global_load_lds_dwordx4 v[4:5], off
	v_lshl_add_u64 v[2:3], v[2:3], 0, s[24:25]
	s_add_i32 m0, s33, 0x1e000
	s_sext_i32_i8 s2, s0
	global_load_lds_dwordx4 v[2:3], off
	v_lshlrev_b32_e32 v3, 2, v158
	s_lshl_b32 s0, s27, 13
	v_lshl_or_b32 v2, v158, 6, v160
	v_and_b32_e32 v3, 32, v3
	v_bitop3_b32 v2, v2, s0, v3 bitop3:0xde
	v_lshlrev_b32_e32 v3, 8, v0
	v_and_b32_e32 v3, 0x18000, v3
	v_lshlrev_b32_e32 v4, 11, v155
	s_lshl_b32 s0, s26, 5
	v_or3_b32 v3, v1, v3, v4
	s_and_b32 s0, s0, 0x60
	v_add_u32_e32 v168, v3, v154
	v_lshlrev_b32_e32 v3, 4, v156
	s_waitcnt vmcnt(6)
	s_cmpk_lt_u32 s1, 0x100
	v_and_b32_e32 v3, 0x38000, v3
	v_lshl_or_b32 v183, s0, 7, v159
	s_cselect_b64 s[40:41], -1, 0
	v_or3_b32 v1, v1, v3, v4
	s_add_i32 s88, 0, 0x10000
	s_add_i32 s89, 0, 0x14000
	v_lshl_or_b32 v182, s27, 6, v158
	v_or_b32_e32 v184, s0, v157
	v_mov_b32_e32 v169, v165
	v_add_u32_e32 v170, v1, v154
	v_mov_b32_e32 v171, v165
	v_mov_b64_e32 v[172:173], 0x400
	v_mov_b64_e32 v[174:175], 0x3ff
	v_add_u32_e32 v1, s88, v183
	v_add_u32_e32 v185, s89, v183
	v_add_u32_e32 v186, 0, v2
	v_mov_b32_e32 v187, 0x79797979
	v_mov_b32_e32 v188, 0x7f7f7f7f
	s_barrier
	v_mov_b32_e32 v251, 0
	global_load_dword v250, v251, s[28:29]
	global_load_dword v250, v251, s[28:29]
	global_load_dword v250, v251, s[28:29]
	global_load_dword v250, v251, s[28:29]
	global_load_dword v250, v251, s[28:29]
	global_load_dword v250, v251, s[28:29]
	global_load_dword v250, v251, s[28:29]
	global_load_dword v250, v251, s[28:29]
	global_load_dword v250, v251, s[28:29]
	global_load_dword v250, v251, s[28:29]
	global_load_dword v250, v251, s[28:29]
	global_load_dword v250, v251, s[28:29]
	global_load_dword v250, v251, s[28:29]
	global_load_dword v250, v251, s[28:29]
	global_load_dword v250, v251, s[28:29]
	global_load_dword v250, v251, s[28:29]
	s_branch .LBB0_278

.LBB0_284:
	s_ashr_i32 s51, s50, 31
	s_lshl_b64 s[26:27], s[50:51], 19
	v_readlane_b32 s54, v254, 58
	v_readlane_b32 s55, v254, 59
	s_add_u32 s54, s54, s26
	s_addc_u32 s55, s55, s27
	s_and_b64 s[26:27], s[0:1], exec
	s_cselect_b32 s51, s55, s73
	s_cselect_b32 s90, s54, s72
	s_ashr_i32 s45, s44, 31
	s_lshl_b64 s[26:27], s[44:45], 19
	s_add_u32 s56, s81, s26
	s_addc_u32 s57, s82, s27
	s_and_b64 s[26:27], s[0:1], exec
	s_cselect_b32 s45, s57, s71
	s_cselect_b32 s91, s56, s70
	s_add_u32 s92, s70, 0x10000
	s_addc_u32 s93, s71, 0
	s_add_u32 s70, s72, 0x40080
	s_addc_u32 s71, s73, 0
	s_mov_b32 s94, -2
	ds_read_b128 v[26:29], v1
	ds_read_b128 v[30:33], v1 offset:1024
	ds_read_b128 v[18:21], v1 offset:2048
	ds_read_b128 v[22:25], v1 offset:3072
	ds_read_b128 v[10:13], v185
	ds_read_b128 v[14:17], v185 offset:1024
	ds_read_b128 v[2:5], v185 offset:2048
	ds_read_b128 v[6:9], v185 offset:3072
	s_add_u32 s26, s70, 0xfffc0080
	s_addc_u32 s27, s71, -1
	s_cmp_eq_u32 s94, 12
	s_cselect_b32 s73, s51, s27
	s_cselect_b32 s72, s90, s26
	s_cselect_b32 s75, s45, s93
	s_cselect_b32 s74, s91, s92
	v_lshl_add_u64 v[176:177], s[70:71], 0, v[168:169]
	s_add_i32 m0, s33, 0xc000
	ds_read_b128 v[190:193], v186
	ds_read_b128 v[194:197], v186 offset:1024
	ds_read_b128 v[198:201], v186 offset:2048
	ds_read_b128 v[202:205], v186 offset:3072
	ds_read_b128 v[206:209], v186 offset:4096
	ds_read_b128 v[210:213], v186 offset:5120
	ds_read_b128 v[220:223], v186 offset:6144
	ds_read_b128 v[224:227], v186 offset:7168
	global_load_lds_dwordx4 v[176:177], off
	v_lshl_add_u64 v[176:177], s[70:71], 0, v[170:171]
	s_add_i32 m0, s33, 0xe000
	s_nop 0
	global_load_lds_dwordx4 v[176:177], off
	s_waitcnt vmcnt(24)
	s_waitcnt lgkmcnt(0)
	s_barrier
	s_waitcnt lgkmcnt(0)
	v_mfma_scale_f32_16x16x128_f8f6f4 v[158:161], v[26:33], v[190:197], 0, v187, v188 op_sel_hi:[0,0,0]
	v_mfma_scale_f32_16x16x128_f8f6f4 v[154:157], v[18:25], v[190:197], 0, v187, v188 op_sel_hi:[0,0,0]
	v_mfma_scale_f32_16x16x128_f8f6f4 v[150:153], v[26:33], v[198:205], 0, v187, v188 op_sel_hi:[0,0,0]
	v_mfma_scale_f32_16x16x128_f8f6f4 v[142:145], v[18:25], v[198:205], 0, v187, v188 op_sel_hi:[0,0,0]
	v_mfma_scale_f32_16x16x128_f8f6f4 v[134:137], v[26:33], v[206:213], 0, v187, v188 op_sel_hi:[0,0,0]
	v_mfma_scale_f32_16x16x128_f8f6f4 v[126:129], v[18:25], v[206:213], 0, v187, v188 op_sel_hi:[0,0,0]
	v_mfma_scale_f32_16x16x128_f8f6f4 v[118:121], v[26:33], v[220:227], 0, v187, v188 op_sel_hi:[0,0,0]
	v_mfma_scale_f32_16x16x128_f8f6f4 v[110:113], v[18:25], v[220:227], 0, v187, v188 op_sel_hi:[0,0,0]
	v_mfma_scale_f32_16x16x128_f8f6f4 v[146:149], v[10:17], v[190:197], 0, v187, v188 op_sel_hi:[0,0,0]
	v_mfma_scale_f32_16x16x128_f8f6f4 v[138:141], v[2:9], v[190:197], 0, v187, v188 op_sel_hi:[0,0,0]
	v_mfma_scale_f32_16x16x128_f8f6f4 v[130:133], v[10:17], v[198:205], 0, v187, v188 op_sel_hi:[0,0,0]
	v_mfma_scale_f32_16x16x128_f8f6f4 v[122:125], v[2:9], v[198:205], 0, v187, v188 op_sel_hi:[0,0,0]
	v_mfma_scale_f32_16x16x128_f8f6f4 v[114:117], v[10:17], v[206:213], 0, v187, v188 op_sel_hi:[0,0,0]
	v_mfma_scale_f32_16x16x128_f8f6f4 v[106:109], v[2:9], v[206:213], 0, v187, v188 op_sel_hi:[0,0,0]
	v_mfma_scale_f32_16x16x128_f8f6f4 v[102:105], v[10:17], v[220:227], 0, v187, v188 op_sel_hi:[0,0,0]
	v_mfma_scale_f32_16x16x128_f8f6f4 v[98:101], v[2:9], v[220:227], 0, v187, v188 op_sel_hi:[0,0,0]
	s_barrier
	s_add_i32 s26, s88, s80
	v_lshl_add_u64 v[176:177], s[74:75], 0, v[162:163]
	s_mov_b32 m0, s26
	ds_read_b128 v[190:193], v186 offset:16384
	ds_read_b128 v[194:197], v186 offset:17408
	ds_read_b128 v[198:201], v186 offset:18432
	ds_read_b128 v[202:205], v186 offset:19456
	ds_read_b128 v[206:209], v186 offset:20480
	ds_read_b128 v[210:213], v186 offset:21504
	ds_read_b128 v[220:223], v186 offset:22528
	ds_read_b128 v[224:227], v186 offset:23552
	global_load_lds_dwordx4 v[176:177], off
	v_lshl_add_u64 v[178:179], v[176:177], 0, s[8:9]
	s_add_i32 m0, s26, 0x2000
	s_add_i32 s26, s89, s80
	global_load_lds_dwordx4 v[178:179], off
	v_lshl_add_u64 v[178:179], v[176:177], 0, s[10:11]
	s_mov_b32 m0, s26
	v_lshl_add_u64 v[180:181], s[72:73], 0, v[166:167]
	global_load_lds_dwordx4 v[178:179], off
	v_lshl_add_u64 v[178:179], v[176:177], 0, s[12:13]
	s_add_i32 m0, s26, 0x2000
	s_nop 0
	global_load_lds_dwordx4 v[178:179], off
	v_lshl_add_u64 v[178:179], s[72:73], 0, v[164:165]
	s_mov_b32 m0, s33
	s_nop 0
	global_load_lds_dwordx4 v[178:179], off
	s_mov_b32 m0, s69
	s_nop 0
	global_load_lds_dwordx4 v[180:181], off
	s_waitcnt vmcnt(24)
	s_waitcnt lgkmcnt(0)
	s_barrier
	s_waitcnt lgkmcnt(0)
	v_mfma_scale_f32_16x16x128_f8f6f4 v[94:97], v[26:33], v[190:197], 0, v187, v188 op_sel_hi:[0,0,0]
	v_mfma_scale_f32_16x16x128_f8f6f4 v[90:93], v[18:25], v[190:197], 0, v187, v188 op_sel_hi:[0,0,0]
	v_mfma_scale_f32_16x16x128_f8f6f4 v[86:89], v[26:33], v[198:205], 0, v187, v188 op_sel_hi:[0,0,0]
	v_mfma_scale_f32_16x16x128_f8f6f4 v[78:81], v[18:25], v[198:205], 0, v187, v188 op_sel_hi:[0,0,0]
	v_mfma_scale_f32_16x16x128_f8f6f4 v[70:73], v[26:33], v[206:213], 0, v187, v188 op_sel_hi:[0,0,0]
	v_mfma_scale_f32_16x16x128_f8f6f4 v[62:65], v[18:25], v[206:213], 0, v187, v188 op_sel_hi:[0,0,0]
	v_mfma_scale_f32_16x16x128_f8f6f4 v[54:57], v[26:33], v[220:227], 0, v187, v188 op_sel_hi:[0,0,0]
	v_mfma_scale_f32_16x16x128_f8f6f4 v[46:49], v[18:25], v[220:227], 0, v187, v188 op_sel_hi:[0,0,0]
	v_mfma_scale_f32_16x16x128_f8f6f4 v[82:85], v[10:17], v[190:197], 0, v187, v188 op_sel_hi:[0,0,0]
	v_mfma_scale_f32_16x16x128_f8f6f4 v[74:77], v[2:9], v[190:197], 0, v187, v188 op_sel_hi:[0,0,0]
	v_mfma_scale_f32_16x16x128_f8f6f4 v[66:69], v[10:17], v[198:205], 0, v187, v188 op_sel_hi:[0,0,0]
	v_mfma_scale_f32_16x16x128_f8f6f4 v[58:61], v[2:9], v[198:205], 0, v187, v188 op_sel_hi:[0,0,0]
	v_mfma_scale_f32_16x16x128_f8f6f4 v[50:53], v[10:17], v[206:213], 0, v187, v188 op_sel_hi:[0,0,0]
	v_mfma_scale_f32_16x16x128_f8f6f4 v[42:45], v[2:9], v[206:213], 0, v187, v188 op_sel_hi:[0,0,0]
	v_mfma_scale_f32_16x16x128_f8f6f4 v[38:41], v[10:17], v[220:227], 0, v187, v188 op_sel_hi:[0,0,0]
	v_mfma_scale_f32_16x16x128_f8f6f4 v[34:37], v[2:9], v[220:227], 0, v187, v188 op_sel_hi:[0,0,0]
	s_barrier
	s_add_i32 s74, 0, 0x18000
	s_add_i32 s75, 0, 0x1c000
	v_add_u32_e32 v14, s74, v183
	v_add_u32_e32 v30, s75, v183
	ds_read_b128 v[2:5], v14
	ds_read_b128 v[6:9], v14 offset:1024
	ds_read_b128 v[10:13], v14 offset:2048
	ds_read_b128 v[14:17], v14 offset:3072
	ds_read_b128 v[18:21], v30
	ds_read_b128 v[22:25], v30 offset:1024
	ds_read_b128 v[26:29], v30 offset:2048
	ds_read_b128 v[30:33], v30 offset:3072
	s_add_u32 s26, s72, 0x40000
	s_addc_u32 s27, s73, 0
	s_mov_b32 m0, s83
	v_lshl_add_u64 v[214:215], s[26:27], 0, v[164:165]
	ds_read_b128 v[190:193], v186 offset:32768
	ds_read_b128 v[194:197], v186 offset:33792
	ds_read_b128 v[198:201], v186 offset:34816
	ds_read_b128 v[202:205], v186 offset:35840
	ds_read_b128 v[206:209], v186 offset:36864
	ds_read_b128 v[210:213], v186 offset:37888
	ds_read_b128 v[220:223], v186 offset:38912
	ds_read_b128 v[224:227], v186 offset:39936
	global_load_lds_dwordx4 v[214:215], off
	v_lshl_add_u64 v[214:215], s[26:27], 0, v[166:167]
	s_mov_b32 m0, s84
	s_nop 0
	global_load_lds_dwordx4 v[214:215], off
	s_waitcnt vmcnt(8)
	s_waitcnt lgkmcnt(0)
	s_barrier
	s_waitcnt lgkmcnt(0)
	v_mfma_scale_f32_16x16x128_f8f6f4 v[158:161], v[2:9], v[190:197], v[158:161], v187, v188 op_sel_hi:[0,0,0]
	v_mfma_scale_f32_16x16x128_f8f6f4 v[154:157], v[10:17], v[190:197], v[154:157], v187, v188 op_sel_hi:[0,0,0]
	v_mfma_scale_f32_16x16x128_f8f6f4 v[150:153], v[2:9], v[198:205], v[150:153], v187, v188 op_sel_hi:[0,0,0]
	v_mfma_scale_f32_16x16x128_f8f6f4 v[142:145], v[10:17], v[198:205], v[142:145], v187, v188 op_sel_hi:[0,0,0]
	v_mfma_scale_f32_16x16x128_f8f6f4 v[134:137], v[2:9], v[206:213], v[134:137], v187, v188 op_sel_hi:[0,0,0]
	v_mfma_scale_f32_16x16x128_f8f6f4 v[126:129], v[10:17], v[206:213], v[126:129], v187, v188 op_sel_hi:[0,0,0]
	v_mfma_scale_f32_16x16x128_f8f6f4 v[118:121], v[2:9], v[220:227], v[118:121], v187, v188 op_sel_hi:[0,0,0]
	v_mfma_scale_f32_16x16x128_f8f6f4 v[110:113], v[10:17], v[220:227], v[110:113], v187, v188 op_sel_hi:[0,0,0]
	v_mfma_scale_f32_16x16x128_f8f6f4 v[146:149], v[18:25], v[190:197], v[146:149], v187, v188 op_sel_hi:[0,0,0]
	v_mfma_scale_f32_16x16x128_f8f6f4 v[138:141], v[26:33], v[190:197], v[138:141], v187, v188 op_sel_hi:[0,0,0]
	v_mfma_scale_f32_16x16x128_f8f6f4 v[130:133], v[18:25], v[198:205], v[130:133], v187, v188 op_sel_hi:[0,0,0]
	v_mfma_scale_f32_16x16x128_f8f6f4 v[122:125], v[26:33], v[198:205], v[122:125], v187, v188 op_sel_hi:[0,0,0]
	v_mfma_scale_f32_16x16x128_f8f6f4 v[114:117], v[18:25], v[206:213], v[114:117], v187, v188 op_sel_hi:[0,0,0]
	v_mfma_scale_f32_16x16x128_f8f6f4 v[106:109], v[26:33], v[206:213], v[106:109], v187, v188 op_sel_hi:[0,0,0]
	v_mfma_scale_f32_16x16x128_f8f6f4 v[102:105], v[18:25], v[220:227], v[102:105], v187, v188 op_sel_hi:[0,0,0]
	v_mfma_scale_f32_16x16x128_f8f6f4 v[98:101], v[26:33], v[220:227], v[98:101], v187, v188 op_sel_hi:[0,0,0]
	s_barrier
	s_add_i32 s26, s74, s80
	v_lshl_add_u64 v[214:215], v[176:177], 0, s[16:17]
	s_mov_b32 m0, s26
	ds_read_b128 v[190:193], v186 offset:49152
	ds_read_b128 v[194:197], v186 offset:50176
	ds_read_b128 v[198:201], v186 offset:51200
	ds_read_b128 v[202:205], v186 offset:52224
	ds_read_b128 v[206:209], v186 offset:53248
	ds_read_b128 v[210:213], v186 offset:54272
	ds_read_b128 v[220:223], v186 offset:55296
	ds_read_b128 v[224:227], v186 offset:56320
	global_load_lds_dwordx4 v[214:215], off
	v_lshl_add_u64 v[214:215], v[176:177], 0, s[18:19]
	s_add_i32 m0, s26, 0x2000
	s_add_i32 s26, s75, s80
	global_load_lds_dwordx4 v[214:215], off
	v_lshl_add_u64 v[214:215], v[176:177], 0, s[22:23]
	s_mov_b32 m0, s26
	v_lshl_add_u64 v[176:177], v[176:177], 0, s[24:25]
	global_load_lds_dwordx4 v[214:215], off
	s_add_i32 m0, s26, 0x2000
	s_nop 0
	global_load_lds_dwordx4 v[176:177], off
	v_lshl_add_u64 v[176:177], v[178:179], 0, s[20:21]
	s_mov_b32 m0, s86
	s_nop 0
	global_load_lds_dwordx4 v[176:177], off
	v_lshl_add_u64 v[176:177], v[180:181], 0, s[20:21]
	s_mov_b32 m0, s87
	s_nop 0
	global_load_lds_dwordx4 v[176:177], off
	s_waitcnt vmcnt(8)
	s_waitcnt lgkmcnt(0)
	s_barrier
	s_waitcnt lgkmcnt(0)
	v_mfma_scale_f32_16x16x128_f8f6f4 v[94:97], v[2:9], v[190:197], v[94:97], v187, v188 op_sel_hi:[0,0,0]
	v_mfma_scale_f32_16x16x128_f8f6f4 v[90:93], v[10:17], v[190:197], v[90:93], v187, v188 op_sel_hi:[0,0,0]
	v_mfma_scale_f32_16x16x128_f8f6f4 v[86:89], v[2:9], v[198:205], v[86:89], v187, v188 op_sel_hi:[0,0,0]
	v_mfma_scale_f32_16x16x128_f8f6f4 v[78:81], v[10:17], v[198:205], v[78:81], v187, v188 op_sel_hi:[0,0,0]
	v_mfma_scale_f32_16x16x128_f8f6f4 v[70:73], v[2:9], v[206:213], v[70:73], v187, v188 op_sel_hi:[0,0,0]
	v_mfma_scale_f32_16x16x128_f8f6f4 v[62:65], v[10:17], v[206:213], v[62:65], v187, v188 op_sel_hi:[0,0,0]
	v_mfma_scale_f32_16x16x128_f8f6f4 v[54:57], v[2:9], v[220:227], v[54:57], v187, v188 op_sel_hi:[0,0,0]
	v_mfma_scale_f32_16x16x128_f8f6f4 v[46:49], v[10:17], v[220:227], v[46:49], v187, v188 op_sel_hi:[0,0,0]
	v_mfma_scale_f32_16x16x128_f8f6f4 v[82:85], v[18:25], v[190:197], v[82:85], v187, v188 op_sel_hi:[0,0,0]
	v_mfma_scale_f32_16x16x128_f8f6f4 v[74:77], v[26:33], v[190:197], v[74:77], v187, v188 op_sel_hi:[0,0,0]
	v_mfma_scale_f32_16x16x128_f8f6f4 v[66:69], v[18:25], v[198:205], v[66:69], v187, v188 op_sel_hi:[0,0,0]
	v_mfma_scale_f32_16x16x128_f8f6f4 v[58:61], v[26:33], v[198:205], v[58:61], v187, v188 op_sel_hi:[0,0,0]
	v_mfma_scale_f32_16x16x128_f8f6f4 v[50:53], v[18:25], v[206:213], v[50:53], v187, v188 op_sel_hi:[0,0,0]
	v_mfma_scale_f32_16x16x128_f8f6f4 v[42:45], v[26:33], v[206:213], v[42:45], v187, v188 op_sel_hi:[0,0,0]
	v_mfma_scale_f32_16x16x128_f8f6f4 v[38:41], v[18:25], v[220:227], v[38:41], v187, v188 op_sel_hi:[0,0,0]
	v_mfma_scale_f32_16x16x128_f8f6f4 v[34:37], v[26:33], v[220:227], v[34:37], v187, v188 op_sel_hi:[0,0,0]
	s_barrier
	s_add_i32 s94, s94, 2
	s_add_u32 s92, s92, 0x10000
	s_addc_u32 s93, s93, 0
	s_add_u32 s70, s70, 0x100
	s_addc_u32 s71, s71, 0
	s_cmp_gt_u32 s94, 13

.LBB0_777:
	s_add_u32 s14, s28, 0x31400000
	s_mov_b64 s[16:17], 0x8000
	s_addc_u32 s15, s29, 0
	s_add_i32 m0, s61, 0x18000
	v_lshl_add_u64 v[12:13], v[2:3], 0, s[16:17]
	s_mov_b64 s[18:19], 0xa000
	s_waitcnt vmcnt(2)
	s_barrier
	global_load_lds_dwordx4 v[12:13], off
	v_lshl_add_u64 v[12:13], v[2:3], 0, s[18:19]
	s_add_i32 m0, s61, 0x1a000
	s_mov_b64 s[20:21], 0x80
	s_add_i32 s70, s61, 0x8000
	global_load_lds_dwordx4 v[12:13], off
	v_lshl_add_u64 v[4:5], v[4:5], 0, s[20:21]
	s_mov_b32 m0, s70
	s_add_i32 s71, s61, 0xa000
	global_load_lds_dwordx4 v[4:5], off
	v_lshl_add_u64 v[4:5], v[6:7], 0, s[20:21]
	s_mov_b32 m0, s71
	s_mov_b64 s[22:23], 0xc000
	global_load_lds_dwordx4 v[4:5], off
	s_add_i32 m0, s61, 0x1c000
	v_lshl_add_u64 v[4:5], v[2:3], 0, s[22:23]
	s_mov_b64 s[24:25], 0xe000
	global_load_lds_dwordx4 v[4:5], off
	v_lshl_add_u64 v[2:3], v[2:3], 0, s[24:25]
	s_add_i32 m0, s61, 0x1e000
	s_sext_i32_i16 s2, s0
	global_load_lds_dwordx4 v[2:3], off
	v_lshrrev_b32_e32 v3, 1, v0
	v_and_b32_e32 v3, 24, v3
	v_and_b32_e32 v2, 15, v0
	v_lshlrev_b32_e32 v4, 1, v3
	v_lshlrev_b32_e32 v5, 6, v0
	s_movk_i32 s0, 0x3c0
	v_lshlrev_b32_e32 v6, 2, v0
	v_and_or_b32 v5, v5, s0, v4
	v_and_b32_e32 v6, 32, v6
	v_lshl_or_b32 v148, s27, 6, v2
	s_lshl_b32 s0, s27, 13
	v_lshl_or_b32 v2, v2, 6, v4
	v_bitop3_b32 v2, v2, s0, v6 bitop3:0xde
	s_lshl_b32 s0, s26, 5
	s_and_b32 s0, s0, 0x60
	v_or_b32_e32 v150, s0, v3
	v_lshlrev_b32_e32 v3, 9, v0
	v_and_b32_e32 v3, 0x30000, v3
	v_lshlrev_b32_e32 v4, 12, v10
	v_or3_b32 v3, v8, v3, v4
	s_ashr_i32 s72, s34, 31
	s_lshl_b32 s26, s0, 7
	v_add_u32_e32 v136, v3, v9
	v_lshlrev_b32_e32 v3, 5, v11
	s_waitcnt vmcnt(6)
	s_cmpk_lt_u32 s1, 0x100
	v_and_b32_e32 v3, 0x70000, v3
	v_bitop3_b32 v149, s26, v5, v6 bitop3:0xf6
	s_cselect_b64 s[40:41], -1, 0
	v_or3_b32 v3, v8, v3, v4
	s_add_i32 s73, 0, 0x10000
	s_add_i32 s74, 0, 0x14000
	v_mov_b32_e32 v137, v131
	v_add_u32_e32 v138, v3, v9
	v_mov_b32_e32 v139, v131
	v_mov_b64_e32 v[140:141], 0xb00
	v_mov_b64_e32 v[142:143], 0xaff
	v_add_u32_e32 v151, s73, v149
	v_add_u32_e32 v152, s74, v149
	v_add_u32_e32 v153, 0, v2
	s_movk_i32 s75, 0x1600
	s_mov_b32 s44, 0xbfb8aa3b
	s_mov_b32 s50, 0x3e000000
	s_mov_b32 s80, 0xc3e00000
	v_mov_b32_e32 v154, 0x43e00000
	s_barrier
	v_mov_b32_e32 v251, 0
	global_load_dword v250, v251, s[28:29]
	global_load_dword v250, v251, s[28:29]
	global_load_dword v250, v251, s[28:29]
	global_load_dword v250, v251, s[28:29]
	global_load_dword v250, v251, s[28:29]
	global_load_dword v250, v251, s[28:29]
	global_load_dword v250, v251, s[28:29]
	global_load_dword v250, v251, s[28:29]
	s_branch .LBB0_780

.LBB0_782:
	s_ashr_i32 s55, s54, 31
	s_lshl_b64 s[26:27], s[54:55], 20
	v_readlane_b32 s56, v254, 56
	v_readlane_b32 s57, v254, 57
	s_add_u32 s56, s56, s26
	s_addc_u32 s57, s57, s27
	s_and_b64 s[26:27], s[0:1], exec
	s_cselect_b32 s55, s57, s65
	s_cselect_b32 s81, s56, s64
	s_ashr_i32 s53, s52, 31
	s_lshl_b64 s[26:27], s[52:53], 20
	s_add_u32 s58, s3, s26
	s_addc_u32 s59, s33, s27
	s_and_b64 s[26:27], s[0:1], exec
	s_cselect_b32 s53, s59, s63
	s_cselect_b32 s82, s58, s62
	s_add_u32 s83, s62, 0x10000
	s_addc_u32 s84, s63, 0
	s_add_u32 s62, s64, 0x80080
	s_addc_u32 s63, s65, 0
	s_mov_b32 s85, -2
	ds_read_b128 v[144:147], v151
	ds_read_b128 v[156:159], v151 offset:1024
	ds_read_b128 v[160:163], v151 offset:2048
	ds_read_b128 v[164:167], v151 offset:3072
	ds_read_b128 v[168:171], v152
	ds_read_b128 v[172:175], v152 offset:1024
	ds_read_b128 v[176:179], v152 offset:2048
	ds_read_b128 v[180:183], v152 offset:3072
	s_add_u32 s26, s62, 0xfff80080
	s_addc_u32 s27, s63, -1
	s_cmp_eq_u32 s85, 28
	s_cselect_b32 s65, s55, s27
	s_cselect_b32 s64, s81, s26
	s_cselect_b32 s27, s53, s84
	s_cselect_b32 s26, s82, s83
	v_lshl_add_u64 v[216:217], s[62:63], 0, v[136:137]
	s_add_i32 m0, s61, 0xc000
	ds_read_b128 v[184:187], v153
	ds_read_b128 v[188:191], v153 offset:1024
	ds_read_b128 v[192:195], v153 offset:2048
	ds_read_b128 v[196:199], v153 offset:3072
	ds_read_b128 v[200:203], v153 offset:4096
	ds_read_b128 v[204:207], v153 offset:5120
	ds_read_b128 v[208:211], v153 offset:6144
	ds_read_b128 v[212:215], v153 offset:7168
	global_load_lds_dwordx4 v[216:217], off
	v_lshl_add_u64 v[216:217], s[62:63], 0, v[138:139]
	s_add_i32 m0, s61, 0xe000
	s_nop 0
	global_load_lds_dwordx4 v[216:217], off
	s_waitcnt vmcnt(16)
	s_waitcnt lgkmcnt(0)
	s_barrier
	s_waitcnt lgkmcnt(0)
	v_mfma_f32_16x16x32_bf16 v[126:129], v[144:147], v[184:187], 0
	v_mfma_f32_16x16x32_bf16 v[118:121], v[160:163], v[184:187], 0
	v_mfma_f32_16x16x32_bf16 v[110:113], v[144:147], v[192:195], 0
	v_mfma_f32_16x16x32_bf16 v[102:105], v[160:163], v[192:195], 0
	v_mfma_f32_16x16x32_bf16 v[94:97], v[144:147], v[200:203], 0
	v_mfma_f32_16x16x32_bf16 v[86:89], v[160:163], v[200:203], 0
	v_mfma_f32_16x16x32_bf16 v[78:81], v[144:147], v[208:211], 0
	v_mfma_f32_16x16x32_bf16 v[70:73], v[160:163], v[208:211], 0
	v_mfma_f32_16x16x32_bf16 v[126:129], v[156:159], v[188:191], v[126:129]
	v_mfma_f32_16x16x32_bf16 v[118:121], v[164:167], v[188:191], v[118:121]
	v_mfma_f32_16x16x32_bf16 v[110:113], v[156:159], v[196:199], v[110:113]
	v_mfma_f32_16x16x32_bf16 v[102:105], v[164:167], v[196:199], v[102:105]
	v_mfma_f32_16x16x32_bf16 v[94:97], v[156:159], v[204:207], v[94:97]
	v_mfma_f32_16x16x32_bf16 v[86:89], v[164:167], v[204:207], v[86:89]
	v_mfma_f32_16x16x32_bf16 v[78:81], v[156:159], v[212:215], v[78:81]
	v_mfma_f32_16x16x32_bf16 v[70:73], v[164:167], v[212:215], v[70:73]
	v_mfma_f32_16x16x32_bf16 v[122:125], v[168:171], v[184:187], 0
	v_mfma_f32_16x16x32_bf16 v[114:117], v[176:179], v[184:187], 0
	v_mfma_f32_16x16x32_bf16 v[106:109], v[168:171], v[192:195], 0
	v_mfma_f32_16x16x32_bf16 v[98:101], v[176:179], v[192:195], 0
	v_mfma_f32_16x16x32_bf16 v[90:93], v[168:171], v[200:203], 0
	v_mfma_f32_16x16x32_bf16 v[82:85], v[176:179], v[200:203], 0
	v_mfma_f32_16x16x32_bf16 v[74:77], v[168:171], v[208:211], 0
	v_mfma_f32_16x16x32_bf16 v[66:69], v[176:179], v[208:211], 0
	v_mfma_f32_16x16x32_bf16 v[122:125], v[172:175], v[188:191], v[122:125]
	v_mfma_f32_16x16x32_bf16 v[114:117], v[180:183], v[188:191], v[114:117]
	v_mfma_f32_16x16x32_bf16 v[106:109], v[172:175], v[196:199], v[106:109]
	v_mfma_f32_16x16x32_bf16 v[98:101], v[180:183], v[196:199], v[98:101]
	v_mfma_f32_16x16x32_bf16 v[90:93], v[172:175], v[204:207], v[90:93]
	v_mfma_f32_16x16x32_bf16 v[82:85], v[180:183], v[204:207], v[82:85]
	v_mfma_f32_16x16x32_bf16 v[74:77], v[172:175], v[212:215], v[74:77]
	v_mfma_f32_16x16x32_bf16 v[66:69], v[180:183], v[212:215], v[66:69]
	s_barrier
	v_lshl_add_u64 v[216:217], s[26:27], 0, v[130:131]
	s_add_i32 s26, s73, s35
	s_mov_b32 m0, s26
	ds_read_b128 v[184:187], v153 offset:16384
	ds_read_b128 v[188:191], v153 offset:17408
	ds_read_b128 v[192:195], v153 offset:18432
	ds_read_b128 v[196:199], v153 offset:19456
	ds_read_b128 v[200:203], v153 offset:20480
	ds_read_b128 v[204:207], v153 offset:21504
	ds_read_b128 v[208:211], v153 offset:22528
	ds_read_b128 v[212:215], v153 offset:23552
	global_load_lds_dwordx4 v[216:217], off
	v_lshl_add_u64 v[220:221], v[216:217], 0, s[6:7]
	s_add_i32 m0, s26, 0x2000
	s_add_i32 s26, s74, s35
	global_load_lds_dwordx4 v[220:221], off
	v_lshl_add_u64 v[220:221], v[216:217], 0, s[8:9]
	s_mov_b32 m0, s26
	v_lshl_add_u64 v[222:223], s[64:65], 0, v[134:135]
	global_load_lds_dwordx4 v[220:221], off
	v_lshl_add_u64 v[220:221], v[216:217], 0, s[10:11]
	s_add_i32 m0, s26, 0x2000
	s_nop 0
	global_load_lds_dwordx4 v[220:221], off
	v_lshl_add_u64 v[220:221], s[64:65], 0, v[132:133]
	s_mov_b32 m0, s61
	s_nop 0
	global_load_lds_dwordx4 v[220:221], off
	s_mov_b32 m0, s66
	s_nop 0
	global_load_lds_dwordx4 v[222:223], off
	s_waitcnt vmcnt(16)
	s_waitcnt lgkmcnt(0)
	s_barrier
	s_waitcnt lgkmcnt(0)
	v_mfma_f32_16x16x32_bf16 v[62:65], v[144:147], v[184:187], 0
	v_mfma_f32_16x16x32_bf16 v[54:57], v[160:163], v[184:187], 0
	v_mfma_f32_16x16x32_bf16 v[46:49], v[144:147], v[192:195], 0
	v_mfma_f32_16x16x32_bf16 v[38:41], v[160:163], v[192:195], 0
	v_mfma_f32_16x16x32_bf16 v[30:33], v[144:147], v[200:203], 0
	v_mfma_f32_16x16x32_bf16 v[22:25], v[160:163], v[200:203], 0
	v_mfma_f32_16x16x32_bf16 v[14:17], v[144:147], v[208:211], 0
	v_mfma_f32_16x16x32_bf16 v[6:9], v[160:163], v[208:211], 0
	v_mfma_f32_16x16x32_bf16 v[62:65], v[156:159], v[188:191], v[62:65]
	v_mfma_f32_16x16x32_bf16 v[54:57], v[164:167], v[188:191], v[54:57]
	v_mfma_f32_16x16x32_bf16 v[46:49], v[156:159], v[196:199], v[46:49]
	v_mfma_f32_16x16x32_bf16 v[38:41], v[164:167], v[196:199], v[38:41]
	v_mfma_f32_16x16x32_bf16 v[30:33], v[156:159], v[204:207], v[30:33]
	v_mfma_f32_16x16x32_bf16 v[22:25], v[164:167], v[204:207], v[22:25]
	v_mfma_f32_16x16x32_bf16 v[14:17], v[156:159], v[212:215], v[14:17]
	v_mfma_f32_16x16x32_bf16 v[6:9], v[164:167], v[212:215], v[6:9]
	v_mfma_f32_16x16x32_bf16 v[58:61], v[168:171], v[184:187], 0
	v_mfma_f32_16x16x32_bf16 v[50:53], v[176:179], v[184:187], 0
	v_mfma_f32_16x16x32_bf16 v[42:45], v[168:171], v[192:195], 0
	v_mfma_f32_16x16x32_bf16 v[34:37], v[176:179], v[192:195], 0
	v_mfma_f32_16x16x32_bf16 v[26:29], v[168:171], v[200:203], 0
	v_mfma_f32_16x16x32_bf16 v[18:21], v[176:179], v[200:203], 0
	v_mfma_f32_16x16x32_bf16 v[10:13], v[168:171], v[208:211], 0
	v_mfma_f32_16x16x32_bf16 v[2:5], v[176:179], v[208:211], 0
	v_mfma_f32_16x16x32_bf16 v[58:61], v[172:175], v[188:191], v[58:61]
	v_mfma_f32_16x16x32_bf16 v[50:53], v[180:183], v[188:191], v[50:53]
	v_mfma_f32_16x16x32_bf16 v[42:45], v[172:175], v[196:199], v[42:45]
	v_mfma_f32_16x16x32_bf16 v[34:37], v[180:183], v[196:199], v[34:37]
	v_mfma_f32_16x16x32_bf16 v[26:29], v[172:175], v[204:207], v[26:29]
	v_mfma_f32_16x16x32_bf16 v[18:21], v[180:183], v[204:207], v[18:21]
	v_mfma_f32_16x16x32_bf16 v[10:13], v[172:175], v[212:215], v[10:13]
	v_mfma_f32_16x16x32_bf16 v[2:5], v[180:183], v[212:215], v[2:5]
	s_barrier
	s_add_i32 s86, 0, 0x18000
	v_add_u32_e32 v155, s86, v149
	s_add_i32 s87, 0, 0x1c000
	ds_read_b128 v[144:147], v155
	ds_read_b128 v[156:159], v155 offset:1024
	ds_read_b128 v[160:163], v155 offset:2048
	ds_read_b128 v[164:167], v155 offset:3072
	v_add_u32_e32 v155, s87, v149
	ds_read_b128 v[168:171], v155
	ds_read_b128 v[172:175], v155 offset:1024
	ds_read_b128 v[176:179], v155 offset:2048
	ds_read_b128 v[180:183], v155 offset:3072
	s_add_u32 s26, s64, 0x80000
	s_addc_u32 s27, s65, 0
	s_mov_b32 m0, s67
	v_lshl_add_u64 v[224:225], s[26:27], 0, v[132:133]
	ds_read_b128 v[184:187], v153 offset:32768
	ds_read_b128 v[188:191], v153 offset:33792
	ds_read_b128 v[192:195], v153 offset:34816
	ds_read_b128 v[196:199], v153 offset:35840
	ds_read_b128 v[200:203], v153 offset:36864
	ds_read_b128 v[204:207], v153 offset:37888
	ds_read_b128 v[208:211], v153 offset:38912
	ds_read_b128 v[212:215], v153 offset:39936
	global_load_lds_dwordx4 v[224:225], off
	v_lshl_add_u64 v[224:225], s[26:27], 0, v[134:135]
	s_mov_b32 m0, s68
	s_nop 0
	global_load_lds_dwordx4 v[224:225], off
	s_waitcnt vmcnt(8)
	s_waitcnt lgkmcnt(0)
	s_barrier
	s_waitcnt lgkmcnt(0)
	v_mfma_f32_16x16x32_bf16 v[126:129], v[144:147], v[184:187], v[126:129]
	v_mfma_f32_16x16x32_bf16 v[118:121], v[160:163], v[184:187], v[118:121]
	v_mfma_f32_16x16x32_bf16 v[110:113], v[144:147], v[192:195], v[110:113]
	v_mfma_f32_16x16x32_bf16 v[102:105], v[160:163], v[192:195], v[102:105]
	v_mfma_f32_16x16x32_bf16 v[94:97], v[144:147], v[200:203], v[94:97]
	v_mfma_f32_16x16x32_bf16 v[86:89], v[160:163], v[200:203], v[86:89]
	v_mfma_f32_16x16x32_bf16 v[78:81], v[144:147], v[208:211], v[78:81]
	v_mfma_f32_16x16x32_bf16 v[70:73], v[160:163], v[208:211], v[70:73]
	v_mfma_f32_16x16x32_bf16 v[126:129], v[156:159], v[188:191], v[126:129]
	v_mfma_f32_16x16x32_bf16 v[118:121], v[164:167], v[188:191], v[118:121]
	v_mfma_f32_16x16x32_bf16 v[110:113], v[156:159], v[196:199], v[110:113]
	v_mfma_f32_16x16x32_bf16 v[102:105], v[164:167], v[196:199], v[102:105]
	v_mfma_f32_16x16x32_bf16 v[94:97], v[156:159], v[204:207], v[94:97]
	v_mfma_f32_16x16x32_bf16 v[86:89], v[164:167], v[204:207], v[86:89]
	v_mfma_f32_16x16x32_bf16 v[78:81], v[156:159], v[212:215], v[78:81]
	v_mfma_f32_16x16x32_bf16 v[70:73], v[164:167], v[212:215], v[70:73]
	v_mfma_f32_16x16x32_bf16 v[122:125], v[168:171], v[184:187], v[122:125]
	v_mfma_f32_16x16x32_bf16 v[114:117], v[176:179], v[184:187], v[114:117]
	v_mfma_f32_16x16x32_bf16 v[106:109], v[168:171], v[192:195], v[106:109]
	v_mfma_f32_16x16x32_bf16 v[98:101], v[176:179], v[192:195], v[98:101]
	v_mfma_f32_16x16x32_bf16 v[90:93], v[168:171], v[200:203], v[90:93]
	v_mfma_f32_16x16x32_bf16 v[82:85], v[176:179], v[200:203], v[82:85]
	v_mfma_f32_16x16x32_bf16 v[74:77], v[168:171], v[208:211], v[74:77]
	v_mfma_f32_16x16x32_bf16 v[66:69], v[176:179], v[208:211], v[66:69]
	v_mfma_f32_16x16x32_bf16 v[122:125], v[172:175], v[188:191], v[122:125]
	v_mfma_f32_16x16x32_bf16 v[114:117], v[180:183], v[188:191], v[114:117]
	v_mfma_f32_16x16x32_bf16 v[106:109], v[172:175], v[196:199], v[106:109]
	v_mfma_f32_16x16x32_bf16 v[98:101], v[180:183], v[196:199], v[98:101]
	v_mfma_f32_16x16x32_bf16 v[90:93], v[172:175], v[204:207], v[90:93]
	v_mfma_f32_16x16x32_bf16 v[82:85], v[180:183], v[204:207], v[82:85]
	v_mfma_f32_16x16x32_bf16 v[74:77], v[172:175], v[212:215], v[74:77]
	v_mfma_f32_16x16x32_bf16 v[66:69], v[180:183], v[212:215], v[66:69]
	s_barrier
	s_add_i32 s26, s86, s35
	v_lshl_add_u64 v[224:225], v[216:217], 0, s[16:17]
	s_mov_b32 m0, s26
	ds_read_b128 v[184:187], v153 offset:49152
	ds_read_b128 v[188:191], v153 offset:50176
	ds_read_b128 v[192:195], v153 offset:51200
	ds_read_b128 v[196:199], v153 offset:52224
	ds_read_b128 v[200:203], v153 offset:53248
	ds_read_b128 v[204:207], v153 offset:54272
	ds_read_b128 v[208:211], v153 offset:55296
	ds_read_b128 v[212:215], v153 offset:56320
	global_load_lds_dwordx4 v[224:225], off
	v_lshl_add_u64 v[224:225], v[216:217], 0, s[18:19]
	s_add_i32 m0, s26, 0x2000
	s_add_i32 s26, s87, s35
	global_load_lds_dwordx4 v[224:225], off
	v_lshl_add_u64 v[224:225], v[216:217], 0, s[22:23]
	s_mov_b32 m0, s26
	v_lshl_add_u64 v[216:217], v[216:217], 0, s[24:25]
	global_load_lds_dwordx4 v[224:225], off
	s_add_i32 m0, s26, 0x2000
	s_nop 0
	global_load_lds_dwordx4 v[216:217], off
	v_lshl_add_u64 v[216:217], v[220:221], 0, s[20:21]
	s_mov_b32 m0, s70
	s_nop 0
	global_load_lds_dwordx4 v[216:217], off
	v_lshl_add_u64 v[216:217], v[222:223], 0, s[20:21]
	s_mov_b32 m0, s71
	s_nop 0
	global_load_lds_dwordx4 v[216:217], off
	s_waitcnt vmcnt(8)
	s_waitcnt lgkmcnt(0)
	s_barrier
	s_waitcnt lgkmcnt(0)
	v_mfma_f32_16x16x32_bf16 v[62:65], v[144:147], v[184:187], v[62:65]
	v_mfma_f32_16x16x32_bf16 v[54:57], v[160:163], v[184:187], v[54:57]
	v_mfma_f32_16x16x32_bf16 v[46:49], v[144:147], v[192:195], v[46:49]
	v_mfma_f32_16x16x32_bf16 v[38:41], v[160:163], v[192:195], v[38:41]
	v_mfma_f32_16x16x32_bf16 v[30:33], v[144:147], v[200:203], v[30:33]
	v_mfma_f32_16x16x32_bf16 v[22:25], v[160:163], v[200:203], v[22:25]
	v_mfma_f32_16x16x32_bf16 v[14:17], v[144:147], v[208:211], v[14:17]
	v_mfma_f32_16x16x32_bf16 v[6:9], v[160:163], v[208:211], v[6:9]
	v_mfma_f32_16x16x32_bf16 v[62:65], v[156:159], v[188:191], v[62:65]
	v_mfma_f32_16x16x32_bf16 v[54:57], v[164:167], v[188:191], v[54:57]
	v_mfma_f32_16x16x32_bf16 v[46:49], v[156:159], v[196:199], v[46:49]
	v_mfma_f32_16x16x32_bf16 v[38:41], v[164:167], v[196:199], v[38:41]
	v_mfma_f32_16x16x32_bf16 v[30:33], v[156:159], v[204:207], v[30:33]
	v_mfma_f32_16x16x32_bf16 v[22:25], v[164:167], v[204:207], v[22:25]
	v_mfma_f32_16x16x32_bf16 v[14:17], v[156:159], v[212:215], v[14:17]
	v_mfma_f32_16x16x32_bf16 v[6:9], v[164:167], v[212:215], v[6:9]
	v_mfma_f32_16x16x32_bf16 v[58:61], v[168:171], v[184:187], v[58:61]
	v_mfma_f32_16x16x32_bf16 v[50:53], v[176:179], v[184:187], v[50:53]
	v_mfma_f32_16x16x32_bf16 v[42:45], v[168:171], v[192:195], v[42:45]
	v_mfma_f32_16x16x32_bf16 v[34:37], v[176:179], v[192:195], v[34:37]
	v_mfma_f32_16x16x32_bf16 v[26:29], v[168:171], v[200:203], v[26:29]
	v_mfma_f32_16x16x32_bf16 v[18:21], v[176:179], v[200:203], v[18:21]
	v_mfma_f32_16x16x32_bf16 v[10:13], v[168:171], v[208:211], v[10:13]
	v_mfma_f32_16x16x32_bf16 v[2:5], v[176:179], v[208:211], v[2:5]
	v_mfma_f32_16x16x32_bf16 v[58:61], v[172:175], v[188:191], v[58:61]
	v_mfma_f32_16x16x32_bf16 v[50:53], v[180:183], v[188:191], v[50:53]
	v_mfma_f32_16x16x32_bf16 v[42:45], v[172:175], v[196:199], v[42:45]
	v_mfma_f32_16x16x32_bf16 v[34:37], v[180:183], v[196:199], v[34:37]
	v_mfma_f32_16x16x32_bf16 v[26:29], v[172:175], v[204:207], v[26:29]
	v_mfma_f32_16x16x32_bf16 v[18:21], v[180:183], v[204:207], v[18:21]
	v_mfma_f32_16x16x32_bf16 v[10:13], v[172:175], v[212:215], v[10:13]
	v_mfma_f32_16x16x32_bf16 v[2:5], v[180:183], v[212:215], v[2:5]
	s_barrier
	s_add_i32 s85, s85, 2
	s_add_u32 s83, s83, 0x10000
	s_addc_u32 s84, s84, 0
	s_add_u32 s62, s62, 0x100
	s_addc_u32 s63, s63, 0
	s_cmp_gt_u32 s85, 29

.LBB0_786:
	v_pk_mul_f32 v[156:157], v[126:127], s[44:45] op_sel_hi:[1,0]
	v_pk_mul_f32 v[122:123], v[126:127], v[122:123]
	v_exp_f32_e32 v156, v156
	v_exp_f32_e32 v157, v157
	v_pk_mul_f32 v[126:127], v[118:119], s[44:45] op_sel_hi:[1,0]
	v_pk_mul_f32 v[158:159], v[128:129], s[44:45] op_sel_hi:[1,0]
	v_exp_f32_e32 v126, v126
	v_exp_f32_e32 v127, v127
	v_pk_fma_f32 v[156:157], v[156:157], s[50:51], s[50:51] op_sel_hi:[1,0,0]
	v_pk_mul_f32 v[124:125], v[128:129], v[124:125]
	v_pk_mul_f32 v[128:129], v[120:121], s[44:45] op_sel_hi:[1,0]
	v_exp_f32_e32 v158, v158
	v_exp_f32_e32 v159, v159
	v_rcp_f32_e32 v156, v156
	v_rcp_f32_e32 v157, v157
	v_exp_f32_e32 v128, v128
	v_exp_f32_e32 v129, v129
	v_pk_fma_f32 v[126:127], v[126:127], s[50:51], s[50:51] op_sel_hi:[1,0,0]
	v_pk_fma_f32 v[158:159], v[158:159], s[50:51], s[50:51] op_sel_hi:[1,0,0]
	v_rcp_f32_e32 v126, v126
	v_rcp_f32_e32 v127, v127
	v_pk_mul_f32 v[122:123], v[156:157], v[122:123]
	v_pk_fma_f32 v[128:129], v[128:129], s[50:51], s[50:51] op_sel_hi:[1,0,0]
	v_pk_mul_f32 v[114:115], v[118:119], v[114:115]
	v_rcp_f32_e32 v158, v158
	v_rcp_f32_e32 v159, v159
	v_rcp_f32_e32 v128, v128
	v_rcp_f32_e32 v129, v129
	v_pk_mul_f32 v[116:117], v[120:121], v[116:117]
	v_pk_mul_f32 v[114:115], v[126:127], v[114:115]
	v_med3_f32 v119, v122, s80, v154
	v_med3_f32 v120, v123, s80, v154
	v_cvt_pk_fp8_f32 v118, v119, v120
	v_med3_f32 v114, v114, s80, v154
	v_med3_f32 v115, v115, s80, v154
	v_cvt_pk_fp8_f32 v119, v114, v115
	v_pk_mul_f32 v[124:125], v[158:159], v[124:125]
	v_pk_mul_f32 v[116:117], v[128:129], v[116:117]
	v_med3_f32 v120, v124, s80, v154
	v_med3_f32 v121, v125, s80, v154
	v_med3_f32 v114, v116, s80, v154
	v_med3_f32 v115, v117, s80, v154
	v_cvt_pk_fp8_f32 v118, v120, v121 op_sel:[0,0,1]
	v_cvt_pk_fp8_f32 v119, v114, v115 op_sel:[0,0,1]
	v_lshl_add_u32 v155, s60, 8, v148
	v_lshl_or_b32 v144, s2, 7, v150
	v_mov_b64_e32 v[146:147], s[14:15]
	v_ashrrev_i32_e32 v145, 31, v144
	v_mad_i64_i32 v[114:115], s[26:27], v155, s75, v[146:147]
	v_lshl_add_u64 v[114:115], v[114:115], 0, v[144:145]
	global_store_dwordx2 v[114:115], v[118:119], off
	v_pk_mul_f32 v[114:115], v[110:111], s[44:45] op_sel_hi:[1,0]
	v_pk_mul_f32 v[106:107], v[110:111], v[106:107]
	v_exp_f32_e32 v114, v114
	v_exp_f32_e32 v115, v115
	v_pk_mul_f32 v[110:111], v[102:103], s[44:45] op_sel_hi:[1,0]
	v_pk_mul_f32 v[116:117], v[112:113], s[44:45] op_sel_hi:[1,0]
	v_exp_f32_e32 v110, v110
	v_exp_f32_e32 v111, v111
	v_pk_fma_f32 v[114:115], v[114:115], s[50:51], s[50:51] op_sel_hi:[1,0,0]
	v_pk_mul_f32 v[108:109], v[112:113], v[108:109]
	v_pk_mul_f32 v[112:113], v[104:105], s[44:45] op_sel_hi:[1,0]
	v_exp_f32_e32 v116, v116
	v_exp_f32_e32 v117, v117
	v_rcp_f32_e32 v114, v114
	v_rcp_f32_e32 v115, v115
	v_exp_f32_e32 v112, v112
	v_exp_f32_e32 v113, v113
	v_pk_fma_f32 v[110:111], v[110:111], s[50:51], s[50:51] op_sel_hi:[1,0,0]
	v_pk_fma_f32 v[116:117], v[116:117], s[50:51], s[50:51] op_sel_hi:[1,0,0]
	v_rcp_f32_e32 v110, v110
	v_rcp_f32_e32 v111, v111
	v_pk_mul_f32 v[106:107], v[114:115], v[106:107]
	v_pk_fma_f32 v[112:113], v[112:113], s[50:51], s[50:51] op_sel_hi:[1,0,0]
	v_pk_mul_f32 v[98:99], v[102:103], v[98:99]
	v_rcp_f32_e32 v116, v116
	v_rcp_f32_e32 v117, v117
	v_rcp_f32_e32 v112, v112
	v_rcp_f32_e32 v113, v113
	v_pk_mul_f32 v[100:101], v[104:105], v[100:101]
	v_pk_mul_f32 v[98:99], v[110:111], v[98:99]
	v_med3_f32 v103, v106, s80, v154
	v_med3_f32 v104, v107, s80, v154
	v_cvt_pk_fp8_f32 v102, v103, v104
	v_med3_f32 v98, v98, s80, v154
	v_med3_f32 v99, v99, s80, v154
	v_cvt_pk_fp8_f32 v103, v98, v99
	v_pk_mul_f32 v[108:109], v[116:117], v[108:109]
	v_pk_mul_f32 v[100:101], v[112:113], v[100:101]
	v_med3_f32 v104, v108, s80, v154
	v_med3_f32 v105, v109, s80, v154
	v_med3_f32 v98, v100, s80, v154
	v_med3_f32 v99, v101, s80, v154
	v_cvt_pk_fp8_f32 v102, v104, v105 op_sel:[0,0,1]
	v_cvt_pk_fp8_f32 v103, v98, v99 op_sel:[0,0,1]
	v_or_b32_e32 v118, 16, v155
	v_mad_i64_i32 v[98:99], s[26:27], v118, s75, v[146:147]
	v_lshl_add_u64 v[98:99], v[98:99], 0, v[144:145]
	global_store_dwordx2 v[98:99], v[102:103], off
	v_pk_mul_f32 v[98:99], v[94:95], s[44:45] op_sel_hi:[1,0]
	v_pk_mul_f32 v[90:91], v[94:95], v[90:91]
	v_exp_f32_e32 v98, v98
	v_exp_f32_e32 v99, v99
	v_pk_mul_f32 v[94:95], v[86:87], s[44:45] op_sel_hi:[1,0]
	v_pk_mul_f32 v[100:101], v[96:97], s[44:45] op_sel_hi:[1,0]
	v_exp_f32_e32 v94, v94
	v_exp_f32_e32 v95, v95
	v_pk_fma_f32 v[98:99], v[98:99], s[50:51], s[50:51] op_sel_hi:[1,0,0]
	v_pk_mul_f32 v[92:93], v[96:97], v[92:93]
	v_pk_mul_f32 v[96:97], v[88:89], s[44:45] op_sel_hi:[1,0]
	v_exp_f32_e32 v100, v100
	v_exp_f32_e32 v101, v101
	v_rcp_f32_e32 v98, v98
	v_rcp_f32_e32 v99, v99
	v_exp_f32_e32 v96, v96
	v_exp_f32_e32 v97, v97
	v_pk_fma_f32 v[94:95], v[94:95], s[50:51], s[50:51] op_sel_hi:[1,0,0]
	v_pk_fma_f32 v[100:101], v[100:101], s[50:51], s[50:51] op_sel_hi:[1,0,0]
	v_rcp_f32_e32 v94, v94
	v_rcp_f32_e32 v95, v95
	v_pk_mul_f32 v[90:91], v[98:99], v[90:91]
	v_pk_fma_f32 v[96:97], v[96:97], s[50:51], s[50:51] op_sel_hi:[1,0,0]
	v_pk_mul_f32 v[82:83], v[86:87], v[82:83]
	v_rcp_f32_e32 v100, v100
	v_rcp_f32_e32 v101, v101
	v_rcp_f32_e32 v96, v96
	v_rcp_f32_e32 v97, v97
	v_pk_mul_f32 v[84:85], v[88:89], v[84:85]
	v_pk_mul_f32 v[82:83], v[94:95], v[82:83]
	v_med3_f32 v87, v90, s80, v154
	v_med3_f32 v88, v91, s80, v154
	v_cvt_pk_fp8_f32 v86, v87, v88
	v_med3_f32 v82, v82, s80, v154
	v_med3_f32 v83, v83, s80, v154
	v_cvt_pk_fp8_f32 v87, v82, v83
	v_pk_mul_f32 v[92:93], v[100:101], v[92:93]
	v_pk_mul_f32 v[84:85], v[96:97], v[84:85]
	v_med3_f32 v88, v92, s80, v154
	v_med3_f32 v89, v93, s80, v154
	v_med3_f32 v82, v84, s80, v154
	v_med3_f32 v83, v85, s80, v154
	v_cvt_pk_fp8_f32 v86, v88, v89 op_sel:[0,0,1]
	v_cvt_pk_fp8_f32 v87, v82, v83 op_sel:[0,0,1]
	v_or_b32_e32 v102, 32, v155
	v_mad_i64_i32 v[82:83], s[26:27], v102, s75, v[146:147]
	v_lshl_add_u64 v[82:83], v[82:83], 0, v[144:145]
	global_store_dwordx2 v[82:83], v[86:87], off
	v_pk_mul_f32 v[82:83], v[78:79], s[44:45] op_sel_hi:[1,0]
	v_pk_mul_f32 v[74:75], v[78:79], v[74:75]
	v_exp_f32_e32 v82, v82
	v_exp_f32_e32 v83, v83
	v_pk_mul_f32 v[78:79], v[70:71], s[44:45] op_sel_hi:[1,0]
	v_pk_mul_f32 v[84:85], v[80:81], s[44:45] op_sel_hi:[1,0]
	v_exp_f32_e32 v78, v78
	v_exp_f32_e32 v79, v79
	v_pk_fma_f32 v[82:83], v[82:83], s[50:51], s[50:51] op_sel_hi:[1,0,0]
	v_pk_mul_f32 v[76:77], v[80:81], v[76:77]
	v_pk_mul_f32 v[80:81], v[72:73], s[44:45] op_sel_hi:[1,0]
	v_exp_f32_e32 v84, v84
	v_exp_f32_e32 v85, v85
	v_rcp_f32_e32 v82, v82
	v_rcp_f32_e32 v83, v83
	v_exp_f32_e32 v80, v80
	v_exp_f32_e32 v81, v81
	v_pk_fma_f32 v[78:79], v[78:79], s[50:51], s[50:51] op_sel_hi:[1,0,0]
	v_pk_fma_f32 v[84:85], v[84:85], s[50:51], s[50:51] op_sel_hi:[1,0,0]
	v_rcp_f32_e32 v78, v78
	v_rcp_f32_e32 v79, v79
	v_pk_mul_f32 v[74:75], v[82:83], v[74:75]
	v_pk_fma_f32 v[80:81], v[80:81], s[50:51], s[50:51] op_sel_hi:[1,0,0]
	v_pk_mul_f32 v[66:67], v[70:71], v[66:67]
	v_rcp_f32_e32 v84, v84
	v_rcp_f32_e32 v85, v85
	v_rcp_f32_e32 v80, v80
	v_rcp_f32_e32 v81, v81
	v_pk_mul_f32 v[68:69], v[72:73], v[68:69]
	v_pk_mul_f32 v[66:67], v[78:79], v[66:67]
	v_med3_f32 v71, v74, s80, v154
	v_med3_f32 v72, v75, s80, v154
	v_cvt_pk_fp8_f32 v70, v71, v72
	v_med3_f32 v66, v66, s80, v154
	v_med3_f32 v67, v67, s80, v154
	v_cvt_pk_fp8_f32 v71, v66, v67
	v_pk_mul_f32 v[76:77], v[84:85], v[76:77]
	v_pk_mul_f32 v[68:69], v[80:81], v[68:69]
	v_med3_f32 v72, v76, s80, v154
	v_med3_f32 v73, v77, s80, v154
	v_med3_f32 v66, v68, s80, v154
	v_med3_f32 v67, v69, s80, v154
	v_cvt_pk_fp8_f32 v70, v72, v73 op_sel:[0,0,1]
	v_cvt_pk_fp8_f32 v71, v66, v67 op_sel:[0,0,1]
	v_or_b32_e32 v86, 48, v155
	v_mad_i64_i32 v[66:67], s[26:27], v86, s75, v[146:147]
	v_lshl_add_u64 v[66:67], v[66:67], 0, v[144:145]
	global_store_dwordx2 v[66:67], v[70:71], off
	v_pk_mul_f32 v[66:67], v[62:63], s[44:45] op_sel_hi:[1,0]
	v_pk_mul_f32 v[58:59], v[62:63], v[58:59]
	v_exp_f32_e32 v66, v66
	v_exp_f32_e32 v67, v67
	v_pk_mul_f32 v[62:63], v[54:55], s[44:45] op_sel_hi:[1,0]
	v_pk_mul_f32 v[68:69], v[64:65], s[44:45] op_sel_hi:[1,0]
	v_exp_f32_e32 v62, v62
	v_exp_f32_e32 v63, v63
	v_pk_fma_f32 v[66:67], v[66:67], s[50:51], s[50:51] op_sel_hi:[1,0,0]
	v_pk_mul_f32 v[60:61], v[64:65], v[60:61]
	v_pk_mul_f32 v[64:65], v[56:57], s[44:45] op_sel_hi:[1,0]
	v_exp_f32_e32 v68, v68
	v_exp_f32_e32 v69, v69
	v_rcp_f32_e32 v66, v66
	v_rcp_f32_e32 v67, v67
	v_exp_f32_e32 v64, v64
	v_exp_f32_e32 v65, v65
	v_pk_fma_f32 v[62:63], v[62:63], s[50:51], s[50:51] op_sel_hi:[1,0,0]
	v_pk_fma_f32 v[68:69], v[68:69], s[50:51], s[50:51] op_sel_hi:[1,0,0]
	v_rcp_f32_e32 v62, v62
	v_rcp_f32_e32 v63, v63
	v_pk_mul_f32 v[58:59], v[66:67], v[58:59]
	v_pk_fma_f32 v[64:65], v[64:65], s[50:51], s[50:51] op_sel_hi:[1,0,0]
	v_pk_mul_f32 v[50:51], v[54:55], v[50:51]
	v_rcp_f32_e32 v68, v68
	v_rcp_f32_e32 v69, v69
	v_rcp_f32_e32 v64, v64
	v_rcp_f32_e32 v65, v65
	v_pk_mul_f32 v[52:53], v[56:57], v[52:53]
	v_pk_mul_f32 v[50:51], v[62:63], v[50:51]
	v_med3_f32 v55, v58, s80, v154
	v_med3_f32 v56, v59, s80, v154
	v_cvt_pk_fp8_f32 v54, v55, v56
	v_med3_f32 v50, v50, s80, v154
	v_med3_f32 v51, v51, s80, v154
	v_cvt_pk_fp8_f32 v55, v50, v51
	v_pk_mul_f32 v[60:61], v[68:69], v[60:61]
	v_pk_mul_f32 v[52:53], v[64:65], v[52:53]
	v_med3_f32 v56, v60, s80, v154
	v_med3_f32 v57, v61, s80, v154
	v_med3_f32 v50, v52, s80, v154
	v_med3_f32 v51, v53, s80, v154
	v_cvt_pk_fp8_f32 v54, v56, v57 op_sel:[0,0,1]
	v_cvt_pk_fp8_f32 v55, v50, v51 op_sel:[0,0,1]
	v_add_u32_e32 v70, 0x80, v155
	v_mad_i64_i32 v[50:51], s[26:27], v70, s75, v[146:147]
	v_lshl_add_u64 v[50:51], v[50:51], 0, v[144:145]
	global_store_dwordx2 v[50:51], v[54:55], off
	v_pk_mul_f32 v[50:51], v[46:47], s[44:45] op_sel_hi:[1,0]
	v_pk_mul_f32 v[42:43], v[46:47], v[42:43]
	v_exp_f32_e32 v50, v50
	v_exp_f32_e32 v51, v51
	v_pk_mul_f32 v[46:47], v[38:39], s[44:45] op_sel_hi:[1,0]
	v_pk_mul_f32 v[52:53], v[48:49], s[44:45] op_sel_hi:[1,0]
	v_exp_f32_e32 v46, v46
	v_exp_f32_e32 v47, v47
	v_pk_fma_f32 v[50:51], v[50:51], s[50:51], s[50:51] op_sel_hi:[1,0,0]
	v_pk_mul_f32 v[44:45], v[48:49], v[44:45]
	v_pk_mul_f32 v[48:49], v[40:41], s[44:45] op_sel_hi:[1,0]
	v_exp_f32_e32 v52, v52
	v_exp_f32_e32 v53, v53
	v_rcp_f32_e32 v50, v50
	v_rcp_f32_e32 v51, v51
	v_exp_f32_e32 v48, v48
	v_exp_f32_e32 v49, v49
	v_pk_fma_f32 v[46:47], v[46:47], s[50:51], s[50:51] op_sel_hi:[1,0,0]
	v_pk_fma_f32 v[52:53], v[52:53], s[50:51], s[50:51] op_sel_hi:[1,0,0]
	v_rcp_f32_e32 v46, v46
	v_rcp_f32_e32 v47, v47
	v_pk_mul_f32 v[42:43], v[50:51], v[42:43]
	v_pk_fma_f32 v[48:49], v[48:49], s[50:51], s[50:51] op_sel_hi:[1,0,0]
	v_pk_mul_f32 v[34:35], v[38:39], v[34:35]
	v_rcp_f32_e32 v52, v52
	v_rcp_f32_e32 v53, v53
	v_rcp_f32_e32 v48, v48
	v_rcp_f32_e32 v49, v49
	v_pk_mul_f32 v[36:37], v[40:41], v[36:37]
	v_pk_mul_f32 v[34:35], v[46:47], v[34:35]
	v_med3_f32 v39, v42, s80, v154
	v_med3_f32 v40, v43, s80, v154
	v_cvt_pk_fp8_f32 v38, v39, v40
	v_med3_f32 v34, v34, s80, v154
	v_med3_f32 v35, v35, s80, v154
	v_cvt_pk_fp8_f32 v39, v34, v35
	v_pk_mul_f32 v[44:45], v[52:53], v[44:45]
	v_pk_mul_f32 v[36:37], v[48:49], v[36:37]
	v_med3_f32 v40, v44, s80, v154
	v_med3_f32 v41, v45, s80, v154
	v_med3_f32 v34, v36, s80, v154
	v_med3_f32 v35, v37, s80, v154
	v_cvt_pk_fp8_f32 v38, v40, v41 op_sel:[0,0,1]
	v_cvt_pk_fp8_f32 v39, v34, v35 op_sel:[0,0,1]
	v_add_u32_e32 v54, 0x90, v155
	v_mad_i64_i32 v[34:35], s[26:27], v54, s75, v[146:147]
	v_lshl_add_u64 v[34:35], v[34:35], 0, v[144:145]
	global_store_dwordx2 v[34:35], v[38:39], off
	v_pk_mul_f32 v[34:35], v[30:31], s[44:45] op_sel_hi:[1,0]
	v_pk_mul_f32 v[26:27], v[30:31], v[26:27]
	v_exp_f32_e32 v34, v34
	v_exp_f32_e32 v35, v35
	v_pk_mul_f32 v[30:31], v[22:23], s[44:45] op_sel_hi:[1,0]
	v_pk_mul_f32 v[36:37], v[32:33], s[44:45] op_sel_hi:[1,0]
	v_exp_f32_e32 v30, v30
	v_exp_f32_e32 v31, v31
	v_pk_fma_f32 v[34:35], v[34:35], s[50:51], s[50:51] op_sel_hi:[1,0,0]
	v_pk_mul_f32 v[28:29], v[32:33], v[28:29]
	v_pk_mul_f32 v[32:33], v[24:25], s[44:45] op_sel_hi:[1,0]
	v_exp_f32_e32 v36, v36
	v_exp_f32_e32 v37, v37
	v_rcp_f32_e32 v34, v34
	v_rcp_f32_e32 v35, v35
	v_exp_f32_e32 v32, v32
	v_exp_f32_e32 v33, v33
	v_pk_fma_f32 v[30:31], v[30:31], s[50:51], s[50:51] op_sel_hi:[1,0,0]
	v_pk_fma_f32 v[36:37], v[36:37], s[50:51], s[50:51] op_sel_hi:[1,0,0]
	v_rcp_f32_e32 v30, v30
	v_rcp_f32_e32 v31, v31
	v_pk_mul_f32 v[26:27], v[34:35], v[26:27]
	v_pk_fma_f32 v[32:33], v[32:33], s[50:51], s[50:51] op_sel_hi:[1,0,0]
	v_pk_mul_f32 v[18:19], v[22:23], v[18:19]
	v_rcp_f32_e32 v36, v36
	v_rcp_f32_e32 v37, v37
	v_rcp_f32_e32 v32, v32
	v_rcp_f32_e32 v33, v33
	v_pk_mul_f32 v[20:21], v[24:25], v[20:21]
	v_pk_mul_f32 v[18:19], v[30:31], v[18:19]
	v_med3_f32 v23, v26, s80, v154
	v_med3_f32 v24, v27, s80, v154
	v_cvt_pk_fp8_f32 v22, v23, v24
	v_med3_f32 v18, v18, s80, v154
	v_med3_f32 v19, v19, s80, v154
	v_cvt_pk_fp8_f32 v23, v18, v19
	v_pk_mul_f32 v[28:29], v[36:37], v[28:29]
	v_pk_mul_f32 v[20:21], v[32:33], v[20:21]
	v_med3_f32 v24, v28, s80, v154
	v_med3_f32 v25, v29, s80, v154
	v_med3_f32 v18, v20, s80, v154
	v_med3_f32 v19, v21, s80, v154
	v_cvt_pk_fp8_f32 v22, v24, v25 op_sel:[0,0,1]
	v_cvt_pk_fp8_f32 v23, v18, v19 op_sel:[0,0,1]
	v_add_u32_e32 v38, 0xa0, v155
	v_mad_i64_i32 v[18:19], s[26:27], v38, s75, v[146:147]
	v_lshl_add_u64 v[18:19], v[18:19], 0, v[144:145]
	global_store_dwordx2 v[18:19], v[22:23], off
	v_pk_mul_f32 v[18:19], v[14:15], s[44:45] op_sel_hi:[1,0]
	v_pk_mul_f32 v[10:11], v[14:15], v[10:11]
	v_exp_f32_e32 v18, v18
	v_exp_f32_e32 v19, v19
	v_pk_mul_f32 v[14:15], v[6:7], s[44:45] op_sel_hi:[1,0]
	v_pk_mul_f32 v[20:21], v[16:17], s[44:45] op_sel_hi:[1,0]
	v_exp_f32_e32 v14, v14
	v_exp_f32_e32 v15, v15
	v_pk_fma_f32 v[18:19], v[18:19], s[50:51], s[50:51] op_sel_hi:[1,0,0]
	v_pk_mul_f32 v[12:13], v[16:17], v[12:13]
	v_pk_mul_f32 v[16:17], v[8:9], s[44:45] op_sel_hi:[1,0]
	v_exp_f32_e32 v20, v20
	v_exp_f32_e32 v21, v21
	v_rcp_f32_e32 v18, v18
	v_rcp_f32_e32 v19, v19
	v_exp_f32_e32 v16, v16
	v_exp_f32_e32 v17, v17
	v_pk_fma_f32 v[14:15], v[14:15], s[50:51], s[50:51] op_sel_hi:[1,0,0]
	v_pk_fma_f32 v[20:21], v[20:21], s[50:51], s[50:51] op_sel_hi:[1,0,0]
	v_rcp_f32_e32 v14, v14
	v_rcp_f32_e32 v15, v15
	v_pk_mul_f32 v[10:11], v[18:19], v[10:11]
	v_pk_fma_f32 v[16:17], v[16:17], s[50:51], s[50:51] op_sel_hi:[1,0,0]
	v_pk_mul_f32 v[2:3], v[6:7], v[2:3]
	v_rcp_f32_e32 v20, v20
	v_rcp_f32_e32 v21, v21
	v_rcp_f32_e32 v16, v16
	v_rcp_f32_e32 v17, v17
	v_pk_mul_f32 v[4:5], v[8:9], v[4:5]
	v_pk_mul_f32 v[2:3], v[14:15], v[2:3]
	v_med3_f32 v7, v10, s80, v154
	v_med3_f32 v8, v11, s80, v154
	v_cvt_pk_fp8_f32 v6, v7, v8
	v_med3_f32 v2, v2, s80, v154
	v_med3_f32 v3, v3, s80, v154
	v_cvt_pk_fp8_f32 v7, v2, v3
	v_pk_mul_f32 v[12:13], v[20:21], v[12:13]
	v_pk_mul_f32 v[4:5], v[16:17], v[4:5]
	v_med3_f32 v8, v12, s80, v154
	v_med3_f32 v9, v13, s80, v154
	v_med3_f32 v2, v4, s80, v154
	v_med3_f32 v3, v5, s80, v154
	v_cvt_pk_fp8_f32 v6, v8, v9 op_sel:[0,0,1]
	v_cvt_pk_fp8_f32 v7, v2, v3 op_sel:[0,0,1]
	v_add_u32_e32 v22, 0xb0, v155
	v_mad_i64_i32 v[2:3], s[26:27], v22, s75, v[146:147]
	v_lshl_add_u64 v[2:3], v[2:3], 0, v[144:145]
	s_andn2_b64 vcc, exec, s[0:1]
	s_mov_b64 s[0:1], -1
	global_store_dwordx2 v[2:3], v[6:7], off
	s_cbranch_vccnz .LBB0_779
	s_andn2_b64 vcc, exec, s[12:13]
	s_cbranch_vccnz .LBB0_778
	s_barrier
	s_branch .LBB0_778

.LBB0_918:
	v_mul_f32_e32 v110, v95, v95
	v_mul_f32_e32 v111, v97, v97
	v_fmac_f32_e32 v110, v94, v94
	v_fmac_f32_e32 v111, v96, v96
	v_add_f32_e32 v110, v110, v111
	v_mul_f32_e32 v111, v91, v91
	v_mul_f32_e32 v112, v93, v93
	v_fmac_f32_e32 v111, v90, v90
	v_fmac_f32_e32 v112, v92, v92
	v_add_f32_e32 v111, v111, v112
	v_add_f32_e32 v110, v111, v110
	v_mul_f32_e32 v111, v87, v87
	v_mul_f32_e32 v112, v89, v89
	v_fmac_f32_e32 v111, v86, v86
	v_fmac_f32_e32 v112, v88, v88
	v_add_f32_e32 v111, v111, v112
	v_add_f32_e32 v110, v111, v110
	v_mul_f32_e32 v111, v83, v83
	v_mul_f32_e32 v112, v85, v85
	v_fmac_f32_e32 v111, v82, v82
	v_fmac_f32_e32 v112, v84, v84
	v_add_f32_e32 v111, v111, v112
	v_add_f32_e32 v110, v111, v110
	v_mul_f32_e32 v111, v79, v79
	v_mul_f32_e32 v112, v81, v81
	v_fmac_f32_e32 v111, v78, v78
	v_fmac_f32_e32 v112, v80, v80
	v_add_f32_e32 v111, v111, v112
	v_add_f32_e32 v110, v111, v110
	v_mul_f32_e32 v111, v43, v43
	v_mul_f32_e32 v112, v45, v45
	v_fmac_f32_e32 v111, v42, v42
	v_fmac_f32_e32 v112, v44, v44
	v_add_f32_e32 v111, v111, v112
	v_add_f32_e32 v110, v111, v110
	v_mul_f32_e32 v111, v39, v39
	v_mul_f32_e32 v112, v41, v41
	v_fmac_f32_e32 v111, v38, v38
	v_fmac_f32_e32 v112, v40, v40
	v_add_f32_e32 v111, v111, v112
	v_add_f32_e32 v110, v111, v110
	v_mul_f32_e32 v111, v35, v35
	v_mul_f32_e32 v112, v37, v37
	v_fmac_f32_e32 v111, v34, v34
	v_fmac_f32_e32 v112, v36, v36
	v_add_f32_e32 v111, v111, v112
	v_add_f32_e32 v110, v111, v110
	ds_bpermute_b32 v111, v102, v110
	v_lshl_add_u64 v[100:101], v[100:101], 0, s[10:11]
	s_waitcnt lgkmcnt(0)
	v_add_f32_e32 v110, v110, v111
	ds_bpermute_b32 v111, v103, v110
	s_waitcnt lgkmcnt(0)
	v_add_f32_e32 v110, v110, v111
	ds_bpermute_b32 v111, v104, v110
	s_waitcnt lgkmcnt(0)
	v_add_f32_e32 v110, v110, v111
	ds_bpermute_b32 v111, v105, v110
	s_waitcnt lgkmcnt(0)
	v_add_f32_e32 v110, v110, v111
	ds_bpermute_b32 v111, v106, v110
	s_waitcnt lgkmcnt(0)
	v_add_f32_e32 v110, v110, v111
	ds_bpermute_b32 v111, v107, v110
	s_waitcnt lgkmcnt(0)
	v_add_f32_e32 v110, v110, v111
	v_fmamk_f32 v110, v110, 0x3a000000, v108
	v_mul_f32_e32 v111, 0x4b800000, v110
	v_cmp_gt_f32_e32 vcc, s1, v110
	s_nop 1
	v_cndmask_b32_e32 v110, v110, v111, vcc
	v_rsq_f32_e32 v110, v110
	s_nop 0
	v_mul_f32_e32 v111, 0x45800000, v110
	v_cndmask_b32_e32 v110, v110, v111, vcc
	v_pk_mul_f32 v[94:95], v[94:95], v[110:111] op_sel_hi:[1,0]
	v_pk_mul_f32 v[96:97], v[96:97], v[110:111] op_sel_hi:[1,0]
	v_pk_mul_f32 v[94:95], v[2:3], v[94:95]
	v_med3_f32 v94, v94, s2, v109
	v_med3_f32 v95, v95, s2, v109
	v_cvt_pk_fp8_f32 v111, v94, v95
	v_pk_mul_f32 v[94:95], v[4:5], v[96:97]
	s_andn2_b64 vcc, exec, s[12:13]
	v_med3_f32 v94, v94, s2, v109
	v_med3_f32 v95, v95, s2, v109
	v_cvt_pk_fp8_f32 v111, v94, v95 op_sel:[0,0,1]
	s_nop 0
	v_pk_mul_f32 v[90:91], v[90:91], v[110:111] op_sel_hi:[1,0]
	s_nop 0
	v_pk_mul_f32 v[90:91], v[6:7], v[90:91]
	v_pk_mul_f32 v[92:93], v[92:93], v[110:111] op_sel_hi:[1,0]
	v_med3_f32 v90, v90, s2, v109
	v_med3_f32 v91, v91, s2, v109
	v_cvt_pk_fp8_f32 v94, v90, v91
	v_pk_mul_f32 v[90:91], v[8:9], v[92:93]
	v_pk_mul_f32 v[86:87], v[86:87], v[110:111] op_sel_hi:[1,0]
	v_med3_f32 v90, v90, s2, v109
	v_med3_f32 v91, v91, s2, v109
	v_pk_mul_f32 v[86:87], v[10:11], v[86:87]
	v_cvt_pk_fp8_f32 v94, v90, v91 op_sel:[0,0,1]
	v_med3_f32 v86, v86, s2, v109
	v_med3_f32 v87, v87, s2, v109
	v_cvt_pk_fp8_f32 v90, v86, v87
	v_pk_mul_f32 v[88:89], v[88:89], v[110:111] op_sel_hi:[1,0]
	v_pk_mul_f32 v[82:83], v[82:83], v[110:111] op_sel_hi:[1,0]
	v_pk_mul_f32 v[86:87], v[12:13], v[88:89]
	v_pk_mul_f32 v[82:83], v[14:15], v[82:83]
	v_med3_f32 v86, v86, s2, v109
	v_med3_f32 v87, v87, s2, v109
	v_cvt_pk_fp8_f32 v90, v86, v87 op_sel:[0,0,1]
	v_med3_f32 v82, v82, s2, v109
	v_med3_f32 v83, v83, s2, v109
	v_cvt_pk_fp8_f32 v86, v82, v83
	v_pk_mul_f32 v[84:85], v[84:85], v[110:111] op_sel_hi:[1,0]
	v_pk_mul_f32 v[78:79], v[78:79], v[110:111] op_sel_hi:[1,0]
	v_pk_mul_f32 v[82:83], v[16:17], v[84:85]
	v_pk_mul_f32 v[78:79], v[18:19], v[78:79]
	v_med3_f32 v82, v82, s2, v109
	v_med3_f32 v83, v83, s2, v109
	v_cvt_pk_fp8_f32 v86, v82, v83 op_sel:[0,0,1]
	v_med3_f32 v78, v78, s2, v109
	v_med3_f32 v79, v79, s2, v109
	v_cvt_pk_fp8_f32 v82, v78, v79
	v_pk_mul_f32 v[80:81], v[80:81], v[110:111] op_sel_hi:[1,0]
	v_pk_mul_f32 v[42:43], v[42:43], v[110:111] op_sel_hi:[1,0]
	v_pk_mul_f32 v[78:79], v[20:21], v[80:81]
	v_pk_mul_f32 v[42:43], v[22:23], v[42:43]
	v_med3_f32 v78, v78, s2, v109
	v_med3_f32 v79, v79, s2, v109
	v_cvt_pk_fp8_f32 v82, v78, v79 op_sel:[0,0,1]
	v_med3_f32 v42, v42, s2, v109
	v_med3_f32 v43, v43, s2, v109
	v_cvt_pk_fp8_f32 v78, v42, v43
	v_pk_mul_f32 v[44:45], v[44:45], v[110:111] op_sel_hi:[1,0]
	v_pk_mul_f32 v[38:39], v[38:39], v[110:111] op_sel_hi:[1,0]
	v_pk_mul_f32 v[42:43], v[24:25], v[44:45]
	v_pk_mul_f32 v[38:39], v[26:27], v[38:39]
	v_med3_f32 v42, v42, s2, v109
	v_med3_f32 v43, v43, s2, v109
	v_cvt_pk_fp8_f32 v78, v42, v43 op_sel:[0,0,1]
	v_med3_f32 v38, v38, s2, v109
	v_med3_f32 v39, v39, s2, v109
	v_cvt_pk_fp8_f32 v42, v38, v39
	v_pk_mul_f32 v[40:41], v[40:41], v[110:111] op_sel_hi:[1,0]
	v_pk_mul_f32 v[34:35], v[34:35], v[110:111] op_sel_hi:[1,0]
	v_pk_mul_f32 v[38:39], v[28:29], v[40:41]
	v_pk_mul_f32 v[34:35], v[30:31], v[34:35]
	v_med3_f32 v38, v38, s2, v109
	v_med3_f32 v39, v39, s2, v109
	v_cvt_pk_fp8_f32 v42, v38, v39 op_sel:[0,0,1]
	v_med3_f32 v34, v34, s2, v109
	v_med3_f32 v35, v35, s2, v109
	v_cvt_pk_fp8_f32 v38, v34, v35
	v_pk_mul_f32 v[36:37], v[36:37], v[110:111] op_sel_hi:[1,0]
	global_store_dword v[98:99], v111, off
	global_store_dword v[98:99], v94, off offset:256
	global_store_dword v[98:99], v90, off offset:512
	global_store_dword v[98:99], v86, off offset:768
	v_pk_mul_f32 v[34:35], v[32:33], v[36:37]
	s_waitcnt vmcnt(9)
	v_mov_b64_e32 v[88:89], v[68:69]
	v_med3_f32 v34, v34, s2, v109
	v_med3_f32 v35, v35, s2, v109
	v_cvt_pk_fp8_f32 v38, v34, v35 op_sel:[0,0,1]
	global_store_dword v[98:99], v82, off offset:1024
	global_store_dword v[98:99], v78, off offset:1280
	global_store_dword v[98:99], v42, off offset:1536
	global_store_dword v[98:99], v38, off offset:1792
	s_waitcnt vmcnt(8)
	v_mov_b64_e32 v[34:35], v[46:47]
	v_mov_b64_e32 v[38:39], v[50:51]
	v_mov_b64_e32 v[42:43], v[54:55]
	v_mov_b64_e32 v[80:81], v[60:61]
	v_mov_b64_e32 v[84:85], v[64:65]
	v_mov_b64_e32 v[92:93], v[72:73]
	v_mov_b64_e32 v[96:97], v[76:77]
	v_lshl_add_u64 v[98:99], v[98:99], 0, s[8:9]
	v_mov_b64_e32 v[36:37], v[48:49]
	v_mov_b64_e32 v[40:41], v[52:53]
	v_mov_b64_e32 v[44:45], v[56:57]
	v_mov_b64_e32 v[78:79], v[58:59]
	v_mov_b64_e32 v[82:83], v[62:63]
	v_mov_b64_e32 v[86:87], v[66:67]
	v_mov_b64_e32 v[90:91], v[70:71]
	v_mov_b64_e32 v[94:95], v[74:75]
	s_cbranch_vccz .LBB0_921

.LBB0_975:
	s_mov_b64 s[14:15], 0x8000
	s_add_i32 m0, s55, 0x18000
	v_lshl_add_u64 v[12:13], v[2:3], 0, s[14:15]
	s_mov_b64 s[16:17], 0xa000
	s_waitcnt vmcnt(2)
	s_barrier
	global_load_lds_dwordx4 v[12:13], off
	v_lshl_add_u64 v[12:13], v[2:3], 0, s[16:17]
	s_add_i32 m0, s55, 0x1a000
	s_mov_b64 s[18:19], 0x80
	s_add_i32 s67, s55, 0x8000
	global_load_lds_dwordx4 v[12:13], off
	v_lshl_add_u64 v[4:5], v[4:5], 0, s[18:19]
	s_mov_b32 m0, s67
	s_add_i32 s68, s55, 0xa000
	global_load_lds_dwordx4 v[4:5], off
	v_lshl_add_u64 v[4:5], v[6:7], 0, s[18:19]
	s_mov_b32 m0, s68
	s_mov_b64 s[20:21], 0xc000
	global_load_lds_dwordx4 v[4:5], off
	s_add_i32 m0, s55, 0x1c000
	v_lshl_add_u64 v[4:5], v[2:3], 0, s[20:21]
	s_mov_b64 s[22:23], 0xe000
	global_load_lds_dwordx4 v[4:5], off
	v_lshl_add_u64 v[2:3], v[2:3], 0, s[22:23]
	s_add_i32 m0, s55, 0x1e000
	s_sext_i32_i8 s2, s0
	global_load_lds_dwordx4 v[2:3], off
	v_lshrrev_b32_e32 v3, 1, v0
	v_and_b32_e32 v3, 24, v3
	v_and_b32_e32 v2, 15, v0
	v_lshlrev_b32_e32 v4, 1, v3
	v_lshlrev_b32_e32 v5, 6, v0
	s_movk_i32 s0, 0x3c0
	v_lshlrev_b32_e32 v6, 2, v0
	v_and_or_b32 v5, v5, s0, v4
	v_and_b32_e32 v6, 32, v6
	v_lshl_or_b32 v182, s25, 6, v2
	s_lshl_b32 s0, s25, 13
	v_lshl_or_b32 v2, v2, 6, v4
	v_bitop3_b32 v2, v2, s0, v6 bitop3:0xde
	s_lshl_b32 s0, s24, 5
	s_and_b32 s0, s0, 0x60
	v_or_b32_e32 v184, s0, v3
	v_lshlrev_b32_e32 v3, 8, v0
	v_and_b32_e32 v3, 0x18000, v3
	v_lshlrev_b32_e32 v4, 11, v10
	v_or3_b32 v3, v8, v3, v4
	s_ashr_i32 s69, s34, 31
	s_lshl_b32 s24, s0, 7
	v_add_u32_e32 v168, v3, v9
	v_lshlrev_b32_e32 v3, 4, v11
	s_waitcnt vmcnt(6)
	s_cmpk_lt_u32 s1, 0x100
	v_and_b32_e32 v3, 0x38000, v3
	v_bitop3_b32 v183, s24, v5, v6 bitop3:0xf6
	s_cselect_b64 s[24:25], -1, 0
	v_or3_b32 v3, v8, v3, v4
	s_add_i32 s70, 0, 0x10000
	s_add_i32 s71, 0, 0x14000
	v_mov_b32_e32 v169, v163
	v_add_u32_e32 v170, v3, v9
	v_mov_b32_e32 v171, v163
	v_mov_b64_e32 v[172:173], 0x400
	v_mov_b64_e32 v[174:175], 0x3ff
	v_add_u32_e32 v185, s70, v183
	v_add_u32_e32 v186, s71, v183
	v_add_u32_e32 v187, 0, v2
	v_mov_b32_e32 v188, 0x79797979
	v_mov_b32_e32 v189, 0x7f7f7f7f
	v_mov_b32_e32 v190, 0x3db504f3
	s_barrier
	v_mov_b32_e32 v251, 0
	global_load_dword v250, v251, s[28:29]
	global_load_dword v250, v251, s[28:29]
	global_load_dword v250, v251, s[28:29]
	global_load_dword v250, v251, s[28:29]
	global_load_dword v250, v251, s[28:29]
	global_load_dword v250, v251, s[28:29]
	global_load_dword v250, v251, s[28:29]
	global_load_dword v250, v251, s[28:29]
	global_load_dword v250, v251, s[28:29]
	global_load_dword v250, v251, s[28:29]
	global_load_dword v250, v251, s[28:29]
	global_load_dword v250, v251, s[28:29]
	global_load_dword v250, v251, s[28:29]
	global_load_dword v250, v251, s[28:29]
	global_load_dword v250, v251, s[28:29]
	global_load_dword v250, v251, s[28:29]
	s_branch .LBB0_978

.LBB0_984:
	s_ashr_i32 s45, s44, 31
	s_lshl_b64 s[26:27], s[44:45], 19
	v_readlane_b32 s50, v254, 56
	v_readlane_b32 s51, v254, 57
	s_add_u32 s50, s50, s26
	s_addc_u32 s51, s51, s27
	s_and_b64 s[26:27], s[0:1], exec
	s_cselect_b32 s45, s51, s59
	s_cselect_b32 s72, s50, s58
	s_ashr_i32 s41, s40, 31
	s_lshl_b64 s[26:27], s[40:41], 19
	s_add_u32 s52, s3, s26
	s_addc_u32 s53, s33, s27
	s_and_b64 s[26:27], s[0:1], exec
	s_cselect_b32 s41, s53, s57
	s_cselect_b32 s73, s52, s56
	s_add_u32 s74, s56, 0x10000
	s_addc_u32 s75, s57, 0
	s_add_u32 s56, s58, 0x40080
	s_addc_u32 s57, s59, 0
	s_mov_b32 s80, -2
	ds_read_b128 v[26:29], v185
	ds_read_b128 v[30:33], v185 offset:1024
	ds_read_b128 v[18:21], v185 offset:2048
	ds_read_b128 v[22:25], v185 offset:3072
	ds_read_b128 v[10:13], v186
	ds_read_b128 v[14:17], v186 offset:1024
	ds_read_b128 v[2:5], v186 offset:2048
	ds_read_b128 v[6:9], v186 offset:3072
	s_add_u32 s26, s56, 0xfffc0080
	s_addc_u32 s27, s57, -1
	s_cmp_eq_u32 s80, 12
	s_cselect_b32 s59, s45, s27
	s_cselect_b32 s58, s72, s26
	s_cselect_b32 s61, s41, s75
	s_cselect_b32 s60, s73, s74
	v_lshl_add_u64 v[176:177], s[56:57], 0, v[168:169]
	s_add_i32 m0, s55, 0xc000
	ds_read_b128 v[192:195], v187
	ds_read_b128 v[196:199], v187 offset:1024
	ds_read_b128 v[200:203], v187 offset:2048
	ds_read_b128 v[204:207], v187 offset:3072
	ds_read_b128 v[208:211], v187 offset:4096
	ds_read_b128 v[212:215], v187 offset:5120
	ds_read_b128 v[220:223], v187 offset:6144
	ds_read_b128 v[224:227], v187 offset:7168
	global_load_lds_dwordx4 v[176:177], off
	v_lshl_add_u64 v[176:177], s[56:57], 0, v[170:171]
	s_add_i32 m0, s55, 0xe000
	s_nop 0
	global_load_lds_dwordx4 v[176:177], off
	s_waitcnt vmcnt(24)
	s_waitcnt lgkmcnt(0)
	s_barrier
	s_waitcnt lgkmcnt(0)
	v_mfma_scale_f32_16x16x128_f8f6f4 v[158:161], v[26:33], v[192:199], 0, v188, v189 op_sel_hi:[0,0,0]
	v_mfma_scale_f32_16x16x128_f8f6f4 v[154:157], v[18:25], v[192:199], 0, v188, v189 op_sel_hi:[0,0,0]
	v_mfma_scale_f32_16x16x128_f8f6f4 v[146:149], v[26:33], v[200:207], 0, v188, v189 op_sel_hi:[0,0,0]
	v_mfma_scale_f32_16x16x128_f8f6f4 v[138:141], v[18:25], v[200:207], 0, v188, v189 op_sel_hi:[0,0,0]
	v_mfma_scale_f32_16x16x128_f8f6f4 v[130:133], v[26:33], v[208:215], 0, v188, v189 op_sel_hi:[0,0,0]
	v_mfma_scale_f32_16x16x128_f8f6f4 v[122:125], v[18:25], v[208:215], 0, v188, v189 op_sel_hi:[0,0,0]
	v_mfma_scale_f32_16x16x128_f8f6f4 v[114:117], v[26:33], v[220:227], 0, v188, v189 op_sel_hi:[0,0,0]
	v_mfma_scale_f32_16x16x128_f8f6f4 v[106:109], v[18:25], v[220:227], 0, v188, v189 op_sel_hi:[0,0,0]
	v_mfma_scale_f32_16x16x128_f8f6f4 v[150:153], v[10:17], v[192:199], 0, v188, v189 op_sel_hi:[0,0,0]
	v_mfma_scale_f32_16x16x128_f8f6f4 v[142:145], v[2:9], v[192:199], 0, v188, v189 op_sel_hi:[0,0,0]
	v_mfma_scale_f32_16x16x128_f8f6f4 v[134:137], v[10:17], v[200:207], 0, v188, v189 op_sel_hi:[0,0,0]
	v_mfma_scale_f32_16x16x128_f8f6f4 v[126:129], v[2:9], v[200:207], 0, v188, v189 op_sel_hi:[0,0,0]
	v_mfma_scale_f32_16x16x128_f8f6f4 v[118:121], v[10:17], v[208:215], 0, v188, v189 op_sel_hi:[0,0,0]
	v_mfma_scale_f32_16x16x128_f8f6f4 v[110:113], v[2:9], v[208:215], 0, v188, v189 op_sel_hi:[0,0,0]
	v_mfma_scale_f32_16x16x128_f8f6f4 v[102:105], v[10:17], v[220:227], 0, v188, v189 op_sel_hi:[0,0,0]
	v_mfma_scale_f32_16x16x128_f8f6f4 v[98:101], v[2:9], v[220:227], 0, v188, v189 op_sel_hi:[0,0,0]
	s_barrier
	s_add_i32 s26, s70, s35
	v_lshl_add_u64 v[176:177], s[60:61], 0, v[162:163]
	s_mov_b32 m0, s26
	ds_read_b128 v[192:195], v187 offset:16384
	ds_read_b128 v[196:199], v187 offset:17408
	ds_read_b128 v[200:203], v187 offset:18432
	ds_read_b128 v[204:207], v187 offset:19456
	ds_read_b128 v[208:211], v187 offset:20480
	ds_read_b128 v[212:215], v187 offset:21504
	ds_read_b128 v[220:223], v187 offset:22528
	ds_read_b128 v[224:227], v187 offset:23552
	global_load_lds_dwordx4 v[176:177], off
	v_lshl_add_u64 v[178:179], v[176:177], 0, s[6:7]
	s_add_i32 m0, s26, 0x2000
	s_add_i32 s26, s71, s35
	global_load_lds_dwordx4 v[178:179], off
	v_lshl_add_u64 v[178:179], v[176:177], 0, s[8:9]
	s_mov_b32 m0, s26
	v_lshl_add_u64 v[180:181], s[58:59], 0, v[166:167]
	global_load_lds_dwordx4 v[178:179], off
	v_lshl_add_u64 v[178:179], v[176:177], 0, s[10:11]
	s_add_i32 m0, s26, 0x2000
	s_nop 0
	global_load_lds_dwordx4 v[178:179], off
	v_lshl_add_u64 v[178:179], s[58:59], 0, v[164:165]
	s_mov_b32 m0, s55
	s_nop 0
	global_load_lds_dwordx4 v[178:179], off
	s_mov_b32 m0, s63
	s_nop 0
	global_load_lds_dwordx4 v[180:181], off
	s_waitcnt vmcnt(24)
	s_waitcnt lgkmcnt(0)
	s_barrier
	s_waitcnt lgkmcnt(0)
	v_mfma_scale_f32_16x16x128_f8f6f4 v[94:97], v[26:33], v[192:199], 0, v188, v189 op_sel_hi:[0,0,0]
	v_mfma_scale_f32_16x16x128_f8f6f4 v[90:93], v[18:25], v[192:199], 0, v188, v189 op_sel_hi:[0,0,0]
	v_mfma_scale_f32_16x16x128_f8f6f4 v[82:85], v[26:33], v[200:207], 0, v188, v189 op_sel_hi:[0,0,0]
	v_mfma_scale_f32_16x16x128_f8f6f4 v[74:77], v[18:25], v[200:207], 0, v188, v189 op_sel_hi:[0,0,0]
	v_mfma_scale_f32_16x16x128_f8f6f4 v[66:69], v[26:33], v[208:215], 0, v188, v189 op_sel_hi:[0,0,0]
	v_mfma_scale_f32_16x16x128_f8f6f4 v[58:61], v[18:25], v[208:215], 0, v188, v189 op_sel_hi:[0,0,0]
	v_mfma_scale_f32_16x16x128_f8f6f4 v[50:53], v[26:33], v[220:227], 0, v188, v189 op_sel_hi:[0,0,0]
	v_mfma_scale_f32_16x16x128_f8f6f4 v[42:45], v[18:25], v[220:227], 0, v188, v189 op_sel_hi:[0,0,0]
	v_mfma_scale_f32_16x16x128_f8f6f4 v[86:89], v[10:17], v[192:199], 0, v188, v189 op_sel_hi:[0,0,0]
	v_mfma_scale_f32_16x16x128_f8f6f4 v[78:81], v[2:9], v[192:199], 0, v188, v189 op_sel_hi:[0,0,0]
	v_mfma_scale_f32_16x16x128_f8f6f4 v[70:73], v[10:17], v[200:207], 0, v188, v189 op_sel_hi:[0,0,0]
	v_mfma_scale_f32_16x16x128_f8f6f4 v[62:65], v[2:9], v[200:207], 0, v188, v189 op_sel_hi:[0,0,0]
	v_mfma_scale_f32_16x16x128_f8f6f4 v[54:57], v[10:17], v[208:215], 0, v188, v189 op_sel_hi:[0,0,0]
	v_mfma_scale_f32_16x16x128_f8f6f4 v[46:49], v[2:9], v[208:215], 0, v188, v189 op_sel_hi:[0,0,0]
	v_mfma_scale_f32_16x16x128_f8f6f4 v[38:41], v[10:17], v[220:227], 0, v188, v189 op_sel_hi:[0,0,0]
	v_mfma_scale_f32_16x16x128_f8f6f4 v[34:37], v[2:9], v[220:227], 0, v188, v189 op_sel_hi:[0,0,0]
	s_barrier
	s_add_i32 s60, 0, 0x18000
	s_add_i32 s61, 0, 0x1c000
	v_add_u32_e32 v14, s60, v183
	v_add_u32_e32 v30, s61, v183
	ds_read_b128 v[2:5], v14
	ds_read_b128 v[6:9], v14 offset:1024
	ds_read_b128 v[10:13], v14 offset:2048
	ds_read_b128 v[14:17], v14 offset:3072
	ds_read_b128 v[18:21], v30
	ds_read_b128 v[22:25], v30 offset:1024
	ds_read_b128 v[26:29], v30 offset:2048
	ds_read_b128 v[30:33], v30 offset:3072
	s_add_u32 s26, s58, 0x40000
	s_addc_u32 s27, s59, 0
	s_mov_b32 m0, s64
	v_lshl_add_u64 v[216:217], s[26:27], 0, v[164:165]
	ds_read_b128 v[192:195], v187 offset:32768
	ds_read_b128 v[196:199], v187 offset:33792
	ds_read_b128 v[200:203], v187 offset:34816
	ds_read_b128 v[204:207], v187 offset:35840
	ds_read_b128 v[208:211], v187 offset:36864
	ds_read_b128 v[212:215], v187 offset:37888
	ds_read_b128 v[220:223], v187 offset:38912
	ds_read_b128 v[224:227], v187 offset:39936
	global_load_lds_dwordx4 v[216:217], off
	v_lshl_add_u64 v[216:217], s[26:27], 0, v[166:167]
	s_mov_b32 m0, s65
	s_nop 0
	global_load_lds_dwordx4 v[216:217], off
	s_waitcnt vmcnt(8)
	s_waitcnt lgkmcnt(0)
	s_barrier
	s_waitcnt lgkmcnt(0)
	v_mfma_scale_f32_16x16x128_f8f6f4 v[158:161], v[2:9], v[192:199], v[158:161], v188, v189 op_sel_hi:[0,0,0]
	v_mfma_scale_f32_16x16x128_f8f6f4 v[154:157], v[10:17], v[192:199], v[154:157], v188, v189 op_sel_hi:[0,0,0]
	v_mfma_scale_f32_16x16x128_f8f6f4 v[146:149], v[2:9], v[200:207], v[146:149], v188, v189 op_sel_hi:[0,0,0]
	v_mfma_scale_f32_16x16x128_f8f6f4 v[138:141], v[10:17], v[200:207], v[138:141], v188, v189 op_sel_hi:[0,0,0]
	v_mfma_scale_f32_16x16x128_f8f6f4 v[130:133], v[2:9], v[208:215], v[130:133], v188, v189 op_sel_hi:[0,0,0]
	v_mfma_scale_f32_16x16x128_f8f6f4 v[122:125], v[10:17], v[208:215], v[122:125], v188, v189 op_sel_hi:[0,0,0]
	v_mfma_scale_f32_16x16x128_f8f6f4 v[114:117], v[2:9], v[220:227], v[114:117], v188, v189 op_sel_hi:[0,0,0]
	v_mfma_scale_f32_16x16x128_f8f6f4 v[106:109], v[10:17], v[220:227], v[106:109], v188, v189 op_sel_hi:[0,0,0]
	v_mfma_scale_f32_16x16x128_f8f6f4 v[150:153], v[18:25], v[192:199], v[150:153], v188, v189 op_sel_hi:[0,0,0]
	v_mfma_scale_f32_16x16x128_f8f6f4 v[142:145], v[26:33], v[192:199], v[142:145], v188, v189 op_sel_hi:[0,0,0]
	v_mfma_scale_f32_16x16x128_f8f6f4 v[134:137], v[18:25], v[200:207], v[134:137], v188, v189 op_sel_hi:[0,0,0]
	v_mfma_scale_f32_16x16x128_f8f6f4 v[126:129], v[26:33], v[200:207], v[126:129], v188, v189 op_sel_hi:[0,0,0]
	v_mfma_scale_f32_16x16x128_f8f6f4 v[118:121], v[18:25], v[208:215], v[118:121], v188, v189 op_sel_hi:[0,0,0]
	v_mfma_scale_f32_16x16x128_f8f6f4 v[110:113], v[26:33], v[208:215], v[110:113], v188, v189 op_sel_hi:[0,0,0]
	v_mfma_scale_f32_16x16x128_f8f6f4 v[102:105], v[18:25], v[220:227], v[102:105], v188, v189 op_sel_hi:[0,0,0]
	v_mfma_scale_f32_16x16x128_f8f6f4 v[98:101], v[26:33], v[220:227], v[98:101], v188, v189 op_sel_hi:[0,0,0]
	s_barrier
	s_add_i32 s26, s60, s35
	v_lshl_add_u64 v[216:217], v[176:177], 0, s[14:15]
	s_mov_b32 m0, s26
	ds_read_b128 v[192:195], v187 offset:49152
	ds_read_b128 v[196:199], v187 offset:50176
	ds_read_b128 v[200:203], v187 offset:51200
	ds_read_b128 v[204:207], v187 offset:52224
	ds_read_b128 v[208:211], v187 offset:53248
	ds_read_b128 v[212:215], v187 offset:54272
	ds_read_b128 v[220:223], v187 offset:55296
	ds_read_b128 v[224:227], v187 offset:56320
	global_load_lds_dwordx4 v[216:217], off
	v_lshl_add_u64 v[216:217], v[176:177], 0, s[16:17]
	s_add_i32 m0, s26, 0x2000
	s_add_i32 s26, s61, s35
	global_load_lds_dwordx4 v[216:217], off
	v_lshl_add_u64 v[216:217], v[176:177], 0, s[20:21]
	s_mov_b32 m0, s26
	v_lshl_add_u64 v[176:177], v[176:177], 0, s[22:23]
	global_load_lds_dwordx4 v[216:217], off
	s_add_i32 m0, s26, 0x2000
	s_nop 0
	global_load_lds_dwordx4 v[176:177], off
	v_lshl_add_u64 v[176:177], v[178:179], 0, s[18:19]
	s_mov_b32 m0, s67
	s_nop 0
	global_load_lds_dwordx4 v[176:177], off
	v_lshl_add_u64 v[176:177], v[180:181], 0, s[18:19]
	s_mov_b32 m0, s68
	s_nop 0
	global_load_lds_dwordx4 v[176:177], off
	s_waitcnt vmcnt(8)
	s_waitcnt lgkmcnt(0)
	s_barrier
	s_waitcnt lgkmcnt(0)
	v_mfma_scale_f32_16x16x128_f8f6f4 v[94:97], v[2:9], v[192:199], v[94:97], v188, v189 op_sel_hi:[0,0,0]
	v_mfma_scale_f32_16x16x128_f8f6f4 v[90:93], v[10:17], v[192:199], v[90:93], v188, v189 op_sel_hi:[0,0,0]
	v_mfma_scale_f32_16x16x128_f8f6f4 v[82:85], v[2:9], v[200:207], v[82:85], v188, v189 op_sel_hi:[0,0,0]
	v_mfma_scale_f32_16x16x128_f8f6f4 v[74:77], v[10:17], v[200:207], v[74:77], v188, v189 op_sel_hi:[0,0,0]
	v_mfma_scale_f32_16x16x128_f8f6f4 v[66:69], v[2:9], v[208:215], v[66:69], v188, v189 op_sel_hi:[0,0,0]
	v_mfma_scale_f32_16x16x128_f8f6f4 v[58:61], v[10:17], v[208:215], v[58:61], v188, v189 op_sel_hi:[0,0,0]
	v_mfma_scale_f32_16x16x128_f8f6f4 v[50:53], v[2:9], v[220:227], v[50:53], v188, v189 op_sel_hi:[0,0,0]
	v_mfma_scale_f32_16x16x128_f8f6f4 v[42:45], v[10:17], v[220:227], v[42:45], v188, v189 op_sel_hi:[0,0,0]
	v_mfma_scale_f32_16x16x128_f8f6f4 v[86:89], v[18:25], v[192:199], v[86:89], v188, v189 op_sel_hi:[0,0,0]
	v_mfma_scale_f32_16x16x128_f8f6f4 v[78:81], v[26:33], v[192:199], v[78:81], v188, v189 op_sel_hi:[0,0,0]
	v_mfma_scale_f32_16x16x128_f8f6f4 v[70:73], v[18:25], v[200:207], v[70:73], v188, v189 op_sel_hi:[0,0,0]
	v_mfma_scale_f32_16x16x128_f8f6f4 v[62:65], v[26:33], v[200:207], v[62:65], v188, v189 op_sel_hi:[0,0,0]
	v_mfma_scale_f32_16x16x128_f8f6f4 v[54:57], v[18:25], v[208:215], v[54:57], v188, v189 op_sel_hi:[0,0,0]
	v_mfma_scale_f32_16x16x128_f8f6f4 v[46:49], v[26:33], v[208:215], v[46:49], v188, v189 op_sel_hi:[0,0,0]
	v_mfma_scale_f32_16x16x128_f8f6f4 v[38:41], v[18:25], v[220:227], v[38:41], v188, v189 op_sel_hi:[0,0,0]
	v_mfma_scale_f32_16x16x128_f8f6f4 v[34:37], v[26:33], v[220:227], v[34:37], v188, v189 op_sel_hi:[0,0,0]
	s_barrier
	s_add_i32 s80, s80, 2
	s_add_u32 s74, s74, 0x10000
	s_addc_u32 s75, s75, 0
	s_add_u32 s56, s56, 0x100
	s_addc_u32 s57, s57, 0
	s_cmp_gt_u32 s80, 13

.LBB0_1344:
	s_add_i32 s2, s50, s58
	s_add_i32 s12, s2, 2
	s_ashr_i32 s13, s12, 31
	s_lshl_b64 s[14:15], s[12:13], 13
	v_lshl_add_u64 v[34:35], v[54:55], 0, s[14:15]
	global_load_dwordx4 v[56:59], v[34:35], off
	global_load_dwordx4 v[60:63], v[34:35], off offset:1024
	global_load_dwordx4 v[64:67], v[34:35], off offset:2048
	global_load_dwordx4 v[68:71], v[34:35], off offset:3072
	v_add_co_u32_e32 v42, vcc, s3, v34
	s_lshl_b64 s[12:13], s[12:13], 11
	s_nop 0
	v_addc_co_u32_e32 v43, vcc, 0, v35, vcc
	global_load_dwordx4 v[38:41], v[42:43], off
	global_load_dwordx4 v[46:49], v[42:43], off offset:1024
	global_load_dwordx4 v[34:37], v[42:43], off offset:3072
	s_nop 0
	global_load_dwordx4 v[42:45], v[42:43], off offset:2048
	v_cmp_lt_i32_e32 vcc, v108, v107
	s_waitcnt vmcnt(7)
	v_mov_b32_e32 v74, v57
	v_cndmask_b32_e32 v72, v106, v108, vcc
	s_waitcnt vmcnt(6)
	v_mov_b32_e32 v75, v61
	v_mov_b32_e32 v78, v59
	v_mov_b32_e32 v79, v63
	v_lshlrev_b32_e32 v118, 2, v72
	v_mov_b32_e32 v72, v56
	v_mov_b32_e32 v73, v60
	v_mov_b32_e32 v76, v58
	v_mov_b32_e32 v77, v62
	s_waitcnt vmcnt(5)
	v_pk_mul_f32 v[80:81], v[66:67], v[66:67]
	v_pk_mul_f32 v[82:83], v[64:65], v[64:65]
	v_pk_mul_f32 v[74:75], v[74:75], v[74:75]
	v_pk_mul_f32 v[78:79], v[78:79], v[78:79]
	v_pk_mov_b32 v[88:89], v[82:83], v[80:81] op_sel:[1,0]
	v_mov_b32_e32 v83, v81
	v_pk_fma_f32 v[72:73], v[72:73], v[72:73], v[74:75]
	v_pk_fma_f32 v[74:75], v[76:77], v[76:77], v[78:79]
	s_waitcnt vmcnt(4)
	v_mul_f32_e32 v84, v69, v69
	v_mul_f32_e32 v86, v71, v71
	v_pk_add_f32 v[76:77], v[88:89], v[82:83]
	v_pk_add_f32 v[72:73], v[72:73], v[74:75]
	s_waitcnt vmcnt(3)
	v_mul_f32_e32 v93, v38, v38
	v_mul_f32_e32 v95, v39, v39
	v_mul_f32_e32 v96, v40, v40
	v_mul_f32_e32 v97, v41, v41
	v_pk_fma_f32 v[80:81], v[68:69], v[68:69], v[84:85] op_sel_hi:[1,1,0]
	v_pk_fma_f32 v[84:85], v[70:71], v[70:71], v[86:87] op_sel_hi:[1,1,0]
	v_pk_add_f32 v[74:75], v[76:77], v[76:77] op_sel:[0,1] op_sel_hi:[1,0]
	v_pk_add_f32 v[72:73], v[72:73], v[72:73] op_sel:[0,1] op_sel_hi:[1,0]
	s_waitcnt vmcnt(2)
	v_pk_mul_f32 v[86:87], v[48:49], v[48:49]
	v_pk_mul_f32 v[90:91], v[46:47], v[46:47]
	v_mov_b32_e32 v81, v96
	v_mov_b32_e32 v85, v97
	v_mov_b32_e32 v75, v95
	v_mov_b32_e32 v73, v93
	v_pk_mov_b32 v[78:79], v[90:91], v[86:87] op_sel:[1,0]
	v_mov_b32_e32 v91, v87
	v_pk_add_f32 v[76:77], v[80:81], v[84:85]
	v_pk_add_f32 v[72:73], v[72:73], v[74:75]
	s_waitcnt vmcnt(0)
	v_mul_f32_e32 v92, v43, v43
	v_mul_f32_e32 v94, v45, v45
	v_pk_add_f32 v[78:79], v[78:79], v[90:91]
	v_pk_add_f32 v[72:73], v[72:73], v[76:77]
	v_mul_f32_e32 v98, v34, v34
	v_mul_f32_e32 v99, v35, v35
	v_mul_f32_e32 v100, v36, v36
	v_mul_f32_e32 v101, v37, v37
	v_pk_fma_f32 v[82:83], v[42:43], v[42:43], v[92:93] op_sel_hi:[1,1,0]
	v_pk_fma_f32 v[86:87], v[44:45], v[44:45], v[94:95] op_sel_hi:[1,1,0]
	v_pk_add_f32 v[78:79], v[78:79], v[78:79] op_sel:[0,1] op_sel_hi:[1,0]
	v_pk_add_f32 v[72:73], v[72:73], v[72:73] op_sel:[0,1] op_sel_hi:[1,0]
	v_mov_b32_e32 v83, v100
	v_mov_b32_e32 v87, v101
	v_mov_b32_e32 v79, v99
	v_mov_b32_e32 v73, v98
	v_pk_add_f32 v[80:81], v[82:83], v[86:87]
	v_pk_add_f32 v[72:73], v[72:73], v[78:79]
	v_cmp_lt_i32_e32 vcc, v109, v107
	v_pk_add_f32 v[72:73], v[72:73], v[80:81]
	v_mov_b32_e32 v79, 0
	v_add_f32_e32 v72, v72, v73
	ds_bpermute_b32 v73, v118, v72
	v_cndmask_b32_e32 v74, v106, v109, vcc
	v_lshlrev_b32_e32 v119, 2, v74
	v_cmp_lt_i32_e32 vcc, v110, v107
	v_mov_b32_e32 v85, 0
	s_waitcnt lgkmcnt(0)
	v_add_f32_e32 v72, v72, v73
	ds_bpermute_b32 v73, v119, v72
	v_cndmask_b32_e32 v74, v106, v110, vcc
	v_lshlrev_b32_e32 v120, 2, v74
	v_cmp_lt_i32_e32 vcc, v111, v107
	v_mov_b32_e32 v84, 0
	s_waitcnt lgkmcnt(0)
	v_add_f32_e32 v72, v72, v73
	ds_bpermute_b32 v73, v120, v72
	v_cndmask_b32_e32 v74, v106, v111, vcc
	v_lshlrev_b32_e32 v121, 2, v74
	v_cmp_lt_i32_e32 vcc, v112, v107
	v_lshl_add_u64 v[76:77], v[52:53], 0, s[12:13]
	s_waitcnt lgkmcnt(0)
	v_add_f32_e32 v72, v72, v73
	ds_bpermute_b32 v73, v121, v72
	v_cndmask_b32_e32 v74, v106, v112, vcc
	v_lshlrev_b32_e32 v122, 2, v74
	v_cmp_lt_i32_e32 vcc, v113, v107
	s_add_i32 s12, s2, 3
	s_waitcnt lgkmcnt(0)
	v_add_f32_e32 v72, v72, v73
	ds_bpermute_b32 v73, v122, v72
	v_cndmask_b32_e32 v74, v106, v113, vcc
	v_lshlrev_b32_e32 v123, 2, v74
	s_ashr_i32 s13, s12, 31
	s_lshl_b64 s[14:15], s[12:13], 13
	s_waitcnt lgkmcnt(0)
	v_add_f32_e32 v72, v72, v73
	ds_bpermute_b32 v73, v123, v72
	s_lshl_b64 s[12:13], s[12:13], 11
	s_waitcnt lgkmcnt(0)
	v_add_f32_e32 v72, v72, v73
	v_fmamk_f32 v72, v72, 0x3a000000, v114
	v_mul_f32_e32 v73, 0x4b800000, v72
	v_cmp_gt_f32_e32 vcc, s52, v72
	s_nop 1
	v_cndmask_b32_e32 v72, v72, v73, vcc
	v_rsq_f32_e32 v72, v72
	s_nop 0
	v_mul_f32_e32 v73, 0x45800000, v72
	v_cndmask_b32_e32 v78, v72, v73, vcc
	v_pk_mul_f32 v[56:57], v[56:57], v[78:79] op_sel_hi:[1,0]
	v_pk_mul_f32 v[64:65], v[64:65], v[78:79] op_sel_hi:[1,0]
	v_pk_mul_f32 v[58:59], v[58:59], v[78:79] op_sel_hi:[1,0]
	v_pk_mul_f32 v[74:75], v[2:3], v[56:57]
	v_pk_mul_f32 v[64:65], v[10:11], v[64:65]
	v_pk_mul_f32 v[72:73], v[4:5], v[58:59]
	v_med3_f32 v58, v74, s53, v115
	v_med3_f32 v59, v75, s53, v115
	v_med3_f32 v86, v64, s53, v115
	v_med3_f32 v87, v65, s53, v115
	v_pk_mul_f32 v[60:61], v[60:61], v[78:79] op_sel_hi:[1,0]
	v_pk_mul_f32 v[62:63], v[62:63], v[78:79] op_sel_hi:[1,0]
	v_pk_mul_f32 v[66:67], v[66:67], v[78:79] op_sel_hi:[1,0]
	v_pk_mul_f32 v[80:81], v[68:69], v[78:79] op_sel_hi:[1,0]
	v_pk_mul_f32 v[82:83], v[70:71], v[78:79] op_sel_hi:[1,0]
	v_cvt_pk_fp8_f32 v79, v58, v59
	v_cvt_pk_fp8_f32 v85, v86, v87
	v_pk_mul_f32 v[70:71], v[6:7], v[60:61]
	v_pk_mul_f32 v[60:61], v[12:13], v[66:67]
	v_med3_f32 v66, v70, s53, v115
	v_med3_f32 v67, v71, s53, v115
	v_pk_mul_f32 v[68:69], v[8:9], v[62:63]
	v_pk_mul_f32 v[56:57], v[14:15], v[80:81]
	v_med3_f32 v62, v72, s53, v115
	v_med3_f32 v63, v73, s53, v115
	v_med3_f32 v88, v60, s53, v115
	v_cvt_pk_fp8_f32 v84, v66, v67
	v_med3_f32 v58, v61, s53, v115
	v_cvt_pk_fp8_f32 v79, v62, v63 op_sel:[0,0,1]
	v_cvt_pk_fp8_f32 v85, v88, v58 op_sel:[0,0,1]
	v_med3_f32 v58, v56, s53, v115
	v_med3_f32 v59, v57, s53, v115
	v_cvt_pk_fp8_f32 v62, v58, v59
	v_med3_f32 v80, v68, s53, v115
	v_med3_f32 v81, v69, s53, v115
	v_cvt_pk_fp8_f32 v84, v80, v81 op_sel:[0,0,1]
	v_pk_mul_f32 v[66:67], v[16:17], v[82:83]
	v_pk_mul_f32 v[38:39], v[38:39], v[78:79] op_sel_hi:[1,0]
	v_med3_f32 v58, v66, s53, v115
	v_med3_f32 v59, v67, s53, v115
	v_cvt_pk_fp8_f32 v62, v58, v59 op_sel:[0,0,1]
	v_pk_mul_f32 v[58:59], v[18:19], v[38:39]
	global_store_dword v[76:77], v79, off
	global_store_dword v[76:77], v84, off offset:256
	global_store_dword v[76:77], v85, off offset:512
	global_store_dword v[76:77], v62, off offset:768
	v_pk_mul_f32 v[40:41], v[40:41], v[78:79] op_sel_hi:[1,0]
	v_med3_f32 v38, v58, s53, v115
	v_med3_f32 v39, v59, s53, v115
	v_cvt_pk_fp8_f32 v79, v38, v39
	v_pk_mul_f32 v[62:63], v[20:21], v[40:41]
	v_med3_f32 v38, v62, s53, v115
	v_med3_f32 v39, v63, s53, v115
	v_cvt_pk_fp8_f32 v79, v38, v39 op_sel:[0,0,1]
	v_lshl_add_u64 v[88:89], v[54:55], 0, s[14:15]
	v_add_co_u32_e32 v92, vcc, s3, v88
	v_pk_mul_f32 v[38:39], v[46:47], v[78:79] op_sel_hi:[1,0]
	v_pk_mul_f32 v[40:41], v[48:49], v[78:79] op_sel_hi:[1,0]
	v_pk_mul_f32 v[46:47], v[22:23], v[38:39]
	v_pk_mul_f32 v[48:49], v[24:25], v[40:41]
	v_med3_f32 v38, v46, s53, v115
	v_med3_f32 v39, v47, s53, v115
	v_cvt_pk_fp8_f32 v80, v38, v39
	v_med3_f32 v38, v48, s53, v115
	v_med3_f32 v39, v49, s53, v115
	v_pk_mul_f32 v[40:41], v[44:45], v[78:79] op_sel_hi:[1,0]
	v_cvt_pk_fp8_f32 v80, v38, v39 op_sel:[0,0,1]
	v_pk_mul_f32 v[38:39], v[42:43], v[78:79] op_sel_hi:[1,0]
	v_pk_mul_f32 v[38:39], v[26:27], v[38:39]
	v_pk_mul_f32 v[40:41], v[28:29], v[40:41]
	v_med3_f32 v42, v38, s53, v115
	v_med3_f32 v43, v39, s53, v115
	v_cvt_pk_fp8_f32 v44, v42, v43
	v_pk_mul_f32 v[34:35], v[34:35], v[78:79] op_sel_hi:[1,0]
	v_med3_f32 v42, v40, s53, v115
	v_med3_f32 v43, v41, s53, v115
	v_pk_mul_f32 v[34:35], v[30:31], v[34:35]
	v_cvt_pk_fp8_f32 v44, v42, v43 op_sel:[0,0,1]
	v_med3_f32 v42, v34, s53, v115
	v_med3_f32 v43, v35, s53, v115
	v_cvt_pk_fp8_f32 v45, v42, v43
	v_pk_mul_f32 v[36:37], v[36:37], v[78:79] op_sel_hi:[1,0]
	v_addc_co_u32_e32 v93, vcc, 0, v89, vcc
	v_pk_mul_f32 v[36:37], v[32:33], v[36:37]
	s_nop 0
	v_med3_f32 v42, v36, s53, v115
	v_med3_f32 v43, v37, s53, v115
	v_cvt_pk_fp8_f32 v45, v42, v43 op_sel:[0,0,1]
	global_store_dword v[76:77], v79, off offset:1024
	global_store_dword v[76:77], v80, off offset:1280
	global_store_dword v[76:77], v44, off offset:1536
	global_store_dword v[76:77], v45, off offset:1792
	global_load_dwordx4 v[42:45], v[88:89], off
	s_nop 0
	global_load_dwordx4 v[76:79], v[88:89], off offset:1024
	global_load_dwordx4 v[80:83], v[88:89], off offset:2048
	global_load_dwordx4 v[84:87], v[92:93], off
	s_nop 0
	global_load_dwordx4 v[88:91], v[88:89], off offset:3072
	s_nop 0
	global_load_dwordx4 v[124:127], v[92:93], off offset:1024
	global_load_dwordx4 v[128:131], v[92:93], off offset:3072
	global_load_dwordx4 v[132:135], v[92:93], off offset:2048
	s_waitcnt vmcnt(7)
	v_mov_b32_e32 v94, v43
	s_waitcnt vmcnt(6)
	v_mov_b32_e32 v95, v77
	v_mov_b32_e32 v98, v45
	v_mov_b32_e32 v99, v79
	v_mov_b32_e32 v92, v42
	v_mov_b32_e32 v93, v76
	v_mov_b32_e32 v96, v44
	v_mov_b32_e32 v97, v78
	v_pk_mul_f32 v[94:95], v[94:95], v[94:95]
	v_pk_mul_f32 v[98:99], v[98:99], v[98:99]
	v_pk_fma_f32 v[92:93], v[92:93], v[92:93], v[94:95]
	v_pk_fma_f32 v[94:95], v[96:97], v[96:97], v[98:99]
	s_waitcnt vmcnt(5)
	v_pk_mul_f32 v[96:97], v[80:81], v[80:81]
	v_pk_add_f32 v[92:93], v[92:93], v[94:95]
	v_pk_mul_f32 v[94:95], v[82:83], v[82:83]
	v_pk_add_f32 v[92:93], v[92:93], v[92:93] op_sel:[0,1] op_sel_hi:[1,0]
	v_pk_mov_b32 v[98:99], v[96:97], v[94:95] op_sel:[1,0]
	v_mov_b32_e32 v97, v95
	v_pk_add_f32 v[94:95], v[98:99], v[96:97]
	s_waitcnt vmcnt(4)
	v_mul_f32_e32 v96, v84, v84
	v_mul_f32_e32 v97, v85, v85
	v_pk_add_f32 v[94:95], v[94:95], v[94:95] op_sel:[0,1] op_sel_hi:[1,0]
	v_mov_b32_e32 v93, v96
	v_mov_b32_e32 v95, v97
	v_pk_add_f32 v[92:93], v[92:93], v[94:95]
	s_waitcnt vmcnt(3)
	v_mul_f32_e32 v94, v89, v89
	v_mul_f32_e32 v96, v91, v91
	v_mul_f32_e32 v98, v86, v86
	v_mul_f32_e32 v99, v87, v87
	v_pk_fma_f32 v[94:95], v[88:89], v[88:89], v[94:95] op_sel_hi:[1,1,0]
	v_pk_fma_f32 v[96:97], v[90:91], v[90:91], v[96:97] op_sel_hi:[1,1,0]
	v_mov_b32_e32 v95, v98
	v_mov_b32_e32 v97, v99
	v_pk_add_f32 v[94:95], v[94:95], v[96:97]
	s_waitcnt vmcnt(2)
	v_pk_mul_f32 v[96:97], v[124:125], v[124:125]
	v_pk_add_f32 v[92:93], v[92:93], v[94:95]
	v_pk_mul_f32 v[94:95], v[126:127], v[126:127]
	v_pk_add_f32 v[92:93], v[92:93], v[92:93] op_sel:[0,1] op_sel_hi:[1,0]
	v_pk_mov_b32 v[98:99], v[96:97], v[94:95] op_sel:[1,0]
	v_mov_b32_e32 v97, v95
	v_pk_add_f32 v[94:95], v[98:99], v[96:97]
	s_waitcnt vmcnt(1)
	v_mul_f32_e32 v96, v128, v128
	v_mul_f32_e32 v97, v129, v129
	v_pk_add_f32 v[94:95], v[94:95], v[94:95] op_sel:[0,1] op_sel_hi:[1,0]
	v_mov_b32_e32 v93, v96
	v_mov_b32_e32 v95, v97
	v_pk_add_f32 v[92:93], v[92:93], v[94:95]
	s_waitcnt vmcnt(0)
	v_mul_f32_e32 v94, v133, v133
	v_mul_f32_e32 v96, v135, v135
	v_mul_f32_e32 v98, v130, v130
	v_mul_f32_e32 v99, v131, v131
	v_pk_fma_f32 v[94:95], v[132:133], v[132:133], v[94:95] op_sel_hi:[1,1,0]
	v_pk_fma_f32 v[96:97], v[134:135], v[134:135], v[96:97] op_sel_hi:[1,1,0]
	v_mov_b32_e32 v95, v98
	v_mov_b32_e32 v97, v99
	v_pk_add_f32 v[94:95], v[94:95], v[96:97]
	s_nop 0
	v_pk_add_f32 v[92:93], v[92:93], v[94:95]
	s_nop 0
	v_add_f32_e32 v92, v92, v93
	ds_bpermute_b32 v93, v118, v92
	s_waitcnt lgkmcnt(0)
	v_add_f32_e32 v92, v92, v93
	ds_bpermute_b32 v93, v119, v92
	s_waitcnt lgkmcnt(0)
	v_add_f32_e32 v92, v92, v93
	ds_bpermute_b32 v93, v120, v92
	s_waitcnt lgkmcnt(0)
	v_add_f32_e32 v92, v92, v93
	ds_bpermute_b32 v93, v121, v92
	s_waitcnt lgkmcnt(0)
	v_add_f32_e32 v92, v92, v93
	ds_bpermute_b32 v93, v122, v92
	s_waitcnt lgkmcnt(0)
	v_add_f32_e32 v92, v92, v93
	ds_bpermute_b32 v93, v123, v92
	s_waitcnt lgkmcnt(0)
	v_add_f32_e32 v92, v92, v93
	v_fmamk_f32 v92, v92, 0x3a000000, v114
	v_mul_f32_e32 v93, 0x4b800000, v92
	v_cmp_gt_f32_e32 vcc, s52, v92
	s_nop 1
	v_cndmask_b32_e32 v92, v92, v93, vcc
	v_rsq_f32_e32 v92, v92
	s_nop 0
	v_mul_f32_e32 v93, 0x45800000, v92
	v_cndmask_b32_e32 v136, v92, v93, vcc
	v_pk_mul_f32 v[44:45], v[44:45], v[136:137] op_sel_hi:[1,0]
	v_pk_mul_f32 v[42:43], v[42:43], v[136:137] op_sel_hi:[1,0]
	v_pk_mul_f32 v[104:105], v[4:5], v[44:45]
	v_pk_mul_f32 v[44:45], v[76:77], v[136:137] op_sel_hi:[1,0]
	v_pk_mul_f32 v[76:77], v[78:79], v[136:137] op_sel_hi:[1,0]
	v_pk_mul_f32 v[102:103], v[6:7], v[44:45]
	v_med3_f32 v44, v102, s53, v115
	v_med3_f32 v45, v103, s53, v115
	v_cvt_pk_fp8_f32 v78, v44, v45
	v_pk_mul_f32 v[100:101], v[2:3], v[42:43]
	v_pk_mul_f32 v[98:99], v[8:9], v[76:77]
	v_med3_f32 v42, v100, s53, v115
	v_med3_f32 v43, v101, s53, v115
	v_med3_f32 v44, v98, s53, v115
	v_med3_f32 v45, v99, s53, v115
	v_cvt_pk_fp8_f32 v92, v42, v43
	v_cvt_pk_fp8_f32 v78, v44, v45 op_sel:[0,0,1]
	v_pk_mul_f32 v[44:45], v[80:81], v[136:137] op_sel_hi:[1,0]
	v_pk_mul_f32 v[94:95], v[10:11], v[44:45]
	v_med3_f32 v42, v104, s53, v115
	v_med3_f32 v44, v94, s53, v115
	v_med3_f32 v45, v95, s53, v115
	v_med3_f32 v43, v105, s53, v115
	v_cvt_pk_fp8_f32 v79, v44, v45
	v_cvt_pk_fp8_f32 v92, v42, v43 op_sel:[0,0,1]
	v_pk_mul_f32 v[76:77], v[82:83], v[136:137] op_sel_hi:[1,0]
	v_lshl_add_u64 v[42:43], v[52:53], 0, s[12:13]
	v_pk_mul_f32 v[96:97], v[12:13], v[76:77]
	global_store_dword v[42:43], v92, off
	v_med3_f32 v44, v96, s53, v115
	v_med3_f32 v45, v97, s53, v115
	v_cvt_pk_fp8_f32 v79, v44, v45 op_sel:[0,0,1]
	v_pk_mul_f32 v[44:45], v[88:89], v[136:137] op_sel_hi:[1,0]
	v_pk_mul_f32 v[92:93], v[14:15], v[44:45]
	v_pk_mul_f32 v[76:77], v[90:91], v[136:137] op_sel_hi:[1,0]
	v_med3_f32 v44, v92, s53, v115
	v_med3_f32 v45, v93, s53, v115
	v_cvt_pk_fp8_f32 v80, v44, v45
	v_pk_mul_f32 v[90:91], v[16:17], v[76:77]
	v_med3_f32 v44, v90, s53, v115
	v_med3_f32 v45, v91, s53, v115
	v_cvt_pk_fp8_f32 v80, v44, v45 op_sel:[0,0,1]
	v_pk_mul_f32 v[44:45], v[84:85], v[136:137] op_sel_hi:[1,0]
	v_pk_mul_f32 v[76:77], v[86:87], v[136:137] op_sel_hi:[1,0]
	v_pk_mul_f32 v[82:83], v[18:19], v[44:45]
	v_pk_mul_f32 v[88:89], v[20:21], v[76:77]
	v_med3_f32 v44, v82, s53, v115
	v_med3_f32 v45, v83, s53, v115
	v_cvt_pk_fp8_f32 v81, v44, v45
	v_med3_f32 v44, v88, s53, v115
	v_med3_f32 v45, v89, s53, v115
	v_pk_mul_f32 v[76:77], v[126:127], v[136:137] op_sel_hi:[1,0]
	v_cvt_pk_fp8_f32 v81, v44, v45 op_sel:[0,0,1]
	v_pk_mul_f32 v[44:45], v[124:125], v[136:137] op_sel_hi:[1,0]
	v_pk_mul_f32 v[86:87], v[22:23], v[44:45]
	v_pk_mul_f32 v[84:85], v[24:25], v[76:77]
	v_med3_f32 v44, v86, s53, v115
	v_med3_f32 v45, v87, s53, v115
	v_cvt_pk_fp8_f32 v124, v44, v45
	v_med3_f32 v44, v84, s53, v115
	v_med3_f32 v45, v85, s53, v115
	global_store_dword v[42:43], v78, off offset:256
	global_store_dword v[42:43], v79, off offset:512
	global_store_dword v[42:43], v80, off offset:768
	global_store_dword v[42:43], v81, off offset:1024
	v_cvt_pk_fp8_f32 v124, v44, v45 op_sel:[0,0,1]
	v_pk_mul_f32 v[44:45], v[132:133], v[136:137] op_sel_hi:[1,0]
	v_pk_mul_f32 v[78:79], v[26:27], v[44:45]
	v_pk_mul_f32 v[76:77], v[134:135], v[136:137] op_sel_hi:[1,0]
	v_med3_f32 v44, v78, s53, v115
	v_med3_f32 v45, v79, s53, v115
	v_cvt_pk_fp8_f32 v125, v44, v45
	v_pk_mul_f32 v[80:81], v[28:29], v[76:77]
	v_pk_mul_f32 v[76:77], v[128:129], v[136:137] op_sel_hi:[1,0]
	v_med3_f32 v44, v80, s53, v115
	v_med3_f32 v45, v81, s53, v115
	v_cvt_pk_fp8_f32 v125, v44, v45 op_sel:[0,0,1]
	v_pk_mul_f32 v[44:45], v[130:131], v[136:137] op_sel_hi:[1,0]
	ds_read_b128 v[128:131], v1
	v_pk_mul_f32 v[76:77], v[30:31], v[76:77]
	v_mov_b32_e32 v126, 0
	v_med3_f32 v127, v76, s53, v115
	v_med3_f32 v132, v77, s53, v115
	v_cvt_pk_fp8_f32 v126, v127, v132
	ds_read_b128 v[132:135], v1 offset:1024
	s_waitcnt lgkmcnt(1)
	v_mul_f32_e32 v127, v75, v129
	v_mul_f32_e32 v129, v101, v129
	v_fmac_f32_e32 v127, v74, v128
	v_fmac_f32_e32 v129, v100, v128
	v_mul_f32_e32 v128, v105, v131
	v_mul_f32_e32 v136, v73, v131
	v_fmac_f32_e32 v128, v104, v130
	v_fmac_f32_e32 v136, v72, v130
	v_add_f32_e32 v128, v129, v128
	v_add_f32_e32 v127, v127, v136
	v_add_f32_e32 v136, 0, v128
	s_waitcnt lgkmcnt(0)
	v_mul_f32_e32 v128, v71, v133
	v_mul_f32_e32 v129, v69, v135
	v_fmac_f32_e32 v128, v70, v132
	v_fmac_f32_e32 v129, v68, v134
	v_add_f32_e32 v127, 0, v127
	v_add_f32_e32 v128, v128, v129
	v_add_f32_e32 v127, v127, v128
	v_mul_f32_e32 v133, v103, v133
	ds_read_b128 v[128:131], v1 offset:2048
	v_fmac_f32_e32 v133, v102, v132
	v_mul_f32_e32 v132, v99, v135
	v_fmac_f32_e32 v132, v98, v134
	v_add_f32_e32 v132, v133, v132
	v_add_f32_e32 v136, v136, v132
	ds_read_b128 v[132:135], v1 offset:3072
	s_waitcnt lgkmcnt(1)
	v_mul_f32_e32 v137, v65, v129
	v_mul_f32_e32 v129, v95, v129
	v_fmac_f32_e32 v137, v64, v128
	v_fmac_f32_e32 v129, v94, v128
	v_mul_f32_e32 v128, v97, v131
	v_fmac_f32_e32 v128, v96, v130
	v_mul_f32_e32 v138, v61, v131
	v_add_f32_e32 v128, v129, v128
	v_fmac_f32_e32 v138, v60, v130
	v_add_f32_e32 v136, v136, v128
	s_waitcnt lgkmcnt(0)
	v_mul_f32_e32 v128, v57, v133
	v_mul_f32_e32 v129, v67, v135
	v_add_f32_e32 v137, v137, v138
	v_fmac_f32_e32 v128, v56, v132
	v_fmac_f32_e32 v129, v66, v134
	v_add_f32_e32 v127, v127, v137
	v_add_f32_e32 v128, v128, v129
	v_add_f32_e32 v127, v127, v128
	v_mul_f32_e32 v133, v93, v133
	ds_read_b128 v[128:131], v1 offset:4096
	v_fmac_f32_e32 v133, v92, v132
	v_mul_f32_e32 v132, v91, v135
	v_fmac_f32_e32 v132, v90, v134
	v_add_f32_e32 v132, v133, v132
	v_add_f32_e32 v136, v136, v132
	ds_read_b128 v[132:135], v1 offset:5120
	s_waitcnt lgkmcnt(1)
	v_mul_f32_e32 v137, v59, v129
	v_mul_f32_e32 v129, v83, v129
	v_fmac_f32_e32 v137, v58, v128
	v_fmac_f32_e32 v129, v82, v128
	v_mul_f32_e32 v128, v89, v131
	v_fmac_f32_e32 v128, v88, v130
	v_mul_f32_e32 v138, v63, v131
	v_add_f32_e32 v128, v129, v128
	v_fmac_f32_e32 v138, v62, v130
	v_add_f32_e32 v136, v136, v128
	s_waitcnt lgkmcnt(0)
	v_mul_f32_e32 v128, v47, v133
	v_mul_f32_e32 v129, v49, v135
	v_add_f32_e32 v137, v137, v138
	v_fmac_f32_e32 v128, v46, v132
	v_fmac_f32_e32 v129, v48, v134
	v_add_f32_e32 v127, v127, v137
	v_add_f32_e32 v128, v128, v129
	v_add_f32_e32 v127, v127, v128
	v_mul_f32_e32 v133, v87, v133
	ds_read_b128 v[128:131], v1 offset:6144
	v_fmac_f32_e32 v133, v86, v132
	v_mul_f32_e32 v132, v85, v135
	v_fmac_f32_e32 v132, v84, v134
	v_add_f32_e32 v132, v133, v132
	v_add_f32_e32 v136, v136, v132
	ds_read_b128 v[132:135], v1 offset:7168
	s_waitcnt lgkmcnt(1)
	v_mul_f32_e32 v137, v39, v129
	v_mul_f32_e32 v129, v79, v129
	v_fmac_f32_e32 v137, v38, v128
	v_fmac_f32_e32 v129, v78, v128
	v_mul_f32_e32 v128, v81, v131
	v_fmac_f32_e32 v128, v80, v130
	v_mul_f32_e32 v138, v41, v131
	v_add_f32_e32 v128, v129, v128
	v_fmac_f32_e32 v138, v40, v130
	v_add_f32_e32 v129, v136, v128
	s_waitcnt lgkmcnt(0)
	v_mul_f32_e32 v128, v35, v133
	v_mul_f32_e32 v130, v37, v135
	v_add_f32_e32 v137, v137, v138
	v_fmac_f32_e32 v128, v34, v132
	v_fmac_f32_e32 v130, v36, v134
	v_add_f32_e32 v127, v127, v137
	v_add_f32_e32 v128, v128, v130
	v_add_f32_e32 v128, v127, v128
	v_mul_f32_e32 v127, v77, v133
	v_fmac_f32_e32 v127, v76, v132
	ds_read_b128 v[130:133], v1 offset:8192
	v_pk_mul_f32 v[44:45], v[32:33], v[44:45]
	s_nop 0
	v_mul_f32_e32 v135, v45, v135
	v_fmac_f32_e32 v135, v44, v134
	v_add_f32_e32 v127, v127, v135
	ds_read_b128 v[134:137], v1 offset:9216
	v_add_f32_e32 v127, v129, v127
	s_waitcnt lgkmcnt(1)
	v_mul_f32_e32 v129, v75, v131
	v_mul_f32_e32 v131, v101, v131
	v_fmac_f32_e32 v129, v74, v130
	v_fmac_f32_e32 v131, v100, v130
	v_mul_f32_e32 v130, v105, v133
	v_mul_f32_e32 v138, v73, v133
	v_fmac_f32_e32 v130, v104, v132
	v_fmac_f32_e32 v138, v72, v132
	v_add_f32_e32 v130, v131, v130
	v_add_f32_e32 v129, v129, v138
	v_add_f32_e32 v138, 0, v130
	s_waitcnt lgkmcnt(0)
	v_mul_f32_e32 v130, v71, v135
	v_mul_f32_e32 v131, v69, v137
	v_fmac_f32_e32 v130, v70, v134
	v_fmac_f32_e32 v131, v68, v136
	v_add_f32_e32 v129, 0, v129
	v_add_f32_e32 v130, v130, v131
	v_add_f32_e32 v129, v129, v130
	v_mul_f32_e32 v135, v103, v135
	ds_read_b128 v[130:133], v1 offset:10240
	v_fmac_f32_e32 v135, v102, v134
	v_mul_f32_e32 v134, v99, v137
	v_fmac_f32_e32 v134, v98, v136
	v_add_f32_e32 v134, v135, v134
	v_add_f32_e32 v138, v138, v134
	ds_read_b128 v[134:137], v1 offset:11264
	s_waitcnt lgkmcnt(1)
	v_mul_f32_e32 v139, v65, v131
	v_mul_f32_e32 v131, v95, v131
	v_fmac_f32_e32 v139, v64, v130
	v_fmac_f32_e32 v131, v94, v130
	v_mul_f32_e32 v130, v97, v133
	v_fmac_f32_e32 v130, v96, v132
	v_mul_f32_e32 v140, v61, v133
	v_add_f32_e32 v130, v131, v130
	v_fmac_f32_e32 v140, v60, v132
	v_add_f32_e32 v138, v138, v130
	s_waitcnt lgkmcnt(0)
	v_mul_f32_e32 v130, v57, v135
	v_mul_f32_e32 v131, v67, v137
	v_add_f32_e32 v139, v139, v140
	v_fmac_f32_e32 v130, v56, v134
	v_fmac_f32_e32 v131, v66, v136
	v_add_f32_e32 v129, v129, v139
	v_add_f32_e32 v130, v130, v131
	v_add_f32_e32 v129, v129, v130
	v_mul_f32_e32 v135, v93, v135
	ds_read_b128 v[130:133], v1 offset:12288
	v_fmac_f32_e32 v135, v92, v134
	v_mul_f32_e32 v134, v91, v137
	v_fmac_f32_e32 v134, v90, v136
	v_add_f32_e32 v134, v135, v134
	v_add_f32_e32 v138, v138, v134
	ds_read_b128 v[134:137], v1 offset:13312
	s_waitcnt lgkmcnt(1)
	v_mul_f32_e32 v139, v59, v131
	v_mul_f32_e32 v131, v83, v131
	v_fmac_f32_e32 v139, v58, v130
	v_fmac_f32_e32 v131, v82, v130
	v_mul_f32_e32 v130, v89, v133
	v_fmac_f32_e32 v130, v88, v132
	v_mul_f32_e32 v140, v63, v133
	v_add_f32_e32 v130, v131, v130
	v_fmac_f32_e32 v140, v62, v132
	v_add_f32_e32 v138, v138, v130
	s_waitcnt lgkmcnt(0)
	v_mul_f32_e32 v130, v47, v135
	v_mul_f32_e32 v131, v49, v137
	v_add_f32_e32 v139, v139, v140
	v_fmac_f32_e32 v130, v46, v134
	v_fmac_f32_e32 v131, v48, v136
	v_add_f32_e32 v129, v129, v139
	v_add_f32_e32 v130, v130, v131
	v_add_f32_e32 v129, v129, v130
	v_mul_f32_e32 v135, v87, v135
	ds_read_b128 v[130:133], v1 offset:14336
	v_fmac_f32_e32 v135, v86, v134
	v_mul_f32_e32 v134, v85, v137
	v_fmac_f32_e32 v134, v84, v136
	v_add_f32_e32 v134, v135, v134
	v_add_f32_e32 v138, v138, v134
	ds_read_b128 v[134:137], v1 offset:15360
	s_waitcnt lgkmcnt(1)
	v_mul_f32_e32 v139, v39, v131
	v_mul_f32_e32 v131, v79, v131
	v_fmac_f32_e32 v139, v38, v130
	v_fmac_f32_e32 v131, v78, v130
	v_mul_f32_e32 v130, v81, v133
	v_fmac_f32_e32 v130, v80, v132
	v_mul_f32_e32 v140, v41, v133
	v_add_f32_e32 v130, v131, v130
	v_fmac_f32_e32 v140, v40, v132
	v_add_f32_e32 v131, v138, v130
	s_waitcnt lgkmcnt(0)
	v_mul_f32_e32 v130, v35, v135
	v_mul_f32_e32 v132, v37, v137
	v_add_f32_e32 v139, v139, v140
	v_fmac_f32_e32 v130, v34, v134
	v_fmac_f32_e32 v132, v36, v136
	v_add_f32_e32 v129, v129, v139
	v_add_f32_e32 v130, v130, v132
	v_add_f32_e32 v130, v129, v130
	v_mul_f32_e32 v129, v77, v135
	v_fmac_f32_e32 v129, v76, v134
	ds_read_b128 v[132:135], v1 offset:16384
	v_mul_f32_e32 v137, v45, v137
	v_fmac_f32_e32 v137, v44, v136
	v_add_f32_e32 v129, v129, v137
	ds_read_b128 v[136:139], v1 offset:17408
	v_add_f32_e32 v129, v131, v129
	s_waitcnt lgkmcnt(1)
	v_mul_f32_e32 v131, v75, v133
	v_mul_f32_e32 v133, v101, v133
	v_fmac_f32_e32 v131, v74, v132
	v_fmac_f32_e32 v133, v100, v132
	v_mul_f32_e32 v132, v105, v135
	v_mul_f32_e32 v140, v73, v135
	v_fmac_f32_e32 v132, v104, v134
	v_fmac_f32_e32 v140, v72, v134
	v_add_f32_e32 v132, v133, v132
	v_add_f32_e32 v131, v131, v140
	v_add_f32_e32 v140, 0, v132
	s_waitcnt lgkmcnt(0)
	v_mul_f32_e32 v132, v71, v137
	v_mul_f32_e32 v133, v69, v139
	v_fmac_f32_e32 v132, v70, v136
	v_fmac_f32_e32 v133, v68, v138
	v_add_f32_e32 v131, 0, v131
	v_add_f32_e32 v132, v132, v133
	v_add_f32_e32 v131, v131, v132
	v_mul_f32_e32 v137, v103, v137
	ds_read_b128 v[132:135], v1 offset:18432
	v_fmac_f32_e32 v137, v102, v136
	v_mul_f32_e32 v136, v99, v139
	v_fmac_f32_e32 v136, v98, v138
	v_add_f32_e32 v136, v137, v136
	v_add_f32_e32 v140, v140, v136
	ds_read_b128 v[136:139], v1 offset:19456
	s_waitcnt lgkmcnt(1)
	v_mul_f32_e32 v141, v65, v133
	v_mul_f32_e32 v133, v95, v133
	v_fmac_f32_e32 v141, v64, v132
	v_fmac_f32_e32 v133, v94, v132
	v_mul_f32_e32 v132, v97, v135
	v_fmac_f32_e32 v132, v96, v134
	v_mul_f32_e32 v142, v61, v135
	v_add_f32_e32 v132, v133, v132
	v_fmac_f32_e32 v142, v60, v134
	v_add_f32_e32 v140, v140, v132
	s_waitcnt lgkmcnt(0)
	v_mul_f32_e32 v132, v57, v137
	v_mul_f32_e32 v133, v67, v139
	v_add_f32_e32 v141, v141, v142
	v_fmac_f32_e32 v132, v56, v136
	v_fmac_f32_e32 v133, v66, v138
	v_add_f32_e32 v131, v131, v141
	v_add_f32_e32 v132, v132, v133
	v_add_f32_e32 v131, v131, v132
	v_mul_f32_e32 v137, v93, v137
	ds_read_b128 v[132:135], v1 offset:20480
	v_fmac_f32_e32 v137, v92, v136
	v_mul_f32_e32 v136, v91, v139
	v_fmac_f32_e32 v136, v90, v138
	v_add_f32_e32 v136, v137, v136
	v_add_f32_e32 v140, v140, v136
	ds_read_b128 v[136:139], v1 offset:21504
	s_waitcnt lgkmcnt(1)
	v_mul_f32_e32 v141, v59, v133
	v_mul_f32_e32 v133, v83, v133
	v_fmac_f32_e32 v141, v58, v132
	v_fmac_f32_e32 v133, v82, v132
	v_mul_f32_e32 v132, v89, v135
	v_fmac_f32_e32 v132, v88, v134
	v_mul_f32_e32 v142, v63, v135
	v_add_f32_e32 v132, v133, v132
	v_fmac_f32_e32 v142, v62, v134
	v_add_f32_e32 v140, v140, v132
	s_waitcnt lgkmcnt(0)
	v_mul_f32_e32 v132, v47, v137
	v_mul_f32_e32 v133, v49, v139
	v_add_f32_e32 v141, v141, v142
	v_fmac_f32_e32 v132, v46, v136
	v_fmac_f32_e32 v133, v48, v138
	v_add_f32_e32 v131, v131, v141
	v_add_f32_e32 v132, v132, v133
	v_add_f32_e32 v131, v131, v132
	v_mul_f32_e32 v137, v87, v137
	ds_read_b128 v[132:135], v1 offset:22528
	v_fmac_f32_e32 v137, v86, v136
	v_mul_f32_e32 v136, v85, v139
	v_fmac_f32_e32 v136, v84, v138
	v_add_f32_e32 v136, v137, v136
	v_add_f32_e32 v140, v140, v136
	ds_read_b128 v[136:139], v1 offset:23552
	s_waitcnt lgkmcnt(1)
	v_mul_f32_e32 v141, v39, v133
	v_mul_f32_e32 v133, v79, v133
	v_fmac_f32_e32 v141, v38, v132
	v_fmac_f32_e32 v133, v78, v132
	v_mul_f32_e32 v132, v81, v135
	v_fmac_f32_e32 v132, v80, v134
	v_mul_f32_e32 v142, v41, v135
	v_add_f32_e32 v132, v133, v132
	v_fmac_f32_e32 v142, v40, v134
	v_add_f32_e32 v133, v140, v132
	s_waitcnt lgkmcnt(0)
	v_mul_f32_e32 v132, v35, v137
	v_mul_f32_e32 v134, v37, v139
	v_add_f32_e32 v141, v141, v142
	v_fmac_f32_e32 v132, v34, v136
	v_fmac_f32_e32 v134, v36, v138
	v_add_f32_e32 v131, v131, v141
	v_add_f32_e32 v132, v132, v134
	v_add_f32_e32 v132, v131, v132
	v_mul_f32_e32 v131, v77, v137
	v_fmac_f32_e32 v131, v76, v136
	ds_read_b128 v[134:137], v1 offset:24576
	v_mul_f32_e32 v139, v45, v139
	v_fmac_f32_e32 v139, v44, v138
	v_add_f32_e32 v131, v131, v139
	ds_read_b128 v[138:141], v1 offset:25600
	v_add_f32_e32 v131, v133, v131
	s_waitcnt lgkmcnt(1)
	v_mul_f32_e32 v133, v75, v135
	v_mul_f32_e32 v135, v101, v135
	v_fmac_f32_e32 v133, v74, v134
	v_fmac_f32_e32 v135, v100, v134
	v_mul_f32_e32 v134, v105, v137
	v_mul_f32_e32 v142, v73, v137
	v_fmac_f32_e32 v134, v104, v136
	v_fmac_f32_e32 v142, v72, v136
	v_add_f32_e32 v134, v135, v134
	v_add_f32_e32 v133, v133, v142
	v_add_f32_e32 v142, 0, v134
	s_waitcnt lgkmcnt(0)
	v_mul_f32_e32 v134, v71, v139
	v_mul_f32_e32 v135, v69, v141
	v_fmac_f32_e32 v134, v70, v138
	v_fmac_f32_e32 v135, v68, v140
	v_add_f32_e32 v133, 0, v133
	v_add_f32_e32 v134, v134, v135
	v_add_f32_e32 v133, v133, v134
	v_mul_f32_e32 v139, v103, v139
	ds_read_b128 v[134:137], v1 offset:26624
	v_fmac_f32_e32 v139, v102, v138
	v_mul_f32_e32 v138, v99, v141
	v_fmac_f32_e32 v138, v98, v140
	v_add_f32_e32 v138, v139, v138
	v_add_f32_e32 v142, v142, v138
	ds_read_b128 v[138:141], v1 offset:27648
	s_waitcnt lgkmcnt(1)
	v_mul_f32_e32 v143, v65, v135
	v_mul_f32_e32 v135, v95, v135
	v_fmac_f32_e32 v143, v64, v134
	v_fmac_f32_e32 v135, v94, v134
	v_mul_f32_e32 v134, v97, v137
	v_fmac_f32_e32 v134, v96, v136
	v_mul_f32_e32 v144, v61, v137
	v_add_f32_e32 v134, v135, v134
	v_fmac_f32_e32 v144, v60, v136
	v_add_f32_e32 v142, v142, v134
	s_waitcnt lgkmcnt(0)
	v_mul_f32_e32 v134, v57, v139
	v_mul_f32_e32 v135, v67, v141
	v_add_f32_e32 v143, v143, v144
	v_fmac_f32_e32 v134, v56, v138
	v_fmac_f32_e32 v135, v66, v140
	v_add_f32_e32 v133, v133, v143
	v_add_f32_e32 v134, v134, v135
	v_add_f32_e32 v133, v133, v134
	v_mul_f32_e32 v139, v93, v139
	ds_read_b128 v[134:137], v1 offset:28672
	v_fmac_f32_e32 v139, v92, v138
	v_mul_f32_e32 v138, v91, v141
	v_fmac_f32_e32 v138, v90, v140
	v_add_f32_e32 v138, v139, v138
	v_add_f32_e32 v142, v142, v138
	ds_read_b128 v[138:141], v1 offset:29696
	s_waitcnt lgkmcnt(1)
	v_mul_f32_e32 v143, v59, v135
	v_mul_f32_e32 v135, v83, v135
	v_fmac_f32_e32 v143, v58, v134
	v_fmac_f32_e32 v135, v82, v134
	v_mul_f32_e32 v134, v89, v137
	v_fmac_f32_e32 v134, v88, v136
	v_mul_f32_e32 v144, v63, v137
	v_add_f32_e32 v134, v135, v134
	v_fmac_f32_e32 v144, v62, v136
	v_add_f32_e32 v142, v142, v134
	s_waitcnt lgkmcnt(0)
	v_mul_f32_e32 v134, v47, v139
	v_mul_f32_e32 v135, v49, v141
	v_add_f32_e32 v143, v143, v144
	v_fmac_f32_e32 v134, v46, v138
	v_fmac_f32_e32 v135, v48, v140
	v_add_f32_e32 v133, v133, v143
	v_add_f32_e32 v134, v134, v135
	v_add_f32_e32 v133, v133, v134
	v_mul_f32_e32 v139, v87, v139
	ds_read_b128 v[134:137], v1 offset:30720
	v_fmac_f32_e32 v139, v86, v138
	v_mul_f32_e32 v138, v85, v141
	v_fmac_f32_e32 v138, v84, v140
	v_add_f32_e32 v138, v139, v138
	v_add_f32_e32 v142, v142, v138
	ds_read_b128 v[138:141], v1 offset:31744
	s_waitcnt lgkmcnt(1)
	v_mul_f32_e32 v143, v39, v135
	v_mul_f32_e32 v135, v79, v135
	v_fmac_f32_e32 v143, v38, v134
	v_fmac_f32_e32 v135, v78, v134
	v_mul_f32_e32 v134, v81, v137
	v_fmac_f32_e32 v134, v80, v136
	v_mul_f32_e32 v144, v41, v137
	v_add_f32_e32 v134, v135, v134
	v_fmac_f32_e32 v144, v40, v136
	v_add_f32_e32 v135, v142, v134
	s_waitcnt lgkmcnt(0)
	v_mul_f32_e32 v134, v35, v139
	v_mul_f32_e32 v136, v37, v141
	v_add_f32_e32 v143, v143, v144
	v_fmac_f32_e32 v134, v34, v138
	v_fmac_f32_e32 v136, v36, v140
	v_add_f32_e32 v133, v133, v143
	v_add_f32_e32 v134, v134, v136
	v_add_f32_e32 v134, v133, v134
	v_mul_f32_e32 v133, v77, v139
	v_fmac_f32_e32 v133, v76, v138
	ds_read_b128 v[136:139], v1 offset:32768
	v_mul_f32_e32 v141, v45, v141
	v_fmac_f32_e32 v141, v44, v140
	v_add_f32_e32 v133, v133, v141
	ds_read_b128 v[140:143], v1 offset:33792
	v_add_f32_e32 v133, v135, v133
	s_waitcnt lgkmcnt(1)
	v_mul_f32_e32 v135, v75, v137
	v_mul_f32_e32 v137, v101, v137
	v_fmac_f32_e32 v135, v74, v136
	v_fmac_f32_e32 v137, v100, v136
	v_mul_f32_e32 v136, v105, v139
	v_mul_f32_e32 v144, v73, v139
	v_fmac_f32_e32 v136, v104, v138
	v_fmac_f32_e32 v144, v72, v138
	v_add_f32_e32 v136, v137, v136
	v_add_f32_e32 v135, v135, v144
	v_add_f32_e32 v144, 0, v136
	s_waitcnt lgkmcnt(0)
	v_mul_f32_e32 v136, v71, v141
	v_mul_f32_e32 v137, v69, v143
	v_fmac_f32_e32 v136, v70, v140
	v_fmac_f32_e32 v137, v68, v142
	v_add_f32_e32 v135, 0, v135
	v_add_f32_e32 v136, v136, v137
	v_add_f32_e32 v135, v135, v136
	v_mul_f32_e32 v141, v103, v141
	ds_read_b128 v[136:139], v1 offset:34816
	v_fmac_f32_e32 v141, v102, v140
	v_mul_f32_e32 v140, v99, v143
	v_fmac_f32_e32 v140, v98, v142
	v_add_f32_e32 v140, v141, v140
	v_add_f32_e32 v144, v144, v140
	ds_read_b128 v[140:143], v1 offset:35840
	s_waitcnt lgkmcnt(1)
	v_mul_f32_e32 v145, v65, v137
	v_mul_f32_e32 v137, v95, v137
	v_fmac_f32_e32 v145, v64, v136
	v_fmac_f32_e32 v137, v94, v136
	v_mul_f32_e32 v136, v97, v139
	v_fmac_f32_e32 v136, v96, v138
	v_mul_f32_e32 v146, v61, v139
	v_add_f32_e32 v136, v137, v136
	v_fmac_f32_e32 v146, v60, v138
	v_add_f32_e32 v144, v144, v136
	s_waitcnt lgkmcnt(0)
	v_mul_f32_e32 v136, v57, v141
	v_mul_f32_e32 v137, v67, v143
	v_add_f32_e32 v145, v145, v146
	v_fmac_f32_e32 v136, v56, v140
	v_fmac_f32_e32 v137, v66, v142
	v_add_f32_e32 v135, v135, v145
	v_add_f32_e32 v136, v136, v137
	v_add_f32_e32 v135, v135, v136
	v_mul_f32_e32 v141, v93, v141
	ds_read_b128 v[136:139], v1 offset:36864
	v_fmac_f32_e32 v141, v92, v140
	v_mul_f32_e32 v140, v91, v143
	v_fmac_f32_e32 v140, v90, v142
	v_add_f32_e32 v140, v141, v140
	v_add_f32_e32 v144, v144, v140
	ds_read_b128 v[140:143], v1 offset:37888
	s_waitcnt lgkmcnt(1)
	v_mul_f32_e32 v145, v59, v137
	v_mul_f32_e32 v137, v83, v137
	v_fmac_f32_e32 v145, v58, v136
	v_fmac_f32_e32 v137, v82, v136
	v_mul_f32_e32 v136, v89, v139
	v_fmac_f32_e32 v136, v88, v138
	v_mul_f32_e32 v146, v63, v139
	v_add_f32_e32 v136, v137, v136
	v_fmac_f32_e32 v146, v62, v138
	v_add_f32_e32 v144, v144, v136
	s_waitcnt lgkmcnt(0)
	v_mul_f32_e32 v136, v47, v141
	v_mul_f32_e32 v137, v49, v143
	v_add_f32_e32 v145, v145, v146
	v_fmac_f32_e32 v136, v46, v140
	v_fmac_f32_e32 v137, v48, v142
	v_add_f32_e32 v135, v135, v145
	v_add_f32_e32 v136, v136, v137
	v_add_f32_e32 v135, v135, v136
	v_mul_f32_e32 v141, v87, v141
	ds_read_b128 v[136:139], v1 offset:38912
	v_fmac_f32_e32 v141, v86, v140
	v_mul_f32_e32 v140, v85, v143
	v_fmac_f32_e32 v140, v84, v142
	v_add_f32_e32 v140, v141, v140
	v_add_f32_e32 v144, v144, v140
	ds_read_b128 v[140:143], v1 offset:39936
	s_waitcnt lgkmcnt(1)
	v_mul_f32_e32 v145, v39, v137
	v_mul_f32_e32 v137, v79, v137
	v_fmac_f32_e32 v145, v38, v136
	v_fmac_f32_e32 v137, v78, v136
	v_mul_f32_e32 v136, v81, v139
	v_fmac_f32_e32 v136, v80, v138
	v_mul_f32_e32 v146, v41, v139
	v_add_f32_e32 v136, v137, v136
	v_fmac_f32_e32 v146, v40, v138
	v_add_f32_e32 v137, v144, v136
	s_waitcnt lgkmcnt(0)
	v_mul_f32_e32 v136, v35, v141
	v_mul_f32_e32 v138, v37, v143
	v_add_f32_e32 v145, v145, v146
	v_fmac_f32_e32 v136, v34, v140
	v_fmac_f32_e32 v138, v36, v142
	v_add_f32_e32 v135, v135, v145
	v_add_f32_e32 v136, v136, v138
	v_add_f32_e32 v136, v135, v136
	v_mul_f32_e32 v135, v77, v141
	v_fmac_f32_e32 v135, v76, v140
	ds_read_b128 v[138:141], v1 offset:40960
	v_mul_f32_e32 v143, v45, v143
	v_fmac_f32_e32 v143, v44, v142
	v_add_f32_e32 v135, v135, v143
	ds_read_b128 v[142:145], v1 offset:41984
	v_add_f32_e32 v135, v137, v135
	s_waitcnt lgkmcnt(1)
	v_mul_f32_e32 v137, v75, v139
	v_mul_f32_e32 v139, v101, v139
	v_fmac_f32_e32 v137, v74, v138
	v_fmac_f32_e32 v139, v100, v138
	v_mul_f32_e32 v138, v105, v141
	v_mul_f32_e32 v146, v73, v141
	v_fmac_f32_e32 v138, v104, v140
	v_fmac_f32_e32 v146, v72, v140
	v_add_f32_e32 v138, v139, v138
	v_add_f32_e32 v137, v137, v146
	v_add_f32_e32 v146, 0, v138
	s_waitcnt lgkmcnt(0)
	v_mul_f32_e32 v138, v71, v143
	v_mul_f32_e32 v139, v69, v145
	v_fmac_f32_e32 v138, v70, v142
	v_fmac_f32_e32 v139, v68, v144
	v_add_f32_e32 v137, 0, v137
	v_add_f32_e32 v138, v138, v139
	v_add_f32_e32 v137, v137, v138
	v_mul_f32_e32 v143, v103, v143
	ds_read_b128 v[138:141], v1 offset:43008
	v_fmac_f32_e32 v143, v102, v142
	v_mul_f32_e32 v142, v99, v145
	v_fmac_f32_e32 v142, v98, v144
	v_add_f32_e32 v142, v143, v142
	v_add_f32_e32 v146, v146, v142
	ds_read_b128 v[142:145], v1 offset:44032
	s_waitcnt lgkmcnt(1)
	v_mul_f32_e32 v147, v65, v139
	v_mul_f32_e32 v139, v95, v139
	v_fmac_f32_e32 v147, v64, v138
	v_fmac_f32_e32 v139, v94, v138
	v_mul_f32_e32 v138, v97, v141
	v_fmac_f32_e32 v138, v96, v140
	v_mul_f32_e32 v148, v61, v141
	v_add_f32_e32 v138, v139, v138
	v_fmac_f32_e32 v148, v60, v140
	v_add_f32_e32 v146, v146, v138
	s_waitcnt lgkmcnt(0)
	v_mul_f32_e32 v138, v57, v143
	v_mul_f32_e32 v139, v67, v145
	v_add_f32_e32 v147, v147, v148
	v_fmac_f32_e32 v138, v56, v142
	v_fmac_f32_e32 v139, v66, v144
	v_add_f32_e32 v137, v137, v147
	v_add_f32_e32 v138, v138, v139
	v_add_f32_e32 v137, v137, v138
	v_mul_f32_e32 v143, v93, v143
	ds_read_b128 v[138:141], v1 offset:45056
	v_fmac_f32_e32 v143, v92, v142
	v_mul_f32_e32 v142, v91, v145
	v_fmac_f32_e32 v142, v90, v144
	v_add_f32_e32 v142, v143, v142
	v_add_f32_e32 v146, v146, v142
	ds_read_b128 v[142:145], v1 offset:46080
	s_waitcnt lgkmcnt(1)
	v_mul_f32_e32 v147, v59, v139
	v_mul_f32_e32 v139, v83, v139
	v_fmac_f32_e32 v147, v58, v138
	v_fmac_f32_e32 v139, v82, v138
	v_mul_f32_e32 v138, v89, v141
	v_fmac_f32_e32 v138, v88, v140
	v_mul_f32_e32 v148, v63, v141
	v_add_f32_e32 v138, v139, v138
	v_fmac_f32_e32 v148, v62, v140
	v_add_f32_e32 v146, v146, v138
	s_waitcnt lgkmcnt(0)
	v_mul_f32_e32 v138, v47, v143
	v_mul_f32_e32 v139, v49, v145
	v_add_f32_e32 v147, v147, v148
	v_fmac_f32_e32 v138, v46, v142
	v_fmac_f32_e32 v139, v48, v144
	v_add_f32_e32 v137, v137, v147
	v_add_f32_e32 v138, v138, v139
	v_add_f32_e32 v137, v137, v138
	v_mul_f32_e32 v143, v87, v143
	ds_read_b128 v[138:141], v1 offset:47104
	v_fmac_f32_e32 v143, v86, v142
	v_mul_f32_e32 v142, v85, v145
	v_fmac_f32_e32 v142, v84, v144
	v_add_f32_e32 v142, v143, v142
	v_add_f32_e32 v146, v146, v142
	ds_read_b128 v[142:145], v1 offset:48128
	s_waitcnt lgkmcnt(1)
	v_mul_f32_e32 v147, v39, v139
	v_mul_f32_e32 v139, v79, v139
	v_fmac_f32_e32 v147, v38, v138
	v_fmac_f32_e32 v139, v78, v138
	v_mul_f32_e32 v138, v81, v141
	v_fmac_f32_e32 v138, v80, v140
	v_mul_f32_e32 v148, v41, v141
	v_add_f32_e32 v138, v139, v138
	v_fmac_f32_e32 v148, v40, v140
	v_add_f32_e32 v146, v146, v138
	s_waitcnt lgkmcnt(0)
	v_mul_f32_e32 v138, v35, v143
	v_mul_f32_e32 v139, v37, v145
	v_add_f32_e32 v147, v147, v148
	v_fmac_f32_e32 v138, v34, v142
	v_fmac_f32_e32 v139, v36, v144
	v_add_f32_e32 v137, v137, v147
	v_add_f32_e32 v138, v138, v139
	v_add_f32_e32 v137, v137, v138
	v_mul_f32_e32 v143, v77, v143
	ds_read_b128 v[138:141], v1 offset:49152
	v_fmac_f32_e32 v143, v76, v142
	v_mul_f32_e32 v142, v45, v145
	v_fmac_f32_e32 v142, v44, v144
	v_add_f32_e32 v142, v143, v142
	v_add_f32_e32 v146, v146, v142
	ds_read_b128 v[142:145], v1 offset:50176
	s_waitcnt lgkmcnt(1)
	v_mul_f32_e32 v147, v75, v139
	v_mul_f32_e32 v139, v101, v139
	v_fmac_f32_e32 v147, v74, v138
	v_fmac_f32_e32 v139, v100, v138
	v_mul_f32_e32 v138, v105, v141
	v_mul_f32_e32 v148, v73, v141
	v_fmac_f32_e32 v138, v104, v140
	v_fmac_f32_e32 v148, v72, v140
	v_add_f32_e32 v138, v139, v138
	v_add_f32_e32 v147, v147, v148
	v_add_f32_e32 v148, 0, v138
	s_waitcnt lgkmcnt(0)
	v_mul_f32_e32 v138, v71, v143
	v_mul_f32_e32 v139, v69, v145
	v_fmac_f32_e32 v138, v70, v142
	v_fmac_f32_e32 v139, v68, v144
	v_add_f32_e32 v147, 0, v147
	v_add_f32_e32 v138, v138, v139
	v_add_f32_e32 v147, v147, v138
	v_mul_f32_e32 v143, v103, v143
	ds_read_b128 v[138:141], v1 offset:51200
	v_fmac_f32_e32 v143, v102, v142
	v_mul_f32_e32 v142, v99, v145
	v_fmac_f32_e32 v142, v98, v144
	v_add_f32_e32 v142, v143, v142
	v_add_f32_e32 v148, v148, v142
	ds_read_b128 v[142:145], v1 offset:52224
	s_waitcnt lgkmcnt(1)
	v_mul_f32_e32 v149, v65, v139
	v_mul_f32_e32 v139, v95, v139
	v_fmac_f32_e32 v149, v64, v138
	v_fmac_f32_e32 v139, v94, v138
	v_mul_f32_e32 v138, v97, v141
	v_fmac_f32_e32 v138, v96, v140
	v_mul_f32_e32 v150, v61, v141
	v_add_f32_e32 v138, v139, v138
	v_fmac_f32_e32 v150, v60, v140
	v_add_f32_e32 v148, v148, v138
	s_waitcnt lgkmcnt(0)
	v_mul_f32_e32 v138, v57, v143
	v_mul_f32_e32 v139, v67, v145
	v_add_f32_e32 v149, v149, v150
	v_fmac_f32_e32 v138, v56, v142
	v_fmac_f32_e32 v139, v66, v144
	v_add_f32_e32 v147, v147, v149
	v_add_f32_e32 v138, v138, v139
	v_add_f32_e32 v147, v147, v138
	v_mul_f32_e32 v143, v93, v143
	ds_read_b128 v[138:141], v1 offset:53248
	v_fmac_f32_e32 v143, v92, v142
	v_mul_f32_e32 v142, v91, v145
	v_fmac_f32_e32 v142, v90, v144
	v_add_f32_e32 v142, v143, v142
	v_add_f32_e32 v148, v148, v142
	ds_read_b128 v[142:145], v1 offset:54272
	s_waitcnt lgkmcnt(1)
	v_mul_f32_e32 v149, v59, v139
	v_mul_f32_e32 v139, v83, v139
	v_fmac_f32_e32 v149, v58, v138
	v_fmac_f32_e32 v139, v82, v138
	v_mul_f32_e32 v138, v89, v141
	v_fmac_f32_e32 v138, v88, v140
	v_mul_f32_e32 v150, v63, v141
	v_add_f32_e32 v138, v139, v138
	v_fmac_f32_e32 v150, v62, v140
	v_add_f32_e32 v148, v148, v138
	s_waitcnt lgkmcnt(0)
	v_mul_f32_e32 v138, v47, v143
	v_mul_f32_e32 v139, v49, v145
	v_add_f32_e32 v149, v149, v150
	v_fmac_f32_e32 v138, v46, v142
	v_fmac_f32_e32 v139, v48, v144
	v_add_f32_e32 v147, v147, v149
	v_add_f32_e32 v138, v138, v139
	v_add_f32_e32 v147, v147, v138
	v_mul_f32_e32 v143, v87, v143
	ds_read_b128 v[138:141], v1 offset:55296
	v_fmac_f32_e32 v143, v86, v142
	v_mul_f32_e32 v142, v85, v145
	v_fmac_f32_e32 v142, v84, v144
	v_add_f32_e32 v142, v143, v142
	v_add_f32_e32 v148, v148, v142
	ds_read_b128 v[142:145], v1 offset:56320
	s_waitcnt lgkmcnt(1)
	v_mul_f32_e32 v149, v39, v139
	v_mul_f32_e32 v139, v79, v139
	v_fmac_f32_e32 v149, v38, v138
	v_fmac_f32_e32 v139, v78, v138
	v_mul_f32_e32 v138, v81, v141
	v_fmac_f32_e32 v138, v80, v140
	v_mul_f32_e32 v150, v41, v141
	v_add_f32_e32 v138, v139, v138
	v_fmac_f32_e32 v150, v40, v140
	v_add_f32_e32 v148, v148, v138
	s_waitcnt lgkmcnt(0)
	v_mul_f32_e32 v138, v35, v143
	v_mul_f32_e32 v139, v37, v145
	v_mul_f32_e32 v143, v77, v143
	v_add_f32_e32 v149, v149, v150
	v_fmac_f32_e32 v138, v34, v142
	v_fmac_f32_e32 v139, v36, v144
	v_fmac_f32_e32 v143, v76, v142
	v_mul_f32_e32 v142, v45, v145
	v_add_f32_e32 v147, v147, v149
	v_add_f32_e32 v138, v138, v139
	v_fmac_f32_e32 v142, v44, v144
	v_add_f32_e32 v147, v147, v138
	ds_read_b128 v[138:141], v1 offset:57344
	v_add_f32_e32 v142, v143, v142
	v_add_f32_e32 v148, v148, v142
	ds_read_b128 v[142:145], v1 offset:58368
	s_waitcnt lgkmcnt(1)
	v_mul_f32_e32 v75, v75, v139
	v_mul_f32_e32 v73, v73, v141
	v_fmac_f32_e32 v75, v74, v138
	v_fmac_f32_e32 v73, v72, v140
	s_waitcnt lgkmcnt(0)
	v_mul_f32_e32 v71, v71, v143
	v_mul_f32_e32 v69, v69, v145
	v_add_f32_e32 v72, v75, v73
	v_mul_f32_e32 v73, v101, v139
	v_mul_f32_e32 v74, v105, v141
	v_fmac_f32_e32 v71, v70, v142
	v_fmac_f32_e32 v69, v68, v144
	v_add_f32_e32 v72, 0, v72
	v_fmac_f32_e32 v73, v100, v138
	v_fmac_f32_e32 v74, v104, v140
	v_add_f32_e32 v68, v71, v69
	v_add_f32_e32 v73, v73, v74
	v_add_f32_e32 v100, v72, v68
	v_mul_f32_e32 v72, v103, v143
	v_mul_f32_e32 v74, v99, v145
	v_fmac_f32_e32 v72, v102, v142
	ds_read_b128 v[68:71], v1 offset:59392
	v_fmac_f32_e32 v74, v98, v144
	v_add_f32_e32 v73, 0, v73
	v_add_f32_e32 v72, v72, v74
	v_add_f32_e32 v98, v73, v72
	ds_read_b128 v[72:75], v1 offset:60416
	s_waitcnt lgkmcnt(1)
	v_mul_f32_e32 v65, v65, v69
	v_mul_f32_e32 v61, v61, v71
	v_fmac_f32_e32 v65, v64, v68
	v_fmac_f32_e32 v61, v60, v70
	v_add_f32_e32 v60, v65, v61
	v_mul_f32_e32 v61, v95, v69
	v_mul_f32_e32 v64, v97, v71
	s_waitcnt lgkmcnt(0)
	v_mul_f32_e32 v57, v57, v73
	v_fmac_f32_e32 v61, v94, v68
	v_fmac_f32_e32 v64, v96, v70
	v_fmac_f32_e32 v57, v56, v72
	v_mul_f32_e32 v56, v67, v75
	v_add_f32_e32 v61, v61, v64
	v_fmac_f32_e32 v56, v66, v74
	ds_read_b128 v[64:67], v1 offset:61440
	ds_read_b128 v[68:71], v1 offset:62464
	v_add_f32_e32 v60, v100, v60
	v_add_f32_e32 v56, v57, v56
	v_add_f32_e32 v56, v60, v56
	s_waitcnt lgkmcnt(1)
	v_mul_f32_e32 v59, v59, v65
	v_fmac_f32_e32 v59, v58, v64
	v_mul_f32_e32 v58, v63, v67
	v_fmac_f32_e32 v58, v62, v66
	v_mul_f32_e32 v57, v93, v73
	v_mul_f32_e32 v60, v91, v75
	v_add_f32_e32 v58, v59, v58
	s_waitcnt lgkmcnt(0)
	v_mul_f32_e32 v47, v47, v69
	v_fmac_f32_e32 v57, v92, v72
	v_fmac_f32_e32 v60, v90, v74
	v_add_f32_e32 v56, v56, v58
	v_mul_f32_e32 v58, v83, v65
	v_mul_f32_e32 v59, v89, v67
	v_fmac_f32_e32 v47, v46, v68
	v_mul_f32_e32 v46, v49, v71
	v_add_f32_e32 v61, v98, v61
	v_add_f32_e32 v57, v57, v60
	v_fmac_f32_e32 v58, v82, v64
	v_fmac_f32_e32 v59, v88, v66
	v_fmac_f32_e32 v46, v48, v70
	v_add_f32_e32 v57, v61, v57
	v_add_f32_e32 v58, v58, v59
	v_add_f32_e32 v46, v47, v46
	v_add_f32_e32 v57, v57, v58
	v_add_f32_e32 v60, v56, v46
	v_mul_f32_e32 v56, v87, v69
	v_mul_f32_e32 v58, v85, v71
	v_fmac_f32_e32 v56, v86, v68
	v_fmac_f32_e32 v58, v84, v70
	v_add_f32_e32 v56, v56, v58
	ds_read_b128 v[46:49], v1 offset:63488
	v_add_f32_e32 v61, v57, v56
	ds_read_b128 v[56:59], v1 offset:64512
	s_waitcnt lgkmcnt(1)
	v_mul_f32_e32 v39, v39, v47
	v_fmac_f32_e32 v39, v38, v46
	s_waitcnt lgkmcnt(0)
	v_mul_f32_e32 v35, v35, v57
	v_fmac_f32_e32 v35, v34, v56
	v_mul_f32_e32 v34, v37, v59
	v_fmac_f32_e32 v34, v36, v58
	v_cndmask_b32_e64 v36, v128, v136, s[0:1]
	v_mul_f32_e32 v38, v41, v49
	ds_bpermute_b32 v36, v123, v36
	v_fmac_f32_e32 v38, v40, v48
	v_add_f32_e32 v38, v39, v38
	v_add_f32_e32 v38, v60, v38
	v_add_f32_e32 v34, v35, v34
	v_add_f32_e32 v34, v38, v34
	v_cndmask_b32_e64 v38, v136, v128, s[0:1]
	v_mul_f32_e32 v39, v79, v47
	s_waitcnt lgkmcnt(0)
	v_add_f32_e32 v36, v38, v36
	v_cndmask_b32_e64 v38, v130, v137, s[0:1]
	v_fmac_f32_e32 v39, v78, v46
	ds_bpermute_b32 v38, v123, v38
	v_cndmask_b32_e64 v41, v132, v147, s[0:1]
	v_cndmask_b32_e64 v46, v134, v34, s[0:1]
	ds_bpermute_b32 v41, v123, v41
	ds_bpermute_b32 v46, v123, v46
	v_mul_f32_e32 v40, v81, v49
	v_fmac_f32_e32 v40, v80, v48
	v_add_f32_e32 v39, v39, v40
	v_cndmask_b32_e64 v40, v137, v130, s[0:1]
	s_waitcnt lgkmcnt(2)
	v_add_f32_e32 v38, v40, v38
	v_cndmask_b32_e64 v40, v147, v132, s[0:1]
	v_cndmask_b32_e64 v34, v34, v134, s[0:1]
	s_waitcnt lgkmcnt(1)
	v_add_f32_e32 v40, v40, v41
	s_waitcnt lgkmcnt(0)
	v_add_f32_e32 v34, v34, v46
	v_cndmask_b32_e64 v41, v36, v40, s[4:5]
	v_cndmask_b32_e64 v46, v38, v34, s[4:5]
	ds_bpermute_b32 v41, v122, v41
	ds_bpermute_b32 v46, v122, v46
	v_mul_f32_e32 v35, v77, v57
	v_mul_f32_e32 v37, v45, v59
	v_cndmask_b32_e64 v36, v40, v36, s[4:5]
	v_cndmask_b32_e64 v34, v34, v38, s[4:5]
	v_fmac_f32_e32 v35, v76, v56
	v_fmac_f32_e32 v37, v44, v58
	s_waitcnt lgkmcnt(1)
	v_add_f32_e32 v36, v36, v41
	s_waitcnt lgkmcnt(0)
	v_add_f32_e32 v34, v34, v46
	v_add_f32_e32 v35, v35, v37
	v_cndmask_b32_e64 v37, v36, v34, s[10:11]
	ds_bpermute_b32 v37, v121, v37
	v_add_f32_e32 v39, v61, v39
	v_cndmask_b32_e64 v38, v127, v135, s[0:1]
	v_cndmask_b32_e64 v34, v34, v36, s[10:11]
	ds_bpermute_b32 v38, v123, v38
	v_add_f32_e32 v35, v39, v35
	s_waitcnt lgkmcnt(1)
	v_add_f32_e32 v34, v34, v37
	v_cndmask_b32_e64 v37, v129, v146, s[0:1]
	ds_bpermute_b32 v37, v123, v37
	v_cndmask_b32_e64 v39, v131, v148, s[0:1]
	v_cndmask_b32_e64 v40, v133, v35, s[0:1]
	ds_bpermute_b32 v39, v123, v39
	ds_bpermute_b32 v40, v123, v40
	v_cndmask_b32_e64 v36, v135, v127, s[0:1]
	s_waitcnt lgkmcnt(3)
	v_add_f32_e32 v36, v36, v38
	v_cndmask_b32_e64 v38, v146, v129, s[0:1]
	s_waitcnt lgkmcnt(2)
	v_add_f32_e32 v37, v38, v37
	v_cndmask_b32_e64 v38, v148, v131, s[0:1]
	v_cndmask_b32_e64 v35, v35, v133, s[0:1]
	s_waitcnt lgkmcnt(1)
	v_add_f32_e32 v38, v38, v39
	s_waitcnt lgkmcnt(0)
	v_add_f32_e32 v35, v35, v40
	v_cndmask_b32_e64 v39, v36, v38, s[4:5]
	v_cndmask_b32_e64 v40, v37, v35, s[4:5]
	ds_bpermute_b32 v39, v122, v39
	ds_bpermute_b32 v40, v122, v40
	v_cndmask_b32_e64 v36, v38, v36, s[4:5]
	v_cndmask_b32_e64 v35, v35, v37, s[4:5]
	ds_bpermute_b32 v41, v120, v34
	s_waitcnt lgkmcnt(2)
	v_add_f32_e32 v36, v36, v39
	s_waitcnt lgkmcnt(1)
	v_add_f32_e32 v35, v35, v40
	v_cndmask_b32_e64 v37, v36, v35, s[10:11]
	ds_bpermute_b32 v37, v121, v37
	v_cndmask_b32_e64 v35, v35, v36, s[10:11]
	s_waitcnt lgkmcnt(1)
	v_add_f32_e32 v34, v34, v41
	ds_bpermute_b32 v39, v119, v34
	v_med3_f32 v38, v44, s53, v115
	s_waitcnt lgkmcnt(1)
	v_add_f32_e32 v35, v35, v37
	ds_bpermute_b32 v36, v120, v35
	v_med3_f32 v37, v45, s53, v115
	s_waitcnt lgkmcnt(1)
	v_add_f32_e32 v34, v34, v39
	v_cvt_pk_fp8_f32 v126, v38, v37 op_sel:[0,0,1]
	ds_bpermute_b32 v37, v118, v34
	s_waitcnt lgkmcnt(1)
	v_add_f32_e32 v35, v35, v36
	ds_bpermute_b32 v36, v119, v35
	global_store_dword v[42:43], v124, off offset:1280
	global_store_dword v[42:43], v125, off offset:1536
	global_store_dword v[42:43], v126, off offset:1792
	s_waitcnt lgkmcnt(1)
	v_add_f32_e32 v37, v34, v37
	s_nop 0
	v_readlane_b32 s60, v37, 0
	s_waitcnt lgkmcnt(0)
	v_add_f32_e32 v34, v35, v36
	ds_bpermute_b32 v35, v118, v34
	v_readlane_b32 s59, v37, 8
	v_readlane_b32 s41, v37, 16
	v_readlane_b32 s27, v37, 24
	v_readlane_b32 s26, v37, 32
	v_readlane_b32 s25, v37, 40
	v_readlane_b32 s24, v37, 48
	v_readlane_b32 s2, v37, 56
	s_and_saveexec_b64 s[42:43], s[6:7]
	s_cbranch_execz .LBB0_1349
	v_mov_b32_e32 v36, s60
	v_mov_b32_e32 v37, s59
	v_cmp_gt_f32_e32 vcc, s59, v36
	v_mov_b32_e32 v39, s41
	v_mov_b32_e32 v40, s27
	v_cndmask_b32_e32 v38, v36, v37, vcc
	v_cmp_gt_f32_e64 s[12:13], s41, v38
	v_mov_b32_e32 v41, s26
	v_mov_b32_e32 v42, s25
	v_cndmask_b32_e64 v38, v38, v39, s[12:13]
	v_cmp_gt_f32_e64 s[14:15], s27, v38
	v_mov_b32_e32 v43, s24
	v_cndmask_b32_e64 v45, 0, 1, vcc
	v_cndmask_b32_e64 v38, v38, v40, s[14:15]
	v_cmp_gt_f32_e64 s[16:17], s26, v38
	v_cmp_ngt_f32_e32 vcc, s60, v116
	v_mov_b32_e32 v44, s2
	v_cndmask_b32_e64 v38, v38, v41, s[16:17]
	v_cmp_gt_f32_e64 s[18:19], s25, v38
	s_mov_b64 s[44:45], exec
	s_nop 0
	v_cndmask_b32_e64 v38, v38, v42, s[18:19]
	v_cmp_gt_f32_e64 s[20:21], s24, v38
	s_nop 1
	v_cndmask_b32_e64 v38, v38, v43, s[20:21]
	v_cmp_ngt_f32_e64 s[22:23], s2, v38
	s_and_b64 s[62:63], s[20:21], s[22:23]
	s_and_b64 s[12:13], s[12:13], exec
	v_readfirstlane_b32 s12, v45
	s_cselect_b32 s61, 2, s12
	s_and_b64 s[12:13], s[14:15], exec
	s_cselect_b32 s14, 3, s61
	s_and_b64 s[12:13], s[16:17], exec
	s_cselect_b32 s14, 4, s14
	s_and_b64 s[12:13], s[18:19], exec
	s_cselect_b32 s14, 5, s14
	s_and_b64 s[12:13], s[20:21], exec
	s_cselect_b32 s14, 6, s14
	s_and_b64 s[12:13], s[22:23], exec
	s_cselect_b32 s61, s14, 7
	s_cmp_lg_u32 s61, 5
	s_cselect_b64 s[64:65], -1, 0
	s_cmp_lg_u32 s61, 4
	s_cselect_b64 s[20:21], -1, 0
	s_cmp_lg_u32 s61, 3
	s_cselect_b64 s[18:19], -1, 0
	s_cmp_lg_u32 s61, 2
	s_cselect_b64 s[16:17], -1, 0
	s_cmp_lg_u32 s61, 1
	s_cselect_b64 s[14:15], -1, 0
	s_cmp_eq_u32 s61, 0
	s_cselect_b64 s[12:13], -1, 0
	s_or_b64 vcc, s[12:13], vcc
	v_cndmask_b32_e32 v36, v36, v116, vcc
	v_cmp_gt_f32_e64 s[12:13], s59, v36
	s_and_b64 s[12:13], s[14:15], s[12:13]
	v_cndmask_b32_e64 v38, v44, v38, s[22:23]
	v_cndmask_b32_e64 v36, v36, v37, s[12:13]
	v_cmp_gt_f32_e64 s[14:15], s41, v36
	s_and_b64 s[14:15], s[16:17], s[14:15]
	v_cndmask_b32_e64 v37, 0, -1, vcc
	v_cndmask_b32_e64 v36, v36, v39, s[14:15]
	v_cmp_gt_f32_e64 s[16:17], s27, v36
	s_and_b64 s[16:17], s[18:19], s[16:17]
	s_nop 0
	v_cndmask_b32_e64 v36, v36, v40, s[16:17]
	v_cmp_gt_f32_e64 s[18:19], s26, v36
	s_and_b64 s[18:19], s[20:21], s[18:19]
	s_nop 0
	v_cndmask_b32_e64 v36, v36, v41, s[18:19]
	v_cmp_gt_f32_e64 s[20:21], s25, v36
	s_and_b64 s[20:21], s[64:65], s[20:21]
	s_nop 0
	v_cndmask_b32_e64 v36, v36, v42, s[20:21]
	v_cmp_ngt_f32_e64 s[24:25], s24, v36
	s_or_b64 s[24:25], s[62:63], s[24:25]
	s_nop 0
	v_cndmask_b32_e64 v36, v43, v36, s[24:25]
	v_cmp_gt_f32_e64 s[26:27], s2, v36
	s_and_b64 s[22:23], s[22:23], s[26:27]
	v_cndmask_b32_e64 v36, v36, v44, s[22:23]
	v_sub_f32_e32 v36, v36, v38
	v_readfirstlane_b32 s2, v37
	v_mul_f32_e32 v37, 0x3fb8aa3b, v36
	v_fma_f32 v38, v36, s54, -v37
	v_rndne_f32_e32 v39, v37
	v_fmac_f32_e32 v38, 0x32a5705f, v36
	v_sub_f32_e32 v37, v37, v39
	v_add_f32_e32 v37, v37, v38
	v_exp_f32_e32 v37, v37
	v_cvt_i32_f32_e32 v38, v39
	v_cmp_ngt_f32_e32 vcc, s55, v36
	s_and_b64 s[12:13], s[12:13], exec
	s_cselect_b32 s2, 1, s2
	v_ldexp_f32 v37, v37, v38
	v_cndmask_b32_e32 v37, 0, v37, vcc
	v_cmp_nlt_f32_e32 vcc, s56, v36
	s_and_b64 s[12:13], s[14:15], exec
	s_cselect_b32 s2, 2, s2
	v_cndmask_b32_e32 v36, v117, v37, vcc
	v_add_f32_e32 v36, 1.0, v36
	v_div_scale_f32 v37, s[12:13], v36, v36, 1.0
	v_rcp_f32_e32 v38, v37
	s_and_b64 s[12:13], s[16:17], exec
	s_cselect_b32 s2, 3, s2
	s_and_b64 s[12:13], s[18:19], exec
	s_cselect_b32 s2, 4, s2
	s_and_b64 s[12:13], s[20:21], exec
	v_fma_f32 v39, -v37, v38, 1.0
	s_cselect_b32 s2, 5, s2
	s_and_b64 s[12:13], s[24:25], exec
	v_fmac_f32_e32 v38, v39, v38
	v_div_scale_f32 v39, vcc, 1.0, v36, 1.0
	s_cselect_b32 s2, s2, 6
	s_and_b64 s[12:13], s[22:23], exec
	v_mul_f32_e32 v40, v39, v38
	s_cselect_b32 s2, 7, s2
	v_fma_f32 v41, -v37, v40, v39
	s_ashr_i32 s41, s40, 31
	v_fmac_f32_e32 v40, v41, v38
	s_lshl_b64 s[12:13], s[40:41], 2
	v_fma_f32 v37, -v37, v40, v39
	s_add_u32 s14, s33, s12
	v_div_fmas_f32 v37, v37, v38, v40
	s_addc_u32 s15, s35, s13
	v_div_fixup_f32 v36, v37, v36, 1.0
	s_add_u32 s12, s46, s12
	v_sub_f32_e32 v37, 1.0, v36
	s_addc_u32 s13, s47, s13
	global_store_dwordx2 v51, v[36:37], s[12:13]
	v_mbcnt_lo_u32_b32 v36, s44, 0
	v_mbcnt_hi_u32_b32 v36, s45, v36
	v_mov_b32_e32 v38, s61
	v_mov_b32_e32 v39, s2
	v_cmp_eq_u32_e32 vcc, 0, v36
	global_store_dwordx2 v51, v[38:39], s[14:15]
	s_and_saveexec_b64 s[12:13], vcc
	s_cbranch_execz .LBB0_1347
	s_lshl_b32 s14, s61, 2
	s_add_i32 s14, s14, 0
	s_add_i32 s14, s14, 0x10000
	s_bcnt1_i32_b64 s15, s[44:45]
	v_mov_b32_e32 v36, s14
	v_mov_b32_e32 v37, s15
	ds_add_u32 v36, v37

.LBB0_1485:
	s_mov_b64 s[20:21], 0x8000
	s_add_i32 m0, s62, 0x18000
	v_lshl_add_u64 v[14:15], v[4:5], 0, s[20:21]
	s_mov_b64 s[22:23], 0xa000
	s_waitcnt vmcnt(2)
	s_barrier
	global_load_lds_dwordx4 v[14:15], off
	v_lshl_add_u64 v[14:15], v[4:5], 0, s[22:23]
	s_add_i32 m0, s62, 0x1a000
	s_mov_b64 s[24:25], 0x80
	s_add_i32 s66, s62, 0x8000
	global_load_lds_dwordx4 v[14:15], off
	v_lshl_add_u64 v[6:7], v[6:7], 0, s[24:25]
	s_mov_b32 m0, s66
	s_add_i32 s67, s62, 0xa000
	global_load_lds_dwordx4 v[6:7], off
	v_lshl_add_u64 v[6:7], v[8:9], 0, s[24:25]
	s_mov_b32 m0, s67
	s_mov_b64 s[26:27], 0xc000
	global_load_lds_dwordx4 v[6:7], off
	s_add_i32 m0, s62, 0x1c000
	v_lshl_add_u64 v[6:7], v[4:5], 0, s[26:27]
	s_mov_b64 s[36:37], 0xe000
	global_load_lds_dwordx4 v[6:7], off
	v_lshl_add_u64 v[4:5], v[4:5], 0, s[36:37]
	s_add_i32 m0, s62, 0x1e000
	v_lshrrev_b32_e32 v1, 1, v0
	global_load_lds_dwordx4 v[4:5], off
	v_and_b32_e32 v5, 24, v1
	s_lshl_b32 s4, s4, 5
	v_lshlrev_b32_e32 v6, 1, v5
	v_lshlrev_b32_e32 v1, 6, v0
	s_movk_i32 s38, 0x3c0
	s_and_b32 s4, s4, 0x60
	v_and_b32_e32 v4, 15, v0
	v_and_or_b32 v7, v1, s38, v6
	v_lshlrev_b32_e32 v1, 2, v0
	v_or_b32_e32 v185, s4, v5
	v_lshlrev_b32_e32 v5, 8, v0
	v_and_b32_e32 v8, 32, v1
	v_lshl_or_b32 v1, s5, 6, v4
	v_lshl_or_b32 v4, v4, 6, v6
	v_and_b32_e32 v5, 0x18000, v5
	v_lshlrev_b32_e32 v6, 11, v11
	s_lshl_b32 s5, s5, 13
	v_or3_b32 v5, v12, v5, v6
	s_ashr_i32 s68, s34, 31
	v_bitop3_b32 v4, v4, s5, v8 bitop3:0xde
	s_lshl_b32 s5, s4, 7
	v_add_u32_e32 v168, v5, v10
	v_lshlrev_b32_e32 v5, 4, v13
	s_waitcnt vmcnt(6)
	s_cmpk_lt_u32 s2, 0x100
	v_and_b32_e32 v5, 0x38000, v5
	v_bitop3_b32 v184, s5, v7, v8 bitop3:0xf6
	s_cselect_b64 s[38:39], -1, 0
	v_or3_b32 v5, v12, v5, v6
	s_add_i32 s69, 0, 0x10000
	s_add_i32 s70, 0, 0x14000
	v_mov_b32_e32 v169, v163
	v_add_u32_e32 v170, v5, v10
	v_mov_b32_e32 v171, v163
	v_mov_b64_e32 v[172:173], s[0:1]
	s_mov_b64 s[40:41], 0x10000
	v_add_u32_e32 v186, s69, v184
	v_add_u32_e32 v187, s70, v184
	v_add_u32_e32 v188, 0, v4
	v_mov_b32_e32 v189, 0x79797979
	v_mov_b32_e32 v190, 0x7f7f7f7f
	s_movk_i32 s71, 0x1600
	s_mov_b32 s42, 0xbfb8aa3b
	s_mov_b32 s44, 0x3e000000
	s_mov_b32 s72, 0xc3e00000
	v_mov_b32_e32 v191, 0x43e00000
	s_barrier
	v_mov_b32_e32 v251, 0
	global_load_dword v250, v251, s[28:29]
	global_load_dword v250, v251, s[28:29]
	global_load_dword v250, v251, s[28:29]
	global_load_dword v250, v251, s[28:29]
	global_load_dword v250, v251, s[28:29]
	global_load_dword v250, v251, s[28:29]
	global_load_dword v250, v251, s[28:29]
	global_load_dword v250, v251, s[28:29]
	s_branch .LBB0_1488

.LBB0_1496:
	s_lshl_b64 s[50:51], s[48:49], 19
	s_add_u32 s50, s59, s50
	s_addc_u32 s51, s60, s51
	s_and_b64 s[4:5], s[4:5], exec
	s_cselect_b32 s2, s51, s57
	s_cselect_b32 s47, s50, s56
	s_add_u32 s4, s56, 0x40080
	v_lshl_add_u64 v[176:177], v[2:3], 0, s[40:41]
	s_addc_u32 s5, s57, 0
	s_mov_b32 s49, -2
	ds_read_b128 v[26:29], v186
	ds_read_b128 v[30:33], v186 offset:1024
	ds_read_b128 v[18:21], v186 offset:2048
	ds_read_b128 v[22:25], v186 offset:3072
	ds_read_b128 v[10:13], v187
	ds_read_b128 v[14:17], v187 offset:1024
	ds_read_b128 v[2:5], v187 offset:2048
	ds_read_b128 v[6:9], v187 offset:3072
	s_add_u32 s56, s4, 0xfffc0080
	s_addc_u32 s57, s5, -1
	s_cmp_eq_u32 s49, 12
	s_cselect_b64 vcc, -1, 0
	s_cselect_b32 s57, s2, s57
	s_cselect_b32 s56, s47, s56
	v_cndmask_b32_e32 v179, v177, v175, vcc
	v_cndmask_b32_e32 v178, v176, v174, vcc
	v_lshl_add_u64 v[180:181], s[4:5], 0, v[168:169]
	s_add_i32 m0, s62, 0xc000
	ds_read_b128 v[192:195], v188
	ds_read_b128 v[196:199], v188 offset:1024
	ds_read_b128 v[200:203], v188 offset:2048
	ds_read_b128 v[204:207], v188 offset:3072
	ds_read_b128 v[208:211], v188 offset:4096
	ds_read_b128 v[212:215], v188 offset:5120
	ds_read_b128 v[220:223], v188 offset:6144
	ds_read_b128 v[224:227], v188 offset:7168
	global_load_lds_dwordx4 v[180:181], off
	v_lshl_add_u64 v[180:181], s[4:5], 0, v[170:171]
	s_add_i32 m0, s62, 0xe000
	s_nop 0
	global_load_lds_dwordx4 v[180:181], off
	s_waitcnt vmcnt(16)
	s_waitcnt lgkmcnt(0)
	s_barrier
	s_waitcnt lgkmcnt(0)
	v_mfma_scale_f32_16x16x128_f8f6f4 v[158:161], v[26:33], v[192:199], 0, v189, v190 op_sel_hi:[0,0,0]
	v_mfma_scale_f32_16x16x128_f8f6f4 v[150:153], v[18:25], v[192:199], 0, v189, v190 op_sel_hi:[0,0,0]
	v_mfma_scale_f32_16x16x128_f8f6f4 v[142:145], v[26:33], v[200:207], 0, v189, v190 op_sel_hi:[0,0,0]
	v_mfma_scale_f32_16x16x128_f8f6f4 v[134:137], v[18:25], v[200:207], 0, v189, v190 op_sel_hi:[0,0,0]
	v_mfma_scale_f32_16x16x128_f8f6f4 v[126:129], v[26:33], v[208:215], 0, v189, v190 op_sel_hi:[0,0,0]
	v_mfma_scale_f32_16x16x128_f8f6f4 v[118:121], v[18:25], v[208:215], 0, v189, v190 op_sel_hi:[0,0,0]
	v_mfma_scale_f32_16x16x128_f8f6f4 v[110:113], v[26:33], v[220:227], 0, v189, v190 op_sel_hi:[0,0,0]
	v_mfma_scale_f32_16x16x128_f8f6f4 v[102:105], v[18:25], v[220:227], 0, v189, v190 op_sel_hi:[0,0,0]
	v_mfma_scale_f32_16x16x128_f8f6f4 v[154:157], v[10:17], v[192:199], 0, v189, v190 op_sel_hi:[0,0,0]
	v_mfma_scale_f32_16x16x128_f8f6f4 v[146:149], v[2:9], v[192:199], 0, v189, v190 op_sel_hi:[0,0,0]
	v_mfma_scale_f32_16x16x128_f8f6f4 v[138:141], v[10:17], v[200:207], 0, v189, v190 op_sel_hi:[0,0,0]
	v_mfma_scale_f32_16x16x128_f8f6f4 v[130:133], v[2:9], v[200:207], 0, v189, v190 op_sel_hi:[0,0,0]
	v_mfma_scale_f32_16x16x128_f8f6f4 v[122:125], v[10:17], v[208:215], 0, v189, v190 op_sel_hi:[0,0,0]
	v_mfma_scale_f32_16x16x128_f8f6f4 v[114:117], v[2:9], v[208:215], 0, v189, v190 op_sel_hi:[0,0,0]
	v_mfma_scale_f32_16x16x128_f8f6f4 v[106:109], v[10:17], v[220:227], 0, v189, v190 op_sel_hi:[0,0,0]
	v_mfma_scale_f32_16x16x128_f8f6f4 v[98:101], v[2:9], v[220:227], 0, v189, v190 op_sel_hi:[0,0,0]
	s_barrier
	s_add_i32 s73, s69, s61
	v_lshl_add_u64 v[178:179], v[178:179], 0, v[162:163]
	s_mov_b32 m0, s73
	ds_read_b128 v[192:195], v188 offset:16384
	ds_read_b128 v[196:199], v188 offset:17408
	ds_read_b128 v[200:203], v188 offset:18432
	ds_read_b128 v[204:207], v188 offset:19456
	ds_read_b128 v[208:211], v188 offset:20480
	ds_read_b128 v[212:215], v188 offset:21504
	ds_read_b128 v[220:223], v188 offset:22528
	ds_read_b128 v[224:227], v188 offset:23552
	global_load_lds_dwordx4 v[178:179], off
	v_lshl_add_u64 v[180:181], v[178:179], 0, s[10:11]
	s_add_i32 m0, s73, 0x2000
	s_add_i32 s73, s70, s61
	global_load_lds_dwordx4 v[180:181], off
	v_lshl_add_u64 v[180:181], v[178:179], 0, s[12:13]
	s_mov_b32 m0, s73
	v_lshl_add_u64 v[182:183], s[56:57], 0, v[166:167]
	global_load_lds_dwordx4 v[180:181], off
	v_lshl_add_u64 v[180:181], v[178:179], 0, s[14:15]
	s_add_i32 m0, s73, 0x2000
	s_nop 0
	global_load_lds_dwordx4 v[180:181], off
	v_lshl_add_u64 v[180:181], s[56:57], 0, v[164:165]
	s_mov_b32 m0, s62
	s_nop 0
	global_load_lds_dwordx4 v[180:181], off
	s_mov_b32 m0, s53
	s_nop 0
	global_load_lds_dwordx4 v[182:183], off
	s_waitcnt vmcnt(16)
	s_waitcnt lgkmcnt(0)
	s_barrier
	s_waitcnt lgkmcnt(0)
	v_mfma_scale_f32_16x16x128_f8f6f4 v[94:97], v[26:33], v[192:199], 0, v189, v190 op_sel_hi:[0,0,0]
	v_mfma_scale_f32_16x16x128_f8f6f4 v[86:89], v[18:25], v[192:199], 0, v189, v190 op_sel_hi:[0,0,0]
	v_mfma_scale_f32_16x16x128_f8f6f4 v[78:81], v[26:33], v[200:207], 0, v189, v190 op_sel_hi:[0,0,0]
	v_mfma_scale_f32_16x16x128_f8f6f4 v[70:73], v[18:25], v[200:207], 0, v189, v190 op_sel_hi:[0,0,0]
	v_mfma_scale_f32_16x16x128_f8f6f4 v[62:65], v[26:33], v[208:215], 0, v189, v190 op_sel_hi:[0,0,0]
	v_mfma_scale_f32_16x16x128_f8f6f4 v[54:57], v[18:25], v[208:215], 0, v189, v190 op_sel_hi:[0,0,0]
	v_mfma_scale_f32_16x16x128_f8f6f4 v[46:49], v[26:33], v[220:227], 0, v189, v190 op_sel_hi:[0,0,0]
	v_mfma_scale_f32_16x16x128_f8f6f4 v[38:41], v[18:25], v[220:227], 0, v189, v190 op_sel_hi:[0,0,0]
	v_mfma_scale_f32_16x16x128_f8f6f4 v[90:93], v[10:17], v[192:199], 0, v189, v190 op_sel_hi:[0,0,0]
	v_mfma_scale_f32_16x16x128_f8f6f4 v[82:85], v[2:9], v[192:199], 0, v189, v190 op_sel_hi:[0,0,0]
	v_mfma_scale_f32_16x16x128_f8f6f4 v[74:77], v[10:17], v[200:207], 0, v189, v190 op_sel_hi:[0,0,0]
	v_mfma_scale_f32_16x16x128_f8f6f4 v[66:69], v[2:9], v[200:207], 0, v189, v190 op_sel_hi:[0,0,0]
	v_mfma_scale_f32_16x16x128_f8f6f4 v[58:61], v[10:17], v[208:215], 0, v189, v190 op_sel_hi:[0,0,0]
	v_mfma_scale_f32_16x16x128_f8f6f4 v[50:53], v[2:9], v[208:215], 0, v189, v190 op_sel_hi:[0,0,0]
	v_mfma_scale_f32_16x16x128_f8f6f4 v[42:45], v[10:17], v[220:227], 0, v189, v190 op_sel_hi:[0,0,0]
	v_mfma_scale_f32_16x16x128_f8f6f4 v[34:37], v[2:9], v[220:227], 0, v189, v190 op_sel_hi:[0,0,0]
	s_barrier
	s_add_i32 s73, 0, 0x18000
	s_add_i32 s74, 0, 0x1c000
	v_add_u32_e32 v14, s73, v184
	v_add_u32_e32 v30, s74, v184
	ds_read_b128 v[2:5], v14
	ds_read_b128 v[6:9], v14 offset:1024
	ds_read_b128 v[10:13], v14 offset:2048
	ds_read_b128 v[14:17], v14 offset:3072
	ds_read_b128 v[18:21], v30
	ds_read_b128 v[22:25], v30 offset:1024
	ds_read_b128 v[26:29], v30 offset:2048
	ds_read_b128 v[30:33], v30 offset:3072
	s_add_u32 s56, s56, 0x40000
	s_addc_u32 s57, s57, 0
	s_mov_b32 m0, s63
	v_lshl_add_u64 v[216:217], s[56:57], 0, v[164:165]
	ds_read_b128 v[192:195], v188 offset:32768
	ds_read_b128 v[196:199], v188 offset:33792
	ds_read_b128 v[200:203], v188 offset:34816
	ds_read_b128 v[204:207], v188 offset:35840
	ds_read_b128 v[208:211], v188 offset:36864
	ds_read_b128 v[212:215], v188 offset:37888
	ds_read_b128 v[220:223], v188 offset:38912
	ds_read_b128 v[224:227], v188 offset:39936
	global_load_lds_dwordx4 v[216:217], off
	v_lshl_add_u64 v[216:217], s[56:57], 0, v[166:167]
	s_mov_b32 m0, s64
	s_nop 0
	global_load_lds_dwordx4 v[216:217], off
	s_waitcnt vmcnt(8)
	s_waitcnt lgkmcnt(0)
	s_barrier
	s_waitcnt lgkmcnt(0)
	v_mfma_scale_f32_16x16x128_f8f6f4 v[158:161], v[2:9], v[192:199], v[158:161], v189, v190 op_sel_hi:[0,0,0]
	v_mfma_scale_f32_16x16x128_f8f6f4 v[150:153], v[10:17], v[192:199], v[150:153], v189, v190 op_sel_hi:[0,0,0]
	v_mfma_scale_f32_16x16x128_f8f6f4 v[142:145], v[2:9], v[200:207], v[142:145], v189, v190 op_sel_hi:[0,0,0]
	v_mfma_scale_f32_16x16x128_f8f6f4 v[134:137], v[10:17], v[200:207], v[134:137], v189, v190 op_sel_hi:[0,0,0]
	v_mfma_scale_f32_16x16x128_f8f6f4 v[126:129], v[2:9], v[208:215], v[126:129], v189, v190 op_sel_hi:[0,0,0]
	v_mfma_scale_f32_16x16x128_f8f6f4 v[118:121], v[10:17], v[208:215], v[118:121], v189, v190 op_sel_hi:[0,0,0]
	v_mfma_scale_f32_16x16x128_f8f6f4 v[110:113], v[2:9], v[220:227], v[110:113], v189, v190 op_sel_hi:[0,0,0]
	v_mfma_scale_f32_16x16x128_f8f6f4 v[102:105], v[10:17], v[220:227], v[102:105], v189, v190 op_sel_hi:[0,0,0]
	v_mfma_scale_f32_16x16x128_f8f6f4 v[154:157], v[18:25], v[192:199], v[154:157], v189, v190 op_sel_hi:[0,0,0]
	v_mfma_scale_f32_16x16x128_f8f6f4 v[146:149], v[26:33], v[192:199], v[146:149], v189, v190 op_sel_hi:[0,0,0]
	v_mfma_scale_f32_16x16x128_f8f6f4 v[138:141], v[18:25], v[200:207], v[138:141], v189, v190 op_sel_hi:[0,0,0]
	v_mfma_scale_f32_16x16x128_f8f6f4 v[130:133], v[26:33], v[200:207], v[130:133], v189, v190 op_sel_hi:[0,0,0]
	v_mfma_scale_f32_16x16x128_f8f6f4 v[122:125], v[18:25], v[208:215], v[122:125], v189, v190 op_sel_hi:[0,0,0]
	v_mfma_scale_f32_16x16x128_f8f6f4 v[114:117], v[26:33], v[208:215], v[114:117], v189, v190 op_sel_hi:[0,0,0]
	v_mfma_scale_f32_16x16x128_f8f6f4 v[106:109], v[18:25], v[220:227], v[106:109], v189, v190 op_sel_hi:[0,0,0]
	v_mfma_scale_f32_16x16x128_f8f6f4 v[98:101], v[26:33], v[220:227], v[98:101], v189, v190 op_sel_hi:[0,0,0]
	s_barrier
	s_add_i32 s56, s73, s61
	v_lshl_add_u64 v[216:217], v[178:179], 0, s[20:21]
	s_mov_b32 m0, s56
	ds_read_b128 v[192:195], v188 offset:49152
	ds_read_b128 v[196:199], v188 offset:50176
	ds_read_b128 v[200:203], v188 offset:51200
	ds_read_b128 v[204:207], v188 offset:52224
	ds_read_b128 v[208:211], v188 offset:53248
	ds_read_b128 v[212:215], v188 offset:54272
	ds_read_b128 v[220:223], v188 offset:55296
	ds_read_b128 v[224:227], v188 offset:56320
	global_load_lds_dwordx4 v[216:217], off
	v_lshl_add_u64 v[216:217], v[178:179], 0, s[22:23]
	s_add_i32 m0, s56, 0x2000
	s_add_i32 s56, s74, s61
	global_load_lds_dwordx4 v[216:217], off
	v_lshl_add_u64 v[216:217], v[178:179], 0, s[26:27]
	s_mov_b32 m0, s56
	v_lshl_add_u64 v[178:179], v[178:179], 0, s[36:37]
	global_load_lds_dwordx4 v[216:217], off
	s_add_i32 m0, s56, 0x2000
	s_nop 0
	global_load_lds_dwordx4 v[178:179], off
	v_lshl_add_u64 v[178:179], v[180:181], 0, s[24:25]
	s_mov_b32 m0, s66
	s_nop 0
	global_load_lds_dwordx4 v[178:179], off
	v_lshl_add_u64 v[178:179], v[182:183], 0, s[24:25]
	s_mov_b32 m0, s67
	s_nop 0
	global_load_lds_dwordx4 v[178:179], off
	s_waitcnt vmcnt(8)
	s_waitcnt lgkmcnt(0)
	s_barrier
	s_waitcnt lgkmcnt(0)
	v_mfma_scale_f32_16x16x128_f8f6f4 v[94:97], v[2:9], v[192:199], v[94:97], v189, v190 op_sel_hi:[0,0,0]
	v_mfma_scale_f32_16x16x128_f8f6f4 v[86:89], v[10:17], v[192:199], v[86:89], v189, v190 op_sel_hi:[0,0,0]
	v_mfma_scale_f32_16x16x128_f8f6f4 v[78:81], v[2:9], v[200:207], v[78:81], v189, v190 op_sel_hi:[0,0,0]
	v_mfma_scale_f32_16x16x128_f8f6f4 v[70:73], v[10:17], v[200:207], v[70:73], v189, v190 op_sel_hi:[0,0,0]
	v_mfma_scale_f32_16x16x128_f8f6f4 v[62:65], v[2:9], v[208:215], v[62:65], v189, v190 op_sel_hi:[0,0,0]
	v_mfma_scale_f32_16x16x128_f8f6f4 v[54:57], v[10:17], v[208:215], v[54:57], v189, v190 op_sel_hi:[0,0,0]
	v_mfma_scale_f32_16x16x128_f8f6f4 v[46:49], v[2:9], v[220:227], v[46:49], v189, v190 op_sel_hi:[0,0,0]
	v_mfma_scale_f32_16x16x128_f8f6f4 v[38:41], v[10:17], v[220:227], v[38:41], v189, v190 op_sel_hi:[0,0,0]
	v_mfma_scale_f32_16x16x128_f8f6f4 v[90:93], v[18:25], v[192:199], v[90:93], v189, v190 op_sel_hi:[0,0,0]
	v_mfma_scale_f32_16x16x128_f8f6f4 v[82:85], v[26:33], v[192:199], v[82:85], v189, v190 op_sel_hi:[0,0,0]
	v_mfma_scale_f32_16x16x128_f8f6f4 v[74:77], v[18:25], v[200:207], v[74:77], v189, v190 op_sel_hi:[0,0,0]
	v_mfma_scale_f32_16x16x128_f8f6f4 v[66:69], v[26:33], v[200:207], v[66:69], v189, v190 op_sel_hi:[0,0,0]
	v_mfma_scale_f32_16x16x128_f8f6f4 v[58:61], v[18:25], v[208:215], v[58:61], v189, v190 op_sel_hi:[0,0,0]
	v_mfma_scale_f32_16x16x128_f8f6f4 v[50:53], v[26:33], v[208:215], v[50:53], v189, v190 op_sel_hi:[0,0,0]
	v_mfma_scale_f32_16x16x128_f8f6f4 v[42:45], v[18:25], v[220:227], v[42:45], v189, v190 op_sel_hi:[0,0,0]
	v_mfma_scale_f32_16x16x128_f8f6f4 v[34:37], v[26:33], v[220:227], v[34:37], v189, v190 op_sel_hi:[0,0,0]
	s_barrier
	s_add_i32 s49, s49, 2
	s_add_u32 s4, s4, 0x100
	s_addc_u32 s5, s5, 0
	s_cmp_gt_u32 s49, 13
	v_lshl_add_u64 v[176:177], v[176:177], 0, s[40:41]

.LBB0_1500:
	v_pk_mul_f32 v[10:11], v[160:161], s[42:43] op_sel_hi:[1,0]
	v_pk_mul_f32 v[8:9], v[158:159], s[42:43] op_sel_hi:[1,0]
	v_exp_f32_e32 v10, v10
	v_exp_f32_e32 v11, v11
	v_exp_f32_e32 v8, v8
	v_exp_f32_e32 v9, v9
	v_pk_mul_f32 v[12:13], v[160:161], v[156:157]
	v_pk_fma_f32 v[10:11], v[10:11], s[44:45], s[44:45] op_sel_hi:[1,0,0]
	v_pk_mul_f32 v[14:15], v[158:159], v[154:155]
	v_rcp_f32_e32 v10, v10
	v_rcp_f32_e32 v11, v11
	v_pk_fma_f32 v[8:9], v[8:9], s[44:45], s[44:45] op_sel_hi:[1,0,0]
	v_pk_mul_f32 v[18:19], v[150:151], v[146:147]
	v_rcp_f32_e32 v8, v8
	v_rcp_f32_e32 v9, v9
	v_pk_mul_f32 v[10:11], v[12:13], v[10:11]
	v_pk_mul_f32 v[12:13], v[150:151], s[42:43] op_sel_hi:[1,0]
	v_pk_mul_f32 v[16:17], v[152:153], v[148:149]
	v_exp_f32_e32 v12, v12
	v_exp_f32_e32 v13, v13
	v_pk_mul_f32 v[8:9], v[14:15], v[8:9]
	v_pk_mul_f32 v[14:15], v[152:153], s[42:43] op_sel_hi:[1,0]
	v_med3_f32 v7, v8, s72, v191
	v_exp_f32_e32 v14, v14
	v_exp_f32_e32 v15, v15
	v_pk_fma_f32 v[12:13], v[12:13], s[44:45], s[44:45] op_sel_hi:[1,0,0]
	v_med3_f32 v9, v9, s72, v191
	v_rcp_f32_e32 v12, v12
	v_rcp_f32_e32 v13, v13
	v_pk_fma_f32 v[14:15], v[14:15], s[44:45], s[44:45] op_sel_hi:[1,0,0]
	v_rcp_f32_e32 v14, v14
	v_rcp_f32_e32 v15, v15
	v_pk_mul_f32 v[12:13], v[18:19], v[12:13]
	v_cvt_pk_fp8_f32 v8, v7, v9
	v_med3_f32 v7, v10, s72, v191
	v_med3_f32 v10, v11, s72, v191
	v_med3_f32 v11, v12, s72, v191
	v_med3_f32 v12, v13, s72, v191
	v_cvt_pk_fp8_f32 v9, v11, v12
	v_pk_mul_f32 v[14:15], v[16:17], v[14:15]
	v_readlane_b32 s4, v254, 56
	v_cvt_pk_fp8_f32 v8, v7, v10 op_sel:[0,0,1]
	v_med3_f32 v7, v14, s72, v191
	v_med3_f32 v10, v15, s72, v191
	v_readlane_b32 s5, v254, 57
	v_cvt_pk_fp8_f32 v9, v7, v10 op_sel:[0,0,1]
	v_lshl_add_u32 v6, s54, 8, v1
	v_lshl_or_b32 v2, s52, 7, v185
	v_mov_b64_e32 v[4:5], s[4:5]
	v_ashrrev_i32_e32 v3, 31, v2
	v_mad_i64_i32 v[10:11], s[4:5], v6, s71, v[4:5]
	v_lshl_add_u64 v[10:11], v[10:11], 0, v[2:3]
	s_nop 15
	s_nop 15
	global_store_dwordx2 v[10:11], v[8:9], off
	v_pk_mul_f32 v[8:9], v[142:143], s[42:43] op_sel_hi:[1,0]
	v_pk_mul_f32 v[10:11], v[144:145], s[42:43] op_sel_hi:[1,0]
	v_exp_f32_e32 v8, v8
	v_exp_f32_e32 v9, v9
	v_exp_f32_e32 v10, v10
	v_exp_f32_e32 v11, v11
	v_pk_mul_f32 v[12:13], v[144:145], v[140:141]
	v_pk_fma_f32 v[8:9], v[8:9], s[44:45], s[44:45] op_sel_hi:[1,0,0]
	v_pk_mul_f32 v[14:15], v[142:143], v[138:139]
	v_pk_fma_f32 v[10:11], v[10:11], s[44:45], s[44:45] op_sel_hi:[1,0,0]
	v_rcp_f32_e32 v8, v8
	v_rcp_f32_e32 v9, v9
	v_rcp_f32_e32 v10, v10
	v_rcp_f32_e32 v11, v11
	v_pk_mul_f32 v[16:17], v[136:137], v[132:133]
	v_pk_mul_f32 v[8:9], v[14:15], v[8:9]
	v_pk_mul_f32 v[14:15], v[136:137], s[42:43] op_sel_hi:[1,0]
	v_pk_mul_f32 v[10:11], v[12:13], v[10:11]
	v_pk_mul_f32 v[12:13], v[134:135], s[42:43] op_sel_hi:[1,0]
	v_exp_f32_e32 v14, v14
	v_exp_f32_e32 v12, v12
	v_exp_f32_e32 v13, v13
	v_exp_f32_e32 v15, v15
	v_pk_mul_f32 v[18:19], v[134:135], v[130:131]
	v_med3_f32 v9, v9, s72, v191
	v_pk_fma_f32 v[12:13], v[12:13], s[44:45], s[44:45] op_sel_hi:[1,0,0]
	v_pk_fma_f32 v[14:15], v[14:15], s[44:45], s[44:45] op_sel_hi:[1,0,0]
	v_rcp_f32_e32 v12, v12
	v_rcp_f32_e32 v13, v13
	v_rcp_f32_e32 v14, v14
	v_rcp_f32_e32 v15, v15
	v_med3_f32 v10, v10, s72, v191
	v_pk_mul_f32 v[12:13], v[18:19], v[12:13]
	v_med3_f32 v11, v11, s72, v191
	v_pk_mul_f32 v[14:15], v[16:17], v[14:15]
	v_med3_f32 v16, v8, s72, v191
	v_cvt_pk_fp8_f32 v8, v16, v9
	v_med3_f32 v12, v12, s72, v191
	v_med3_f32 v13, v13, s72, v191
	v_cvt_pk_fp8_f32 v9, v12, v13
	v_cvt_pk_fp8_f32 v8, v10, v11 op_sel:[0,0,1]
	v_med3_f32 v10, v14, s72, v191
	v_med3_f32 v11, v15, s72, v191
	v_cvt_pk_fp8_f32 v9, v10, v11 op_sel:[0,0,1]
	v_or_b32_e32 v7, 16, v6
	v_mad_i64_i32 v[10:11], s[4:5], v7, s71, v[4:5]
	v_lshl_add_u64 v[10:11], v[10:11], 0, v[2:3]
	global_store_dwordx2 v[10:11], v[8:9], off
	v_pk_mul_f32 v[8:9], v[126:127], s[42:43] op_sel_hi:[1,0]
	v_pk_mul_f32 v[10:11], v[128:129], s[42:43] op_sel_hi:[1,0]
	v_exp_f32_e32 v8, v8
	v_exp_f32_e32 v9, v9
	v_exp_f32_e32 v10, v10
	v_exp_f32_e32 v11, v11
	v_pk_mul_f32 v[12:13], v[128:129], v[124:125]
	v_pk_fma_f32 v[8:9], v[8:9], s[44:45], s[44:45] op_sel_hi:[1,0,0]
	v_pk_mul_f32 v[14:15], v[126:127], v[122:123]
	v_pk_fma_f32 v[10:11], v[10:11], s[44:45], s[44:45] op_sel_hi:[1,0,0]
	v_rcp_f32_e32 v8, v8
	v_rcp_f32_e32 v9, v9
	v_rcp_f32_e32 v10, v10
	v_rcp_f32_e32 v11, v11
	v_pk_mul_f32 v[16:17], v[120:121], v[116:117]
	v_pk_mul_f32 v[8:9], v[14:15], v[8:9]
	v_pk_mul_f32 v[14:15], v[120:121], s[42:43] op_sel_hi:[1,0]
	v_pk_mul_f32 v[10:11], v[12:13], v[10:11]
	v_pk_mul_f32 v[12:13], v[118:119], s[42:43] op_sel_hi:[1,0]
	v_exp_f32_e32 v14, v14
	v_exp_f32_e32 v12, v12
	v_exp_f32_e32 v13, v13
	v_exp_f32_e32 v15, v15
	v_pk_mul_f32 v[18:19], v[118:119], v[114:115]
	v_med3_f32 v9, v9, s72, v191
	v_pk_fma_f32 v[12:13], v[12:13], s[44:45], s[44:45] op_sel_hi:[1,0,0]
	v_pk_fma_f32 v[14:15], v[14:15], s[44:45], s[44:45] op_sel_hi:[1,0,0]
	v_rcp_f32_e32 v12, v12
	v_rcp_f32_e32 v13, v13
	v_rcp_f32_e32 v14, v14
	v_rcp_f32_e32 v15, v15
	v_med3_f32 v10, v10, s72, v191
	v_pk_mul_f32 v[12:13], v[18:19], v[12:13]
	v_med3_f32 v11, v11, s72, v191
	v_pk_mul_f32 v[14:15], v[16:17], v[14:15]
	v_med3_f32 v16, v8, s72, v191
	v_cvt_pk_fp8_f32 v8, v16, v9
	v_med3_f32 v12, v12, s72, v191
	v_med3_f32 v13, v13, s72, v191
	v_cvt_pk_fp8_f32 v9, v12, v13
	v_cvt_pk_fp8_f32 v8, v10, v11 op_sel:[0,0,1]
	v_med3_f32 v10, v14, s72, v191
	v_med3_f32 v11, v15, s72, v191
	v_cvt_pk_fp8_f32 v9, v10, v11 op_sel:[0,0,1]
	v_or_b32_e32 v7, 32, v6
	v_mad_i64_i32 v[10:11], s[4:5], v7, s71, v[4:5]
	v_lshl_add_u64 v[10:11], v[10:11], 0, v[2:3]
	global_store_dwordx2 v[10:11], v[8:9], off
	v_pk_mul_f32 v[8:9], v[110:111], s[42:43] op_sel_hi:[1,0]
	v_pk_mul_f32 v[10:11], v[112:113], s[42:43] op_sel_hi:[1,0]
	v_exp_f32_e32 v8, v8
	v_exp_f32_e32 v9, v9
	v_exp_f32_e32 v10, v10
	v_exp_f32_e32 v11, v11
	v_pk_mul_f32 v[12:13], v[112:113], v[108:109]
	v_pk_fma_f32 v[8:9], v[8:9], s[44:45], s[44:45] op_sel_hi:[1,0,0]
	v_pk_mul_f32 v[14:15], v[110:111], v[106:107]
	v_pk_fma_f32 v[10:11], v[10:11], s[44:45], s[44:45] op_sel_hi:[1,0,0]
	v_rcp_f32_e32 v8, v8
	v_rcp_f32_e32 v9, v9
	v_rcp_f32_e32 v10, v10
	v_rcp_f32_e32 v11, v11
	v_pk_mul_f32 v[16:17], v[104:105], v[100:101]
	v_pk_mul_f32 v[8:9], v[14:15], v[8:9]
	v_pk_mul_f32 v[14:15], v[104:105], s[42:43] op_sel_hi:[1,0]
	v_pk_mul_f32 v[10:11], v[12:13], v[10:11]
	v_pk_mul_f32 v[12:13], v[102:103], s[42:43] op_sel_hi:[1,0]
	v_exp_f32_e32 v14, v14
	v_exp_f32_e32 v12, v12
	v_exp_f32_e32 v13, v13
	v_exp_f32_e32 v15, v15
	v_pk_mul_f32 v[18:19], v[102:103], v[98:99]
	v_med3_f32 v9, v9, s72, v191
	v_pk_fma_f32 v[12:13], v[12:13], s[44:45], s[44:45] op_sel_hi:[1,0,0]
	v_pk_fma_f32 v[14:15], v[14:15], s[44:45], s[44:45] op_sel_hi:[1,0,0]
	v_rcp_f32_e32 v12, v12
	v_rcp_f32_e32 v13, v13
	v_rcp_f32_e32 v14, v14
	v_rcp_f32_e32 v15, v15
	v_med3_f32 v10, v10, s72, v191
	v_pk_mul_f32 v[12:13], v[18:19], v[12:13]
	v_med3_f32 v11, v11, s72, v191
	v_pk_mul_f32 v[14:15], v[16:17], v[14:15]
	v_med3_f32 v16, v8, s72, v191
	v_cvt_pk_fp8_f32 v8, v16, v9
	v_med3_f32 v12, v12, s72, v191
	v_med3_f32 v13, v13, s72, v191
	v_cvt_pk_fp8_f32 v9, v12, v13
	v_cvt_pk_fp8_f32 v8, v10, v11 op_sel:[0,0,1]
	v_med3_f32 v10, v14, s72, v191
	v_med3_f32 v11, v15, s72, v191
	v_cvt_pk_fp8_f32 v9, v10, v11 op_sel:[0,0,1]
	v_or_b32_e32 v7, 48, v6
	v_mad_i64_i32 v[10:11], s[4:5], v7, s71, v[4:5]
	v_lshl_add_u64 v[10:11], v[10:11], 0, v[2:3]
	global_store_dwordx2 v[10:11], v[8:9], off
	v_pk_mul_f32 v[8:9], v[94:95], s[42:43] op_sel_hi:[1,0]
	v_pk_mul_f32 v[10:11], v[96:97], s[42:43] op_sel_hi:[1,0]
	v_exp_f32_e32 v8, v8
	v_exp_f32_e32 v9, v9
	v_exp_f32_e32 v10, v10
	v_exp_f32_e32 v11, v11
	v_pk_mul_f32 v[12:13], v[96:97], v[92:93]
	v_pk_fma_f32 v[8:9], v[8:9], s[44:45], s[44:45] op_sel_hi:[1,0,0]
	v_pk_mul_f32 v[14:15], v[94:95], v[90:91]
	v_pk_fma_f32 v[10:11], v[10:11], s[44:45], s[44:45] op_sel_hi:[1,0,0]
	v_rcp_f32_e32 v8, v8
	v_rcp_f32_e32 v9, v9
	v_rcp_f32_e32 v10, v10
	v_rcp_f32_e32 v11, v11
	v_pk_mul_f32 v[16:17], v[88:89], v[84:85]
	v_pk_mul_f32 v[8:9], v[14:15], v[8:9]
	v_pk_mul_f32 v[14:15], v[88:89], s[42:43] op_sel_hi:[1,0]
	v_pk_mul_f32 v[10:11], v[12:13], v[10:11]
	v_pk_mul_f32 v[12:13], v[86:87], s[42:43] op_sel_hi:[1,0]
	v_exp_f32_e32 v14, v14
	v_exp_f32_e32 v12, v12
	v_exp_f32_e32 v13, v13
	v_exp_f32_e32 v15, v15
	v_pk_mul_f32 v[18:19], v[86:87], v[82:83]
	v_med3_f32 v9, v9, s72, v191
	v_pk_fma_f32 v[12:13], v[12:13], s[44:45], s[44:45] op_sel_hi:[1,0,0]
	v_pk_fma_f32 v[14:15], v[14:15], s[44:45], s[44:45] op_sel_hi:[1,0,0]
	v_rcp_f32_e32 v12, v12
	v_rcp_f32_e32 v13, v13
	v_rcp_f32_e32 v14, v14
	v_rcp_f32_e32 v15, v15
	v_med3_f32 v10, v10, s72, v191
	v_pk_mul_f32 v[12:13], v[18:19], v[12:13]
	v_med3_f32 v11, v11, s72, v191
	v_pk_mul_f32 v[14:15], v[16:17], v[14:15]
	v_med3_f32 v16, v8, s72, v191
	v_cvt_pk_fp8_f32 v8, v16, v9
	v_med3_f32 v12, v12, s72, v191
	v_med3_f32 v13, v13, s72, v191
	v_cvt_pk_fp8_f32 v9, v12, v13
	v_cvt_pk_fp8_f32 v8, v10, v11 op_sel:[0,0,1]
	v_med3_f32 v10, v14, s72, v191
	v_med3_f32 v11, v15, s72, v191
	v_cvt_pk_fp8_f32 v9, v10, v11 op_sel:[0,0,1]
	v_add_u32_e32 v7, 0x80, v6
	v_mad_i64_i32 v[10:11], s[4:5], v7, s71, v[4:5]
	v_lshl_add_u64 v[10:11], v[10:11], 0, v[2:3]
	global_store_dwordx2 v[10:11], v[8:9], off
	v_pk_mul_f32 v[8:9], v[78:79], s[42:43] op_sel_hi:[1,0]
	v_pk_mul_f32 v[10:11], v[80:81], s[42:43] op_sel_hi:[1,0]
	v_exp_f32_e32 v8, v8
	v_exp_f32_e32 v9, v9
	v_exp_f32_e32 v10, v10
	v_exp_f32_e32 v11, v11
	v_pk_mul_f32 v[12:13], v[80:81], v[76:77]
	v_pk_fma_f32 v[8:9], v[8:9], s[44:45], s[44:45] op_sel_hi:[1,0,0]
	v_pk_mul_f32 v[14:15], v[78:79], v[74:75]
	v_pk_fma_f32 v[10:11], v[10:11], s[44:45], s[44:45] op_sel_hi:[1,0,0]
	v_rcp_f32_e32 v8, v8
	v_rcp_f32_e32 v9, v9
	v_rcp_f32_e32 v10, v10
	v_rcp_f32_e32 v11, v11
	v_pk_mul_f32 v[16:17], v[72:73], v[68:69]
	v_pk_mul_f32 v[8:9], v[14:15], v[8:9]
	v_pk_mul_f32 v[14:15], v[72:73], s[42:43] op_sel_hi:[1,0]
	v_pk_mul_f32 v[10:11], v[12:13], v[10:11]
	v_pk_mul_f32 v[12:13], v[70:71], s[42:43] op_sel_hi:[1,0]
	v_exp_f32_e32 v14, v14
	v_exp_f32_e32 v12, v12
	v_exp_f32_e32 v13, v13
	v_exp_f32_e32 v15, v15
	v_pk_mul_f32 v[18:19], v[70:71], v[66:67]
	v_med3_f32 v9, v9, s72, v191
	v_pk_fma_f32 v[12:13], v[12:13], s[44:45], s[44:45] op_sel_hi:[1,0,0]
	v_pk_fma_f32 v[14:15], v[14:15], s[44:45], s[44:45] op_sel_hi:[1,0,0]
	v_rcp_f32_e32 v12, v12
	v_rcp_f32_e32 v13, v13
	v_rcp_f32_e32 v14, v14
	v_rcp_f32_e32 v15, v15
	v_med3_f32 v10, v10, s72, v191
	v_pk_mul_f32 v[12:13], v[18:19], v[12:13]
	v_med3_f32 v11, v11, s72, v191
	v_pk_mul_f32 v[14:15], v[16:17], v[14:15]
	v_med3_f32 v16, v8, s72, v191
	v_cvt_pk_fp8_f32 v8, v16, v9
	v_med3_f32 v12, v12, s72, v191
	v_med3_f32 v13, v13, s72, v191
	v_cvt_pk_fp8_f32 v9, v12, v13
	v_cvt_pk_fp8_f32 v8, v10, v11 op_sel:[0,0,1]
	v_med3_f32 v10, v14, s72, v191
	v_med3_f32 v11, v15, s72, v191
	v_cvt_pk_fp8_f32 v9, v10, v11 op_sel:[0,0,1]
	v_add_u32_e32 v7, 0x90, v6
	v_mad_i64_i32 v[10:11], s[4:5], v7, s71, v[4:5]
	v_lshl_add_u64 v[10:11], v[10:11], 0, v[2:3]
	global_store_dwordx2 v[10:11], v[8:9], off
	v_pk_mul_f32 v[8:9], v[62:63], s[42:43] op_sel_hi:[1,0]
	v_pk_mul_f32 v[10:11], v[64:65], s[42:43] op_sel_hi:[1,0]
	v_exp_f32_e32 v8, v8
	v_exp_f32_e32 v9, v9
	v_exp_f32_e32 v10, v10
	v_exp_f32_e32 v11, v11
	v_pk_mul_f32 v[12:13], v[64:65], v[60:61]
	v_pk_fma_f32 v[8:9], v[8:9], s[44:45], s[44:45] op_sel_hi:[1,0,0]
	v_pk_mul_f32 v[14:15], v[62:63], v[58:59]
	v_pk_fma_f32 v[10:11], v[10:11], s[44:45], s[44:45] op_sel_hi:[1,0,0]
	v_rcp_f32_e32 v8, v8
	v_rcp_f32_e32 v9, v9
	v_rcp_f32_e32 v10, v10
	v_rcp_f32_e32 v11, v11
	v_pk_mul_f32 v[16:17], v[56:57], v[52:53]
	v_pk_mul_f32 v[8:9], v[14:15], v[8:9]
	v_pk_mul_f32 v[14:15], v[56:57], s[42:43] op_sel_hi:[1,0]
	v_pk_mul_f32 v[10:11], v[12:13], v[10:11]
	v_pk_mul_f32 v[12:13], v[54:55], s[42:43] op_sel_hi:[1,0]
	v_exp_f32_e32 v14, v14
	v_exp_f32_e32 v12, v12
	v_exp_f32_e32 v13, v13
	v_exp_f32_e32 v15, v15
	v_pk_mul_f32 v[18:19], v[54:55], v[50:51]
	v_med3_f32 v9, v9, s72, v191
	v_pk_fma_f32 v[12:13], v[12:13], s[44:45], s[44:45] op_sel_hi:[1,0,0]
	v_pk_fma_f32 v[14:15], v[14:15], s[44:45], s[44:45] op_sel_hi:[1,0,0]
	v_rcp_f32_e32 v12, v12
	v_rcp_f32_e32 v13, v13
	v_rcp_f32_e32 v14, v14
	v_rcp_f32_e32 v15, v15
	v_med3_f32 v10, v10, s72, v191
	v_pk_mul_f32 v[12:13], v[18:19], v[12:13]
	v_med3_f32 v11, v11, s72, v191
	v_pk_mul_f32 v[14:15], v[16:17], v[14:15]
	v_med3_f32 v16, v8, s72, v191
	v_cvt_pk_fp8_f32 v8, v16, v9
	v_med3_f32 v12, v12, s72, v191
	v_med3_f32 v13, v13, s72, v191
	v_cvt_pk_fp8_f32 v9, v12, v13
	v_cvt_pk_fp8_f32 v8, v10, v11 op_sel:[0,0,1]
	v_med3_f32 v10, v14, s72, v191
	v_med3_f32 v11, v15, s72, v191
	v_cvt_pk_fp8_f32 v9, v10, v11 op_sel:[0,0,1]
	v_add_u32_e32 v7, 0xa0, v6
	v_mad_i64_i32 v[10:11], s[4:5], v7, s71, v[4:5]
	v_lshl_add_u64 v[10:11], v[10:11], 0, v[2:3]
	global_store_dwordx2 v[10:11], v[8:9], off
	v_add_u32_e32 v18, 0xb0, v6
	v_pk_mul_f32 v[6:7], v[46:47], s[42:43] op_sel_hi:[1,0]
	v_pk_mul_f32 v[8:9], v[48:49], s[42:43] op_sel_hi:[1,0]
	v_exp_f32_e32 v6, v6
	v_exp_f32_e32 v7, v7
	v_exp_f32_e32 v8, v8
	v_exp_f32_e32 v9, v9
	v_pk_mul_f32 v[10:11], v[48:49], v[44:45]
	v_pk_fma_f32 v[6:7], v[6:7], s[44:45], s[44:45] op_sel_hi:[1,0,0]
	v_pk_mul_f32 v[12:13], v[46:47], v[42:43]
	v_pk_fma_f32 v[8:9], v[8:9], s[44:45], s[44:45] op_sel_hi:[1,0,0]
	v_rcp_f32_e32 v6, v6
	v_rcp_f32_e32 v7, v7
	v_rcp_f32_e32 v8, v8
	v_rcp_f32_e32 v9, v9
	v_pk_mul_f32 v[14:15], v[40:41], v[36:37]
	v_pk_mul_f32 v[6:7], v[12:13], v[6:7]
	v_pk_mul_f32 v[12:13], v[40:41], s[42:43] op_sel_hi:[1,0]
	v_pk_mul_f32 v[8:9], v[10:11], v[8:9]
	v_pk_mul_f32 v[10:11], v[38:39], s[42:43] op_sel_hi:[1,0]
	v_exp_f32_e32 v12, v12
	v_exp_f32_e32 v10, v10
	v_exp_f32_e32 v11, v11
	v_exp_f32_e32 v13, v13
	v_pk_mul_f32 v[16:17], v[38:39], v[34:35]
	v_med3_f32 v7, v7, s72, v191
	v_pk_fma_f32 v[10:11], v[10:11], s[44:45], s[44:45] op_sel_hi:[1,0,0]
	v_pk_fma_f32 v[12:13], v[12:13], s[44:45], s[44:45] op_sel_hi:[1,0,0]
	v_rcp_f32_e32 v10, v10
	v_rcp_f32_e32 v11, v11
	v_rcp_f32_e32 v12, v12
	v_rcp_f32_e32 v13, v13
	v_med3_f32 v8, v8, s72, v191
	v_pk_mul_f32 v[10:11], v[16:17], v[10:11]
	v_med3_f32 v9, v9, s72, v191
	v_pk_mul_f32 v[12:13], v[14:15], v[12:13]
	v_med3_f32 v14, v6, s72, v191
	v_cvt_pk_fp8_f32 v6, v14, v7
	v_med3_f32 v10, v10, s72, v191
	v_med3_f32 v11, v11, s72, v191
	v_cvt_pk_fp8_f32 v7, v10, v11
	v_cvt_pk_fp8_f32 v6, v8, v9 op_sel:[0,0,1]
	v_med3_f32 v8, v12, s72, v191
	v_med3_f32 v9, v13, s72, v191
	v_cvt_pk_fp8_f32 v7, v8, v9 op_sel:[0,0,1]
	v_mad_i64_i32 v[4:5], s[4:5], v18, s71, v[4:5]
	v_lshl_add_u64 v[2:3], v[4:5], 0, v[2:3]
	s_and_b64 vcc, exec, s[0:1]
	s_mov_b64 s[0:1], -1
	global_store_dwordx2 v[2:3], v[6:7], off
	s_cbranch_vccnz .LBB0_1487
	s_andn2_b64 vcc, exec, s[18:19]
	s_cbranch_vccnz .LBB0_1486
	s_barrier
	s_branch .LBB0_1486

.LBB0_1558:
	s_add_u32 s22, s28, 0x40a00000
	s_mov_b64 s[24:25], 0x8000
	s_addc_u32 s23, s29, 0
	s_add_i32 m0, s61, 0x18000
	v_lshl_add_u64 v[14:15], v[4:5], 0, s[24:25]
	s_mov_b64 s[26:27], 0xa000
	s_waitcnt vmcnt(2)
	s_barrier
	global_load_lds_dwordx4 v[14:15], off
	v_lshl_add_u64 v[14:15], v[4:5], 0, s[26:27]
	s_add_i32 m0, s61, 0x1a000
	s_mov_b64 s[36:37], 0x80
	s_add_i32 s66, s61, 0x8000
	global_load_lds_dwordx4 v[14:15], off
	v_lshl_add_u64 v[8:9], v[8:9], 0, s[36:37]
	s_mov_b32 m0, s66
	s_add_i32 s67, s61, 0xa000
	global_load_lds_dwordx4 v[8:9], off
	v_lshl_add_u64 v[6:7], v[6:7], 0, s[36:37]
	s_mov_b32 m0, s67
	s_mov_b64 s[38:39], 0xc000
	global_load_lds_dwordx4 v[6:7], off
	s_add_i32 m0, s61, 0x1c000
	v_lshl_add_u64 v[6:7], v[4:5], 0, s[38:39]
	s_mov_b64 s[40:41], 0xe000
	global_load_lds_dwordx4 v[6:7], off
	v_lshl_add_u64 v[4:5], v[4:5], 0, s[40:41]
	s_add_i32 m0, s61, 0x1e000
	v_lshrrev_b32_e32 v1, 1, v0
	global_load_lds_dwordx4 v[4:5], off
	v_and_b32_e32 v5, 24, v1
	v_lshlrev_b32_e32 v6, 1, v5
	v_lshlrev_b32_e32 v1, 6, v0
	s_movk_i32 s5, 0x3c0
	v_and_b32_e32 v4, 15, v0
	v_and_or_b32 v7, v1, s5, v6
	v_lshlrev_b32_e32 v1, 2, v0
	s_lshl_b32 s1, s1, 5
	v_and_b32_e32 v8, 32, v1
	v_lshl_or_b32 v1, s4, 6, v4
	s_lshl_b32 s4, s4, 13
	v_lshl_or_b32 v4, v4, 6, v6
	s_and_b32 s1, s1, 0x60
	s_ashr_i32 s68, s34, 31
	v_bitop3_b32 v4, v4, s4, v8 bitop3:0xde
	s_lshl_b32 s4, s1, 7
	s_waitcnt vmcnt(6)
	s_cmpk_lt_u32 s0, 0x100
	v_bitop3_b32 v184, s4, v7, v8 bitop3:0xf6
	s_cselect_b64 s[42:43], -1, 0
	s_add_i32 s69, 0, 0x10000
	s_add_i32 s70, 0, 0x14000
	v_ashrrev_i32_e32 v163, 31, v162
	v_or_b32_e32 v185, s1, v5
	v_add3_u32 v170, v12, v11, v10
	v_mov_b32_e32 v171, v165
	v_add3_u32 v172, v13, v11, v10
	v_mov_b32_e32 v173, v165
	s_mov_b64 s[44:45], 0x10000
	v_add_u32_e32 v186, s69, v184
	v_add_u32_e32 v187, s70, v184
	v_add_u32_e32 v188, 0, v4
	v_mov_b32_e32 v189, 0x79797979
	v_mov_b32_e32 v190, 0x7c7c7c7c
	s_mov_b64 s[46:47], 0x80000
	s_mov_b32 s71, 0x80000
	s_mov_b64 s[48:49], 0x90000
	s_mov_b32 s72, 0x90000
	s_mov_b64 s[50:51], 0xa0000
	s_mov_b32 s73, 0xa0000
	s_mov_b32 s74, 0xb0000
	s_barrier
	v_mov_b32_e32 v251, 0
	global_load_dword v250, v251, s[28:29]
	global_load_dword v250, v251, s[28:29]
	global_load_dword v250, v251, s[28:29]
	global_load_dword v250, v251, s[28:29]
	global_load_dword v250, v251, s[28:29]
	global_load_dword v250, v251, s[28:29]
	global_load_dword v250, v251, s[28:29]
	global_load_dword v250, v251, s[28:29]
	global_load_dword v250, v251, s[28:29]
	global_load_dword v250, v251, s[28:29]
	global_load_dword v250, v251, s[28:29]
	global_load_dword v250, v251, s[28:29]
	global_load_dword v250, v251, s[28:29]
	global_load_dword v250, v251, s[28:29]
	global_load_dword v250, v251, s[28:29]
	global_load_dword v250, v251, s[28:29]
	s_branch .LBB0_1561

.LBB0_1567:
	s_add_u32 s56, s56, 0xb0080
	v_lshl_add_u64 v[176:177], v[2:3], 0, s[44:45]
	s_addc_u32 s57, s57, 0
	s_mov_b32 s53, -2
	ds_read_b128 v[26:29], v186
	ds_read_b128 v[30:33], v186 offset:1024
	ds_read_b128 v[18:21], v186 offset:2048
	ds_read_b128 v[22:25], v186 offset:3072
	ds_read_b128 v[10:13], v187
	ds_read_b128 v[14:17], v187 offset:1024
	ds_read_b128 v[2:5], v187 offset:2048
	ds_read_b128 v[6:9], v187 offset:3072
	s_add_u32 s58, s56, 0xfff50080
	s_addc_u32 s59, s57, -1
	s_cmp_eq_u32 s53, 40
	s_cselect_b64 vcc, -1, 0
	s_cselect_b32 s59, s5, s59
	s_cselect_b32 s58, s4, s58
	v_cndmask_b32_e32 v179, v177, v175, vcc
	v_cndmask_b32_e32 v178, v176, v174, vcc
	v_lshl_add_u64 v[180:181], s[56:57], 0, v[170:171]
	s_add_i32 m0, s61, 0xc000
	ds_read_b128 v[192:195], v188
	ds_read_b128 v[196:199], v188 offset:1024
	ds_read_b128 v[200:203], v188 offset:2048
	ds_read_b128 v[204:207], v188 offset:3072
	ds_read_b128 v[208:211], v188 offset:4096
	ds_read_b128 v[212:215], v188 offset:5120
	ds_read_b128 v[220:223], v188 offset:6144
	ds_read_b128 v[224:227], v188 offset:7168
	global_load_lds_dwordx4 v[180:181], off
	v_lshl_add_u64 v[180:181], s[56:57], 0, v[172:173]
	s_add_i32 m0, s61, 0xe000
	s_nop 0
	global_load_lds_dwordx4 v[180:181], off
	s_waitcnt vmcnt(24)
	s_waitcnt lgkmcnt(0)
	s_barrier
	s_waitcnt lgkmcnt(0)
	v_mfma_scale_f32_16x16x128_f8f6f4 v[158:161], v[26:33], v[192:199], 0, v189, v190 op_sel_hi:[0,0,0]
	v_mfma_scale_f32_16x16x128_f8f6f4 v[154:157], v[18:25], v[192:199], 0, v189, v190 op_sel_hi:[0,0,0]
	v_mfma_scale_f32_16x16x128_f8f6f4 v[150:153], v[26:33], v[200:207], 0, v189, v190 op_sel_hi:[0,0,0]
	v_mfma_scale_f32_16x16x128_f8f6f4 v[142:145], v[18:25], v[200:207], 0, v189, v190 op_sel_hi:[0,0,0]
	v_mfma_scale_f32_16x16x128_f8f6f4 v[134:137], v[26:33], v[208:215], 0, v189, v190 op_sel_hi:[0,0,0]
	v_mfma_scale_f32_16x16x128_f8f6f4 v[126:129], v[18:25], v[208:215], 0, v189, v190 op_sel_hi:[0,0,0]
	v_mfma_scale_f32_16x16x128_f8f6f4 v[118:121], v[26:33], v[220:227], 0, v189, v190 op_sel_hi:[0,0,0]
	v_mfma_scale_f32_16x16x128_f8f6f4 v[110:113], v[18:25], v[220:227], 0, v189, v190 op_sel_hi:[0,0,0]
	v_mfma_scale_f32_16x16x128_f8f6f4 v[146:149], v[10:17], v[192:199], 0, v189, v190 op_sel_hi:[0,0,0]
	v_mfma_scale_f32_16x16x128_f8f6f4 v[138:141], v[2:9], v[192:199], 0, v189, v190 op_sel_hi:[0,0,0]
	v_mfma_scale_f32_16x16x128_f8f6f4 v[130:133], v[10:17], v[200:207], 0, v189, v190 op_sel_hi:[0,0,0]
	v_mfma_scale_f32_16x16x128_f8f6f4 v[122:125], v[2:9], v[200:207], 0, v189, v190 op_sel_hi:[0,0,0]
	v_mfma_scale_f32_16x16x128_f8f6f4 v[114:117], v[10:17], v[208:215], 0, v189, v190 op_sel_hi:[0,0,0]
	v_mfma_scale_f32_16x16x128_f8f6f4 v[106:109], v[2:9], v[208:215], 0, v189, v190 op_sel_hi:[0,0,0]
	v_mfma_scale_f32_16x16x128_f8f6f4 v[102:105], v[10:17], v[220:227], 0, v189, v190 op_sel_hi:[0,0,0]
	v_mfma_scale_f32_16x16x128_f8f6f4 v[98:101], v[2:9], v[220:227], 0, v189, v190 op_sel_hi:[0,0,0]
	s_barrier
	s_add_i32 s80, s69, s33
	v_lshl_add_u64 v[178:179], v[178:179], 0, v[164:165]
	s_mov_b32 m0, s80
	ds_read_b128 v[192:195], v188 offset:16384
	ds_read_b128 v[196:199], v188 offset:17408
	ds_read_b128 v[200:203], v188 offset:18432
	ds_read_b128 v[204:207], v188 offset:19456
	ds_read_b128 v[208:211], v188 offset:20480
	ds_read_b128 v[212:215], v188 offset:21504
	ds_read_b128 v[220:223], v188 offset:22528
	ds_read_b128 v[224:227], v188 offset:23552
	global_load_lds_dwordx4 v[178:179], off
	v_lshl_add_u64 v[180:181], v[178:179], 0, s[10:11]
	s_add_i32 m0, s80, 0x2000
	s_add_i32 s80, s70, s33
	global_load_lds_dwordx4 v[180:181], off
	v_lshl_add_u64 v[180:181], v[178:179], 0, s[12:13]
	s_mov_b32 m0, s80
	v_lshl_add_u64 v[182:183], s[58:59], 0, v[168:169]
	global_load_lds_dwordx4 v[180:181], off
	v_lshl_add_u64 v[180:181], v[178:179], 0, s[14:15]
	s_add_i32 m0, s80, 0x2000
	s_nop 0
	global_load_lds_dwordx4 v[180:181], off
	v_lshl_add_u64 v[180:181], s[58:59], 0, v[166:167]
	s_mov_b32 m0, s61
	s_nop 0
	global_load_lds_dwordx4 v[180:181], off
	s_mov_b32 m0, s62
	s_nop 0
	global_load_lds_dwordx4 v[182:183], off
	s_waitcnt vmcnt(24)
	s_waitcnt lgkmcnt(0)
	s_barrier
	s_waitcnt lgkmcnt(0)
	v_mfma_scale_f32_16x16x128_f8f6f4 v[94:97], v[26:33], v[192:199], 0, v189, v190 op_sel_hi:[0,0,0]
	v_mfma_scale_f32_16x16x128_f8f6f4 v[90:93], v[18:25], v[192:199], 0, v189, v190 op_sel_hi:[0,0,0]
	v_mfma_scale_f32_16x16x128_f8f6f4 v[86:89], v[26:33], v[200:207], 0, v189, v190 op_sel_hi:[0,0,0]
	v_mfma_scale_f32_16x16x128_f8f6f4 v[78:81], v[18:25], v[200:207], 0, v189, v190 op_sel_hi:[0,0,0]
	v_mfma_scale_f32_16x16x128_f8f6f4 v[70:73], v[26:33], v[208:215], 0, v189, v190 op_sel_hi:[0,0,0]
	v_mfma_scale_f32_16x16x128_f8f6f4 v[62:65], v[18:25], v[208:215], 0, v189, v190 op_sel_hi:[0,0,0]
	v_mfma_scale_f32_16x16x128_f8f6f4 v[54:57], v[26:33], v[220:227], 0, v189, v190 op_sel_hi:[0,0,0]
	v_mfma_scale_f32_16x16x128_f8f6f4 v[46:49], v[18:25], v[220:227], 0, v189, v190 op_sel_hi:[0,0,0]
	v_mfma_scale_f32_16x16x128_f8f6f4 v[82:85], v[10:17], v[192:199], 0, v189, v190 op_sel_hi:[0,0,0]
	v_mfma_scale_f32_16x16x128_f8f6f4 v[74:77], v[2:9], v[192:199], 0, v189, v190 op_sel_hi:[0,0,0]
	v_mfma_scale_f32_16x16x128_f8f6f4 v[66:69], v[10:17], v[200:207], 0, v189, v190 op_sel_hi:[0,0,0]
	v_mfma_scale_f32_16x16x128_f8f6f4 v[58:61], v[2:9], v[200:207], 0, v189, v190 op_sel_hi:[0,0,0]
	v_mfma_scale_f32_16x16x128_f8f6f4 v[50:53], v[10:17], v[208:215], 0, v189, v190 op_sel_hi:[0,0,0]
	v_mfma_scale_f32_16x16x128_f8f6f4 v[42:45], v[2:9], v[208:215], 0, v189, v190 op_sel_hi:[0,0,0]
	v_mfma_scale_f32_16x16x128_f8f6f4 v[38:41], v[10:17], v[220:227], 0, v189, v190 op_sel_hi:[0,0,0]
	v_mfma_scale_f32_16x16x128_f8f6f4 v[34:37], v[2:9], v[220:227], 0, v189, v190 op_sel_hi:[0,0,0]
	s_barrier
	s_add_i32 s80, 0, 0x18000
	s_add_i32 s81, 0, 0x1c000
	v_add_u32_e32 v14, s80, v184
	v_add_u32_e32 v30, s81, v184
	ds_read_b128 v[2:5], v14
	ds_read_b128 v[6:9], v14 offset:1024
	ds_read_b128 v[10:13], v14 offset:2048
	ds_read_b128 v[14:17], v14 offset:3072
	ds_read_b128 v[18:21], v30
	ds_read_b128 v[22:25], v30 offset:1024
	ds_read_b128 v[26:29], v30 offset:2048
	ds_read_b128 v[30:33], v30 offset:3072
	s_add_u32 s58, s58, 0xb0000
	s_addc_u32 s59, s59, 0
	s_mov_b32 m0, s63
	v_lshl_add_u64 v[216:217], s[58:59], 0, v[166:167]
	ds_read_b128 v[192:195], v188 offset:32768
	ds_read_b128 v[196:199], v188 offset:33792
	ds_read_b128 v[200:203], v188 offset:34816
	ds_read_b128 v[204:207], v188 offset:35840
	ds_read_b128 v[208:211], v188 offset:36864
	ds_read_b128 v[212:215], v188 offset:37888
	ds_read_b128 v[220:223], v188 offset:38912
	ds_read_b128 v[224:227], v188 offset:39936
	global_load_lds_dwordx4 v[216:217], off
	v_lshl_add_u64 v[216:217], s[58:59], 0, v[168:169]
	s_mov_b32 m0, s64
	s_nop 0
	global_load_lds_dwordx4 v[216:217], off
	s_waitcnt vmcnt(8)
	s_waitcnt lgkmcnt(0)
	s_barrier
	s_waitcnt lgkmcnt(0)
	v_mfma_scale_f32_16x16x128_f8f6f4 v[158:161], v[2:9], v[192:199], v[158:161], v189, v190 op_sel_hi:[0,0,0]
	v_mfma_scale_f32_16x16x128_f8f6f4 v[154:157], v[10:17], v[192:199], v[154:157], v189, v190 op_sel_hi:[0,0,0]
	v_mfma_scale_f32_16x16x128_f8f6f4 v[150:153], v[2:9], v[200:207], v[150:153], v189, v190 op_sel_hi:[0,0,0]
	v_mfma_scale_f32_16x16x128_f8f6f4 v[142:145], v[10:17], v[200:207], v[142:145], v189, v190 op_sel_hi:[0,0,0]
	v_mfma_scale_f32_16x16x128_f8f6f4 v[134:137], v[2:9], v[208:215], v[134:137], v189, v190 op_sel_hi:[0,0,0]
	v_mfma_scale_f32_16x16x128_f8f6f4 v[126:129], v[10:17], v[208:215], v[126:129], v189, v190 op_sel_hi:[0,0,0]
	v_mfma_scale_f32_16x16x128_f8f6f4 v[118:121], v[2:9], v[220:227], v[118:121], v189, v190 op_sel_hi:[0,0,0]
	v_mfma_scale_f32_16x16x128_f8f6f4 v[110:113], v[10:17], v[220:227], v[110:113], v189, v190 op_sel_hi:[0,0,0]
	v_mfma_scale_f32_16x16x128_f8f6f4 v[146:149], v[18:25], v[192:199], v[146:149], v189, v190 op_sel_hi:[0,0,0]
	v_mfma_scale_f32_16x16x128_f8f6f4 v[138:141], v[26:33], v[192:199], v[138:141], v189, v190 op_sel_hi:[0,0,0]
	v_mfma_scale_f32_16x16x128_f8f6f4 v[130:133], v[18:25], v[200:207], v[130:133], v189, v190 op_sel_hi:[0,0,0]
	v_mfma_scale_f32_16x16x128_f8f6f4 v[122:125], v[26:33], v[200:207], v[122:125], v189, v190 op_sel_hi:[0,0,0]
	v_mfma_scale_f32_16x16x128_f8f6f4 v[114:117], v[18:25], v[208:215], v[114:117], v189, v190 op_sel_hi:[0,0,0]
	v_mfma_scale_f32_16x16x128_f8f6f4 v[106:109], v[26:33], v[208:215], v[106:109], v189, v190 op_sel_hi:[0,0,0]
	v_mfma_scale_f32_16x16x128_f8f6f4 v[102:105], v[18:25], v[220:227], v[102:105], v189, v190 op_sel_hi:[0,0,0]
	v_mfma_scale_f32_16x16x128_f8f6f4 v[98:101], v[26:33], v[220:227], v[98:101], v189, v190 op_sel_hi:[0,0,0]
	s_barrier
	s_add_i32 s58, s80, s33
	v_lshl_add_u64 v[216:217], v[178:179], 0, s[24:25]
	s_mov_b32 m0, s58
	ds_read_b128 v[192:195], v188 offset:49152
	ds_read_b128 v[196:199], v188 offset:50176
	ds_read_b128 v[200:203], v188 offset:51200
	ds_read_b128 v[204:207], v188 offset:52224
	ds_read_b128 v[208:211], v188 offset:53248
	ds_read_b128 v[212:215], v188 offset:54272
	ds_read_b128 v[220:223], v188 offset:55296
	ds_read_b128 v[224:227], v188 offset:56320
	global_load_lds_dwordx4 v[216:217], off
	v_lshl_add_u64 v[216:217], v[178:179], 0, s[26:27]
	s_add_i32 m0, s58, 0x2000
	s_add_i32 s58, s81, s33
	global_load_lds_dwordx4 v[216:217], off
	v_lshl_add_u64 v[216:217], v[178:179], 0, s[38:39]
	s_mov_b32 m0, s58
	v_lshl_add_u64 v[178:179], v[178:179], 0, s[40:41]
	global_load_lds_dwordx4 v[216:217], off
	s_add_i32 m0, s58, 0x2000
	s_nop 0
	global_load_lds_dwordx4 v[178:179], off
	v_lshl_add_u64 v[178:179], v[180:181], 0, s[36:37]
	s_mov_b32 m0, s66
	s_nop 0
	global_load_lds_dwordx4 v[178:179], off
	v_lshl_add_u64 v[178:179], v[182:183], 0, s[36:37]
	s_mov_b32 m0, s67
	s_nop 0
	global_load_lds_dwordx4 v[178:179], off
	s_waitcnt vmcnt(8)
	s_waitcnt lgkmcnt(0)
	s_barrier
	s_waitcnt lgkmcnt(0)
	v_mfma_scale_f32_16x16x128_f8f6f4 v[94:97], v[2:9], v[192:199], v[94:97], v189, v190 op_sel_hi:[0,0,0]
	v_mfma_scale_f32_16x16x128_f8f6f4 v[90:93], v[10:17], v[192:199], v[90:93], v189, v190 op_sel_hi:[0,0,0]
	v_mfma_scale_f32_16x16x128_f8f6f4 v[86:89], v[2:9], v[200:207], v[86:89], v189, v190 op_sel_hi:[0,0,0]
	v_mfma_scale_f32_16x16x128_f8f6f4 v[78:81], v[10:17], v[200:207], v[78:81], v189, v190 op_sel_hi:[0,0,0]
	v_mfma_scale_f32_16x16x128_f8f6f4 v[70:73], v[2:9], v[208:215], v[70:73], v189, v190 op_sel_hi:[0,0,0]
	v_mfma_scale_f32_16x16x128_f8f6f4 v[62:65], v[10:17], v[208:215], v[62:65], v189, v190 op_sel_hi:[0,0,0]
	v_mfma_scale_f32_16x16x128_f8f6f4 v[54:57], v[2:9], v[220:227], v[54:57], v189, v190 op_sel_hi:[0,0,0]
	v_mfma_scale_f32_16x16x128_f8f6f4 v[46:49], v[10:17], v[220:227], v[46:49], v189, v190 op_sel_hi:[0,0,0]
	v_mfma_scale_f32_16x16x128_f8f6f4 v[82:85], v[18:25], v[192:199], v[82:85], v189, v190 op_sel_hi:[0,0,0]
	v_mfma_scale_f32_16x16x128_f8f6f4 v[74:77], v[26:33], v[192:199], v[74:77], v189, v190 op_sel_hi:[0,0,0]
	v_mfma_scale_f32_16x16x128_f8f6f4 v[66:69], v[18:25], v[200:207], v[66:69], v189, v190 op_sel_hi:[0,0,0]
	v_mfma_scale_f32_16x16x128_f8f6f4 v[58:61], v[26:33], v[200:207], v[58:61], v189, v190 op_sel_hi:[0,0,0]
	v_mfma_scale_f32_16x16x128_f8f6f4 v[50:53], v[18:25], v[208:215], v[50:53], v189, v190 op_sel_hi:[0,0,0]
	v_mfma_scale_f32_16x16x128_f8f6f4 v[42:45], v[26:33], v[208:215], v[42:45], v189, v190 op_sel_hi:[0,0,0]
	v_mfma_scale_f32_16x16x128_f8f6f4 v[38:41], v[18:25], v[220:227], v[38:41], v189, v190 op_sel_hi:[0,0,0]
	v_mfma_scale_f32_16x16x128_f8f6f4 v[34:37], v[26:33], v[220:227], v[34:37], v189, v190 op_sel_hi:[0,0,0]
	s_barrier
	s_add_i32 s53, s53, 2
	s_add_u32 s56, s56, 0x100
	s_addc_u32 s57, s57, 0
	s_cmp_gt_u32 s53, 41
	v_lshl_add_u64 v[176:177], v[176:177], 0, s[44:45]
